# v78 plus nt policy on the converted dense-weight stores of the P0/P3 conversion loops (44 stores)
# baseline (speedup 1.0000x reference)
; #define LAS __attribute__((address_space(3)))
; __device__ __forceinline__ void tr_item8(const float* W, int ld, int K, int nblk, int item, unsigned char* WT, bool gu, float scale, LAS float* scr, int lane) {
;     const int kb = item / nblk, nb = item % nblk, k0 = 64 * kb, n0 = 32 * nb;
;     int drow0 = n0;
;     if (gu) { const int bj = n0 / FF, j = n0 - bj * FF; drow0 = 256 * (j / 128) + 128 * bj + (j % 128); }
;     { float t_[32];
; #pragma unroll
;       for (int i = 0; i < 32; ++i) t_[i] = W[(size_t)(k0 + 2 * i + (lane >> 5)) * ld + n0 + (lane & 31)];
; #pragma unroll
;       for (int i = 0; i < 32; ++i) scr[(2 * i + (lane >> 5)) * 33 + (lane & 31)] = t_[i] * scale; }
; __device__ __forceinline__ void convert_items(Frame& F, const Args& a, int lo, int hi, int w, int nw) {
;     ...
;     for (int it = lo + w; it < hi; it += nw) {
;         int r = it;
;         if (r < I_FI) { tr_item(a.in[7], 3 * D + 16, D, 96, r, (bf16*)(F.ws + WS_WFOXIN), false, scr, lane); continue; } r -= I_FI;
;         if (r < I_FO) { tr_item(a.in[9], D, D, 32, r, (bf16*)(F.ws + WS_WFOXOUT), false, scr, lane); continue; } r -= I_FO;
;         if (r < I_SI) { tr_item(a.in[10], D + 512, D, 48, r, (bf16*)(F.ws + WS_WSWAIN), false, scr, lane); continue; } r -= I_SI;
;         if (r < I_SO) { tr_item(a.in[12], D, D, 32, r, (bf16*)(F.ws + WS_WSWAOUT), false, scr, lane); continue; } r -= I_SO;
;         if (r < I_GU) { tr_item8(a.in[14], 2 * FF, D, 224, r, F.ws + WS_WGU, true, WSC_GU, scr, lane); continue; } r -= I_GU;
;         if (r < I_DN) { tr_item8(a.in[15], D, FF, 32, r, F.ws + WS_WDN, false, WSC_DN, scr, lane); continue; } r -= I_DN;
;         if (r < NE * I_GU) { const int e = r / I_GU, rr = r % I_GU; tr_item8(a.in[18] + (size_t)e * D * 2 * FF, 2 * FF, D, 224, rr, F.ws + WS_WMGU + (size_t)e * 2 * FF * D, true, WSC_GU, scr, lane); continue; } r -= NE * I_GU;
.LBB0_35:
	s_cmpk_gt_i32 s14, 0x5ff
	s_mov_b64 s[10:11], -1
	s_cbranch_scc0 .LBB0_57
	s_cmpk_gt_u32 s14, 0x7ff
	s_cbranch_scc0 .LBB0_54
	s_cmpk_gt_u32 s14, 0xaff
	s_cbranch_scc0 .LBB0_51
	s_cmpk_gt_u32 s14, 0xcff
	s_cbranch_scc0 .LBB0_48
	s_cmpk_gt_u32 s14, 0x1aff
	s_cbranch_scc0 .LBB0_45
	s_cmpk_gt_u32 s14, 0x21ff
	s_cbranch_scc0 .LBB0_42
	s_add_i32 s0, s14, 0xde00
	s_bfe_u32 s10, s0, 0x70009
	s_mulk_i32 s10, 0x2493
	s_lshr_b32 s10, s10, 16
	s_mulk_i32 s10, 0xe00
	s_sub_i32 s0, s0, s10
	s_bfe_u32 s10, s0, 0xb0005
	s_mulk_i32 s10, 0x2493
	s_lshr_b32 s10, s10, 16
	s_mul_i32 s11, s10, 0xe0
	s_sub_i32 s0, s0, s11
	s_lshl_b32 s11, s0, 5
	s_and_b32 s12, s0, 0xffff
	s_cmpk_gt_u32 s12, 0x6f
	s_cselect_b32 s26, 0xfffff200, 0
	s_cselect_b32 s27, 0x80, 0
	s_lshl_b32 s0, s0, 7
	s_lshl_b32 s10, s10, 6
	s_and_b32 s0, s0, 0x3ff80
	v_add_u32_e32 v64, s10, v28
	v_lshl_add_u64 v[46:47], v[0:1], 0, s[0:1]
	v_mad_i64_i32 v[48:49], s[12:13], v64, s21, v[46:47]
	v_add_u32_e32 v50, 2, v64
	v_add_u32_e32 v52, 4, v64
	v_add_u32_e32 v54, 6, v64
	v_add_u32_e32 v56, 8, v64
	v_add_u32_e32 v58, 10, v64
	v_add_u32_e32 v60, 12, v64
	v_add_u32_e32 v62, 14, v64
	v_mad_i64_i32 v[50:51], s[12:13], v50, s21, v[46:47]
	v_mad_i64_i32 v[52:53], s[12:13], v52, s21, v[46:47]
	v_mad_i64_i32 v[54:55], s[12:13], v54, s21, v[46:47]
	v_mad_i64_i32 v[56:57], s[12:13], v56, s21, v[46:47]
	v_mad_i64_i32 v[58:59], s[12:13], v58, s21, v[46:47]
	v_mad_i64_i32 v[60:61], s[12:13], v60, s21, v[46:47]
	v_mad_i64_i32 v[62:63], s[12:13], v62, s21, v[46:47]
	global_load_dword v65, v[48:49], off nt
	global_load_dword v66, v[50:51], off nt
	global_load_dword v67, v[52:53], off nt
	global_load_dword v68, v[54:55], off nt
	global_load_dword v69, v[56:57], off nt
	global_load_dword v70, v[58:59], off nt
	global_load_dword v71, v[60:61], off nt
	global_load_dword v72, v[62:63], off nt
	v_add_u32_e32 v48, 16, v64
	v_mad_i64_i32 v[48:49], s[12:13], v48, s21, v[46:47]
	v_add_u32_e32 v50, 18, v64
	v_add_u32_e32 v52, 20, v64
	v_add_u32_e32 v54, 22, v64
	v_add_u32_e32 v56, 24, v64
	v_add_u32_e32 v58, 26, v64
	v_add_u32_e32 v60, 28, v64
	v_add_u32_e32 v62, 30, v64
	v_mad_i64_i32 v[50:51], s[12:13], v50, s21, v[46:47]
	v_mad_i64_i32 v[52:53], s[12:13], v52, s21, v[46:47]
	v_mad_i64_i32 v[54:55], s[12:13], v54, s21, v[46:47]
	v_mad_i64_i32 v[56:57], s[12:13], v56, s21, v[46:47]
	v_mad_i64_i32 v[58:59], s[12:13], v58, s21, v[46:47]
	v_mad_i64_i32 v[60:61], s[12:13], v60, s21, v[46:47]
	v_mad_i64_i32 v[62:63], s[12:13], v62, s21, v[46:47]
	global_load_dword v73, v[48:49], off nt
	global_load_dword v74, v[50:51], off nt
	global_load_dword v75, v[52:53], off nt
	global_load_dword v76, v[54:55], off nt
	global_load_dword v77, v[56:57], off nt
	global_load_dword v78, v[58:59], off nt
	global_load_dword v79, v[60:61], off nt
	global_load_dword v80, v[62:63], off nt
	v_add_u32_e32 v48, 32, v64
	v_add_u32_e32 v50, 34, v64
	v_add_u32_e32 v52, 36, v64
	v_add_u32_e32 v54, 38, v64
	v_add_u32_e32 v60, 44, v64
	v_mad_i64_i32 v[48:49], s[12:13], v48, s21, v[46:47]
	v_mad_i64_i32 v[50:51], s[12:13], v50, s21, v[46:47]
	v_mad_i64_i32 v[52:53], s[12:13], v52, s21, v[46:47]
	v_mad_i64_i32 v[54:55], s[12:13], v54, s21, v[46:47]
	v_add_u32_e32 v56, 40, v64
	v_add_u32_e32 v58, 42, v64
	v_mad_i64_i32 v[60:61], s[12:13], v60, s21, v[46:47]
	v_add_u32_e32 v62, 46, v64
	v_mad_i64_i32 v[56:57], s[12:13], v56, s21, v[46:47]
	v_mad_i64_i32 v[58:59], s[12:13], v58, s21, v[46:47]
	v_mad_i64_i32 v[62:63], s[12:13], v62, s21, v[46:47]
	global_load_dword v81, v[48:49], off nt
	global_load_dword v82, v[50:51], off nt
	global_load_dword v83, v[52:53], off nt
	global_load_dword v84, v[54:55], off nt
	global_load_dword v85, v[56:57], off nt
	global_load_dword v86, v[58:59], off nt
	s_nop 0
	global_load_dword v60, v[60:61], off nt
	s_nop 0
	global_load_dword v61, v[62:63], off nt
	v_add_u32_e32 v48, 48, v64
	v_add_u32_e32 v50, 50, v64
	v_add_u32_e32 v52, 52, v64
	v_add_u32_e32 v54, 54, v64
	v_mad_i64_i32 v[48:49], s[12:13], v48, s21, v[46:47]
	v_mad_i64_i32 v[50:51], s[12:13], v50, s21, v[46:47]
	v_mad_i64_i32 v[52:53], s[12:13], v52, s21, v[46:47]
	v_mad_i64_i32 v[54:55], s[12:13], v54, s21, v[46:47]
	v_add_u32_e32 v56, 56, v64
	v_add_u32_e32 v58, 58, v64
	v_mad_i64_i32 v[56:57], s[12:13], v56, s21, v[46:47]
	v_mad_i64_i32 v[58:59], s[12:13], v58, s21, v[46:47]
	global_load_dword v62, v[48:49], off nt
	s_nop 0
	global_load_dword v50, v[50:51], off nt
	s_nop 0
	global_load_dword v51, v[52:53], off nt
	s_nop 0
	global_load_dword v52, v[54:55], off nt
	global_load_dword v53, v[56:57], off nt
	s_nop 0
	global_load_dword v54, v[58:59], off nt
	v_add_u32_e32 v48, 60, v64
	v_add_u32_e32 v55, 62, v64
	v_mad_i64_i32 v[48:49], s[12:13], v48, s21, v[46:47]
	v_mad_i64_i32 v[46:47], s[12:13], v55, s21, v[46:47]
	global_load_dword v48, v[48:49], off nt
	s_nop 0
	global_load_dword v46, v[46:47], off nt
	s_waitcnt vmcnt(31)
	v_mul_f32_e32 v47, 0x42800000, v65
	s_waitcnt vmcnt(30)
	v_mul_f32_e32 v49, 0x42800000, v66
	ds_write2_b32 v29, v47, v49 offset1:66
	s_waitcnt vmcnt(29)
	v_mul_f32_e32 v47, 0x42800000, v67
	s_waitcnt vmcnt(28)
	v_mul_f32_e32 v49, 0x42800000, v68
	ds_write2_b32 v29, v47, v49 offset0:132 offset1:198
	s_waitcnt vmcnt(27)
	v_mul_f32_e32 v47, 0x42800000, v69
	s_waitcnt vmcnt(26)
	v_mul_f32_e32 v49, 0x42800000, v70
	ds_write2_b32 v38, v47, v49 offset0:8 offset1:74
	s_waitcnt vmcnt(25)
	v_mul_f32_e32 v47, 0x42800000, v71
	s_waitcnt vmcnt(24)
	v_mul_f32_e32 v49, 0x42800000, v72
	ds_write2_b32 v38, v47, v49 offset0:140 offset1:206
	s_add_i32 s0, s26, s11
	s_sext_i32_i16 s11, s0
	s_bfe_u32 s11, s11, 0x70018
	s_add_i32 s11, s0, s11
	s_sext_i32_i16 s12, s11
	s_and_b32 s11, s11, 0xff80
	s_sub_i32 s0, s0, s11
	s_lshl_b32 s12, s12, 1
	s_sext_i32_i16 s0, s0
	s_waitcnt vmcnt(23)
; __device__ __forceinline__ unsigned cvt_pk4_fp8(float a, float b, float c, float d) { int w = 0; w = __builtin_amdgcn_cvt_pk_fp8_f32(a, b, w, false); w = __builtin_amdgcn_cvt_pk_fp8_f32(c, d, w, true); return (unsigned)w; }
; #define GAS __attribute__((address_space(1)))
; #define LAS __attribute__((address_space(3)))
; #define LDS_WAIT() asm volatile("s_waitcnt lgkmcnt(0)" ::: "memory")
; __device__ __forceinline__ void tr_item8(const float* W, int ld, int K, int nblk, int item, unsigned char* WT, bool gu, float scale, LAS float* scr, int lane) {
;     ...
;       for (int i = 0; i < 32; ++i) scr[(2 * i + (lane >> 5)) * 33 + (lane & 31)] = t_[i] * scale; }
;     LDS_WAIT(); asm volatile("" ::: "memory");
;     const int c = lane & 3;
; #pragma unroll
;     for (int j = 0; j < 2; ++j) { const int n = (lane >> 2) + 16 * j; const LAS float* sp = scr + (16 * c) * 33 + n;
;         v4u o; o.x = pg8::cvt_pk4_fp8(sp[0 * 33], sp[1 * 33], sp[2 * 33], sp[3 * 33]); o.y = pg8::cvt_pk4_fp8(sp[4 * 33], sp[5 * 33], sp[6 * 33], sp[7 * 33]);
;         o.z = pg8::cvt_pk4_fp8(sp[8 * 33], sp[9 * 33], sp[10 * 33], sp[11 * 33]); o.w = pg8::cvt_pk4_fp8(sp[12 * 33], sp[13 * 33], sp[14 * 33], sp[15 * 33]);
;         *(GAS v4u*)(WT + (size_t)(drow0 + n) * K + k0 + 16 * c) = o; }
;     LDS_WAIT(); asm volatile("" ::: "memory");
	v_mul_f32_e32 v47, 0x42800000, v73
	s_waitcnt vmcnt(22)
	v_mul_f32_e32 v49, 0x42800000, v74
	ds_write2_b32 v39, v47, v49 offset0:16 offset1:82
	s_waitcnt vmcnt(21)
	v_mul_f32_e32 v47, 0x42800000, v75
	s_waitcnt vmcnt(20)
	v_mul_f32_e32 v49, 0x42800000, v76
	ds_write2_b32 v39, v47, v49 offset0:148 offset1:214
	s_waitcnt vmcnt(19)
	v_mul_f32_e32 v47, 0x42800000, v77
	s_waitcnt vmcnt(18)
	v_mul_f32_e32 v49, 0x42800000, v78
	ds_write2_b32 v40, v47, v49 offset0:24 offset1:90
	s_waitcnt vmcnt(17)
	v_mul_f32_e32 v47, 0x42800000, v79
	s_waitcnt vmcnt(16)
	v_mul_f32_e32 v49, 0x42800000, v80
	ds_write2_b32 v40, v47, v49 offset0:156 offset1:222
	s_and_b32 s12, s12, 0xffffff00
	s_add_i32 s0, s27, s0
	s_add_i32 s0, s0, s12
	s_mov_b32 s11, s1
	s_waitcnt vmcnt(15)
	v_mul_f32_e32 v47, 0x42800000, v81
	s_waitcnt vmcnt(14)
	v_mul_f32_e32 v49, 0x42800000, v82
	ds_write2_b32 v41, v47, v49 offset0:32 offset1:98
	s_waitcnt vmcnt(13)
	v_mul_f32_e32 v47, 0x42800000, v83
	s_waitcnt vmcnt(12)
	v_mul_f32_e32 v49, 0x42800000, v84
	ds_write2_b32 v41, v47, v49 offset0:164 offset1:230
	s_waitcnt vmcnt(11)
	v_mul_f32_e32 v47, 0x42800000, v85
	s_waitcnt vmcnt(10)
	v_mul_f32_e32 v49, 0x42800000, v86
	ds_write2_b32 v42, v47, v49 offset0:40 offset1:106
	s_waitcnt vmcnt(9)
	v_mul_f32_e32 v47, 0x42800000, v60
	s_waitcnt vmcnt(8)
	v_mul_f32_e32 v49, 0x42800000, v61
	ds_write2_b32 v42, v47, v49 offset0:172 offset1:238
	v_add_u32_e32 v84, s0, v30
	v_ashrrev_i32_e32 v85, 31, v84
	v_lshlrev_b64 v[84:85], 10, v[84:85]
	s_waitcnt vmcnt(7)
	v_mul_f32_e32 v47, 0x42800000, v62
	s_waitcnt vmcnt(6)
	v_mul_f32_e32 v49, 0x42800000, v50
	ds_write2_b32 v43, v47, v49 offset0:48 offset1:114
	s_waitcnt vmcnt(5)
	v_mul_f32_e32 v47, 0x42800000, v51
	s_waitcnt vmcnt(4)
	v_mul_f32_e32 v49, 0x42800000, v52
	ds_write2_b32 v43, v47, v49 offset0:180 offset1:246
	s_waitcnt vmcnt(3)
	v_mul_f32_e32 v47, 0x42800000, v53
	s_waitcnt vmcnt(2)
	v_mul_f32_e32 v49, 0x42800000, v54
	ds_write2_b32 v44, v47, v49 offset0:56 offset1:122
	v_mov_b32_e32 v49, 0
	v_lshl_add_u64 v[50:51], v[14:15], 0, s[10:11]
	s_waitcnt vmcnt(1)
	v_mul_f32_e32 v47, 0x42800000, v48
	s_waitcnt vmcnt(0)
	v_mul_f32_e32 v46, 0x42800000, v46
	ds_write2_b32 v44, v47, v46 offset0:188 offset1:254
	s_waitcnt lgkmcnt(0)
	ds_read2_b32 v[52:53], v31 offset1:16
	ds_read2_b32 v[54:55], v31 offset0:33 offset1:49
	ds_read2_b32 v[56:57], v31 offset0:66 offset1:82
	ds_read2_b32 v[58:59], v31 offset0:99 offset1:115
	ds_read2_b32 v[60:61], v31 offset0:132 offset1:148
	ds_read2_b32 v[62:63], v31 offset0:165 offset1:181
	ds_read2_b32 v[64:65], v31 offset0:198 offset1:214
	ds_read2_b32 v[66:67], v31 offset0:231 offset1:247
	ds_read2_b32 v[68:69], v45 offset0:8 offset1:24
	ds_read2_b32 v[70:71], v45 offset0:41 offset1:57
	ds_read2_b32 v[72:73], v45 offset0:74 offset1:90
	ds_read2_b32 v[74:75], v45 offset0:107 offset1:123
	ds_read2_b32 v[76:77], v45 offset0:140 offset1:156
	ds_read2_b32 v[78:79], v45 offset0:173 offset1:189
	v_mov_b32_e32 v46, 0
	v_mov_b32_e32 v47, 0
	v_mov_b32_e32 v48, 0
	ds_read2_b32 v[80:81], v45 offset0:206 offset1:222
	ds_read2_b32 v[82:83], v45 offset0:239 offset1:255
	s_waitcnt lgkmcnt(14)
	v_cvt_pk_fp8_f32 v46, v52, v54
	s_waitcnt lgkmcnt(10)
	v_cvt_pk_fp8_f32 v47, v60, v62
	s_waitcnt lgkmcnt(6)
	v_cvt_pk_fp8_f32 v48, v68, v70
	s_waitcnt lgkmcnt(2)
	v_cvt_pk_fp8_f32 v49, v76, v78
	v_cvt_pk_fp8_f32 v46, v56, v58 op_sel:[0,0,1]
	v_cvt_pk_fp8_f32 v47, v64, v66 op_sel:[0,0,1]
	v_cvt_pk_fp8_f32 v48, v72, v74 op_sel:[0,0,1]
	s_waitcnt lgkmcnt(0)
	v_cvt_pk_fp8_f32 v49, v80, v82 op_sel:[0,0,1]
	v_lshl_add_u64 v[84:85], v[50:51], 0, v[84:85]
	v_add_u32_e32 v52, s0, v32
	s_mov_b64 s[10:11], 0
	global_store_dwordx4 v[84:85], v[46:49], off nt
	s_nop 1
	v_mov_b32_e32 v46, 0
	v_mov_b32_e32 v47, 0
	v_mov_b32_e32 v48, 0
	v_mov_b32_e32 v49, 0
	v_cvt_pk_fp8_f32 v46, v53, v55
	v_cvt_pk_fp8_f32 v47, v61, v63
	v_cvt_pk_fp8_f32 v48, v69, v71
	v_cvt_pk_fp8_f32 v49, v77, v79
	v_cvt_pk_fp8_f32 v46, v57, v59 op_sel:[0,0,1]
	v_cvt_pk_fp8_f32 v47, v65, v67 op_sel:[0,0,1]
	v_cvt_pk_fp8_f32 v48, v73, v75 op_sel:[0,0,1]
	v_cvt_pk_fp8_f32 v49, v81, v83 op_sel:[0,0,1]
	v_ashrrev_i32_e32 v53, 31, v52
	v_lshlrev_b64 v[52:53], 10, v[52:53]
	v_lshl_add_u64 v[50:51], v[50:51], 0, v[52:53]
	global_store_dwordx4 v[50:51], v[46:49], off nt
	s_waitcnt lgkmcnt(0)
; #define LAS __attribute__((address_space(3)))
; __device__ __forceinline__ void tr_item8(const float* W, int ld, int K, int nblk, int item, unsigned char* WT, bool gu, float scale, LAS float* scr, int lane) {
;     const int kb = item / nblk, nb = item % nblk, k0 = 64 * kb, n0 = 32 * nb;
;     int drow0 = n0;
;     if (gu) { const int bj = n0 / FF, j = n0 - bj * FF; drow0 = 256 * (j / 128) + 128 * bj + (j % 128); }
;     { float t_[32];
; #pragma unroll
;       for (int i = 0; i < 32; ++i) t_[i] = W[(size_t)(k0 + 2 * i + (lane >> 5)) * ld + n0 + (lane & 31)];
; #pragma unroll
;       for (int i = 0; i < 32; ++i) scr[(2 * i + (lane >> 5)) * 33 + (lane & 31)] = t_[i] * scale; }
; __device__ __forceinline__ void convert_items(Frame& F, const Args& a, int lo, int hi, int w, int nw) {
;     ...
;         if (r < I_DN) { tr_item8(a.in[15], D, FF, 32, r, F.ws + WS_WDN, false, WSC_DN, scr, lane); continue; } r -= I_DN;
.LBB0_42:
	s_andn2_b64 vcc, exec, s[10:11]
	s_cbranch_vccnz .LBB0_44
	s_lshl_b32 s0, s14, 5
	s_and_b32 s10, s18, 0x1ffc0
	s_and_b32 s12, s0, 0x3e0
	v_add_u32_e32 v46, s10, v28
	s_lshl_b32 s0, s12, 2
	v_ashrrev_i32_e32 v47, 31, v46
	v_lshl_add_u64 v[48:49], v[2:3], 0, s[0:1]
	v_lshlrev_b64 v[46:47], 12, v[46:47]
	v_lshl_add_u64 v[46:47], v[48:49], 0, v[46:47]
	v_add_co_u32_e32 v48, vcc, 0x2000, v46
	s_mov_b32 s11, s1
	s_nop 0
	v_addc_co_u32_e32 v49, vcc, 0, v47, vcc
	v_add_co_u32_e32 v50, vcc, 0x4000, v46
	s_nop 1
	v_addc_co_u32_e32 v51, vcc, 0, v47, vcc
	v_add_co_u32_e32 v52, vcc, 0x6000, v46
	s_nop 1
	v_addc_co_u32_e32 v53, vcc, 0, v47, vcc
	v_add_co_u32_e32 v54, vcc, 0x8000, v46
	s_nop 1
	v_addc_co_u32_e32 v55, vcc, 0, v47, vcc
	v_add_co_u32_e32 v56, vcc, 0xa000, v46
	s_nop 1
	v_addc_co_u32_e32 v57, vcc, 0, v47, vcc
	v_add_co_u32_e32 v58, vcc, 0xc000, v46
	s_nop 1
	v_addc_co_u32_e32 v59, vcc, 0, v47, vcc
	v_add_co_u32_e32 v60, vcc, 0xe000, v46
	s_nop 1
	v_addc_co_u32_e32 v61, vcc, 0, v47, vcc
	global_load_dword v64, v[46:47], off nt
	global_load_dword v65, v[48:49], off nt
	global_load_dword v66, v[50:51], off nt
	global_load_dword v67, v[52:53], off nt
	global_load_dword v68, v[54:55], off nt
	global_load_dword v69, v[56:57], off nt
	global_load_dword v70, v[58:59], off nt
	global_load_dword v71, v[60:61], off nt
	v_add_co_u32_e32 v48, vcc, 0x10000, v46
	s_nop 1
	v_addc_co_u32_e32 v49, vcc, 0, v47, vcc
	v_add_co_u32_e32 v50, vcc, 0x12000, v46
	s_nop 1
	v_addc_co_u32_e32 v51, vcc, 0, v47, vcc
	v_add_co_u32_e32 v52, vcc, 0x14000, v46
	s_nop 1
	v_addc_co_u32_e32 v53, vcc, 0, v47, vcc
	v_add_co_u32_e32 v54, vcc, 0x16000, v46
	s_nop 1
	v_addc_co_u32_e32 v55, vcc, 0, v47, vcc
	v_add_co_u32_e32 v56, vcc, 0x18000, v46
	s_nop 1
	v_addc_co_u32_e32 v57, vcc, 0, v47, vcc
	v_add_co_u32_e32 v58, vcc, 0x1a000, v46
	s_nop 1
	v_addc_co_u32_e32 v59, vcc, 0, v47, vcc
	v_add_co_u32_e32 v60, vcc, 0x1c000, v46
	s_nop 1
	v_addc_co_u32_e32 v61, vcc, 0, v47, vcc
	v_add_co_u32_e32 v62, vcc, 0x1e000, v46
	s_nop 1
	v_addc_co_u32_e32 v63, vcc, 0, v47, vcc
	global_load_dword v72, v[48:49], off nt
	global_load_dword v73, v[50:51], off nt
	global_load_dword v74, v[52:53], off nt
	global_load_dword v75, v[54:55], off nt
	global_load_dword v76, v[56:57], off nt
	global_load_dword v77, v[58:59], off nt
	global_load_dword v78, v[60:61], off nt
	global_load_dword v79, v[62:63], off nt
	v_add_co_u32_e32 v48, vcc, 0x20000, v46
	s_nop 1
	v_addc_co_u32_e32 v49, vcc, 0, v47, vcc
	v_add_co_u32_e32 v50, vcc, 0x22000, v46
	s_nop 1
	v_addc_co_u32_e32 v51, vcc, 0, v47, vcc
	v_add_co_u32_e32 v52, vcc, 0x24000, v46
	s_nop 1
	v_addc_co_u32_e32 v53, vcc, 0, v47, vcc
	v_add_co_u32_e32 v54, vcc, 0x26000, v46
	s_nop 1
	v_addc_co_u32_e32 v55, vcc, 0, v47, vcc
	v_add_co_u32_e32 v56, vcc, 0x28000, v46
	s_nop 1
	v_addc_co_u32_e32 v57, vcc, 0, v47, vcc
	v_add_co_u32_e32 v58, vcc, 0x2a000, v46
	s_nop 1
	v_addc_co_u32_e32 v59, vcc, 0, v47, vcc
	v_add_co_u32_e32 v60, vcc, 0x2c000, v46
	s_nop 1
	v_addc_co_u32_e32 v61, vcc, 0, v47, vcc
	v_add_co_u32_e32 v62, vcc, 0x2e000, v46
	s_nop 1
	v_addc_co_u32_e32 v63, vcc, 0, v47, vcc
	global_load_dword v80, v[48:49], off nt
	global_load_dword v81, v[50:51], off nt
	global_load_dword v82, v[52:53], off nt
	global_load_dword v83, v[54:55], off nt
	global_load_dword v84, v[56:57], off nt
	global_load_dword v85, v[58:59], off nt
	s_nop 0
	global_load_dword v60, v[60:61], off nt
	s_nop 0
	global_load_dword v61, v[62:63], off nt
	v_add_co_u32_e32 v48, vcc, 0x30000, v46
	s_nop 1
	v_addc_co_u32_e32 v49, vcc, 0, v47, vcc
	v_add_co_u32_e32 v50, vcc, 0x32000, v46
	s_nop 1
	v_addc_co_u32_e32 v51, vcc, 0, v47, vcc
	v_add_co_u32_e32 v52, vcc, 0x34000, v46
	s_nop 1
	v_addc_co_u32_e32 v53, vcc, 0, v47, vcc
	v_add_co_u32_e32 v54, vcc, 0x36000, v46
	s_nop 1
	v_addc_co_u32_e32 v55, vcc, 0, v47, vcc
	v_add_co_u32_e32 v56, vcc, 0x38000, v46
	s_nop 1
	v_addc_co_u32_e32 v57, vcc, 0, v47, vcc
	v_add_co_u32_e32 v58, vcc, 0x3a000, v46
	s_nop 1
	v_addc_co_u32_e32 v59, vcc, 0, v47, vcc
	global_load_dword v62, v[48:49], off nt
	s_nop 0
	global_load_dword v50, v[50:51], off nt
	s_nop 0
	global_load_dword v51, v[52:53], off nt
	s_nop 0
	global_load_dword v52, v[54:55], off nt
	global_load_dword v53, v[56:57], off nt
	s_nop 0
	global_load_dword v54, v[58:59], off nt
	v_add_co_u32_e32 v48, vcc, 0x3c000, v46
	s_nop 1
	v_addc_co_u32_e32 v49, vcc, 0, v47, vcc
	v_add_co_u32_e32 v46, vcc, 0x3e000, v46
	s_nop 1
	v_addc_co_u32_e32 v47, vcc, 0, v47, vcc
	global_load_dword v48, v[48:49], off nt
	s_nop 0
	global_load_dword v46, v[46:47], off nt
	s_waitcnt vmcnt(31)
	v_mul_f32_e32 v47, 0x43000000, v64
	s_waitcnt vmcnt(30)
; __device__ __forceinline__ unsigned cvt_pk4_fp8(float a, float b, float c, float d) { int w = 0; w = __builtin_amdgcn_cvt_pk_fp8_f32(a, b, w, false); w = __builtin_amdgcn_cvt_pk_fp8_f32(c, d, w, true); return (unsigned)w; }
; #define GAS __attribute__((address_space(1)))
; #define LAS __attribute__((address_space(3)))
; #define LDS_WAIT() asm volatile("s_waitcnt lgkmcnt(0)" ::: "memory")
; __device__ __forceinline__ void tr_item8(const float* W, int ld, int K, int nblk, int item, unsigned char* WT, bool gu, float scale, LAS float* scr, int lane) {
;     ...
;       for (int i = 0; i < 32; ++i) scr[(2 * i + (lane >> 5)) * 33 + (lane & 31)] = t_[i] * scale; }
;     LDS_WAIT(); asm volatile("" ::: "memory");
;     const int c = lane & 3;
; #pragma unroll
;     for (int j = 0; j < 2; ++j) { const int n = (lane >> 2) + 16 * j; const LAS float* sp = scr + (16 * c) * 33 + n;
;         v4u o; o.x = pg8::cvt_pk4_fp8(sp[0 * 33], sp[1 * 33], sp[2 * 33], sp[3 * 33]); o.y = pg8::cvt_pk4_fp8(sp[4 * 33], sp[5 * 33], sp[6 * 33], sp[7 * 33]);
;         o.z = pg8::cvt_pk4_fp8(sp[8 * 33], sp[9 * 33], sp[10 * 33], sp[11 * 33]); o.w = pg8::cvt_pk4_fp8(sp[12 * 33], sp[13 * 33], sp[14 * 33], sp[15 * 33]);
;         *(GAS v4u*)(WT + (size_t)(drow0 + n) * K + k0 + 16 * c) = o; }
;     LDS_WAIT(); asm volatile("" ::: "memory");
	v_mul_f32_e32 v49, 0x43000000, v65
	ds_write2_b32 v29, v47, v49 offset1:66
	s_waitcnt vmcnt(29)
	v_mul_f32_e32 v47, 0x43000000, v66
	s_waitcnt vmcnt(28)
	v_mul_f32_e32 v49, 0x43000000, v67
	ds_write2_b32 v29, v47, v49 offset0:132 offset1:198
	s_waitcnt vmcnt(27)
	v_mul_f32_e32 v47, 0x43000000, v68
	s_waitcnt vmcnt(26)
	v_mul_f32_e32 v49, 0x43000000, v69
	ds_write2_b32 v38, v47, v49 offset0:8 offset1:74
	s_waitcnt vmcnt(25)
	v_mul_f32_e32 v47, 0x43000000, v70
	s_waitcnt vmcnt(24)
	v_mul_f32_e32 v49, 0x43000000, v71
	ds_write2_b32 v38, v47, v49 offset0:140 offset1:206
	s_waitcnt vmcnt(23)
	v_mul_f32_e32 v47, 0x43000000, v72
	s_waitcnt vmcnt(22)
	v_mul_f32_e32 v49, 0x43000000, v73
	ds_write2_b32 v39, v47, v49 offset0:16 offset1:82
	s_waitcnt vmcnt(21)
	v_mul_f32_e32 v47, 0x43000000, v74
	s_waitcnt vmcnt(20)
	v_mul_f32_e32 v49, 0x43000000, v75
	ds_write2_b32 v39, v47, v49 offset0:148 offset1:214
	s_waitcnt vmcnt(19)
	v_mul_f32_e32 v47, 0x43000000, v76
	s_waitcnt vmcnt(18)
	v_mul_f32_e32 v49, 0x43000000, v77
	ds_write2_b32 v40, v47, v49 offset0:24 offset1:90
	s_waitcnt vmcnt(17)
	v_mul_f32_e32 v47, 0x43000000, v78
	s_waitcnt vmcnt(16)
	v_mul_f32_e32 v49, 0x43000000, v79
	ds_write2_b32 v40, v47, v49 offset0:156 offset1:222
	s_waitcnt vmcnt(15)
	v_mul_f32_e32 v47, 0x43000000, v80
	s_waitcnt vmcnt(14)
	v_mul_f32_e32 v49, 0x43000000, v81
	ds_write2_b32 v41, v47, v49 offset0:32 offset1:98
	s_waitcnt vmcnt(13)
	v_mul_f32_e32 v47, 0x43000000, v82
	s_waitcnt vmcnt(12)
	v_mul_f32_e32 v49, 0x43000000, v83
	ds_write2_b32 v41, v47, v49 offset0:164 offset1:230
	s_waitcnt vmcnt(11)
	v_mul_f32_e32 v47, 0x43000000, v84
	s_waitcnt vmcnt(10)
	v_mul_f32_e32 v49, 0x43000000, v85
	ds_write2_b32 v42, v47, v49 offset0:40 offset1:106
	s_waitcnt vmcnt(9)
	v_mul_f32_e32 v47, 0x43000000, v60
	s_waitcnt vmcnt(8)
	v_mul_f32_e32 v49, 0x43000000, v61
	ds_write2_b32 v42, v47, v49 offset0:172 offset1:238
	s_waitcnt vmcnt(7)
	v_mul_f32_e32 v47, 0x43000000, v62
	s_waitcnt vmcnt(6)
	v_mul_f32_e32 v49, 0x43000000, v50
	ds_write2_b32 v43, v47, v49 offset0:48 offset1:114
	s_waitcnt vmcnt(5)
	v_mul_f32_e32 v47, 0x43000000, v51
	s_waitcnt vmcnt(4)
	v_mul_f32_e32 v49, 0x43000000, v52
	ds_write2_b32 v43, v47, v49 offset0:180 offset1:246
	s_waitcnt vmcnt(3)
	v_mul_f32_e32 v47, 0x43000000, v53
	s_waitcnt vmcnt(2)
	v_mul_f32_e32 v49, 0x43000000, v54
	ds_write2_b32 v44, v47, v49 offset0:56 offset1:122
	v_mov_b32_e32 v49, 0
	v_lshl_add_u64 v[50:51], v[16:17], 0, s[10:11]
	s_waitcnt vmcnt(1)
	v_mul_f32_e32 v47, 0x43000000, v48
	s_waitcnt vmcnt(0)
	v_mul_f32_e32 v46, 0x43000000, v46
	ds_write2_b32 v44, v47, v46 offset0:188 offset1:254
	s_waitcnt lgkmcnt(0)
	ds_read2_b32 v[52:53], v31 offset1:16
	ds_read2_b32 v[54:55], v31 offset0:33 offset1:49
	ds_read2_b32 v[56:57], v31 offset0:66 offset1:82
	ds_read2_b32 v[58:59], v31 offset0:99 offset1:115
	ds_read2_b32 v[60:61], v31 offset0:132 offset1:148
	ds_read2_b32 v[62:63], v31 offset0:165 offset1:181
	ds_read2_b32 v[64:65], v31 offset0:198 offset1:214
	ds_read2_b32 v[66:67], v31 offset0:231 offset1:247
	ds_read2_b32 v[68:69], v45 offset0:8 offset1:24
	ds_read2_b32 v[70:71], v45 offset0:41 offset1:57
	ds_read2_b32 v[72:73], v45 offset0:74 offset1:90
	ds_read2_b32 v[74:75], v45 offset0:107 offset1:123
	ds_read2_b32 v[76:77], v45 offset0:140 offset1:156
	ds_read2_b32 v[78:79], v45 offset0:173 offset1:189
	v_mov_b32_e32 v46, 0
	v_mov_b32_e32 v47, 0
	v_mov_b32_e32 v48, 0
	ds_read2_b32 v[80:81], v45 offset0:206 offset1:222
	ds_read2_b32 v[82:83], v45 offset0:239 offset1:255
	s_waitcnt lgkmcnt(14)
	v_cvt_pk_fp8_f32 v46, v52, v54
	s_waitcnt lgkmcnt(10)
	v_cvt_pk_fp8_f32 v47, v60, v62
	s_waitcnt lgkmcnt(6)
	v_cvt_pk_fp8_f32 v48, v68, v70
	s_waitcnt lgkmcnt(2)
	v_cvt_pk_fp8_f32 v49, v76, v78
	v_cvt_pk_fp8_f32 v46, v56, v58 op_sel:[0,0,1]
	v_cvt_pk_fp8_f32 v47, v64, v66 op_sel:[0,0,1]
	v_cvt_pk_fp8_f32 v48, v72, v74 op_sel:[0,0,1]
	s_waitcnt lgkmcnt(0)
	v_cvt_pk_fp8_f32 v49, v80, v82 op_sel:[0,0,1]
	v_add_u32_e32 v52, s12, v30
	v_mad_i64_i32 v[84:85], s[10:11], v52, s20, v[50:51]
	global_store_dwordx4 v[84:85], v[46:49], off nt
	v_add_u32_e32 v52, s12, v32
	v_mad_i64_i32 v[50:51], s[10:11], v52, s20, v[50:51]
	v_mov_b32_e32 v46, 0
	v_mov_b32_e32 v47, 0
	v_mov_b32_e32 v48, 0
	v_mov_b32_e32 v49, 0
	v_cvt_pk_fp8_f32 v46, v53, v55
	v_cvt_pk_fp8_f32 v47, v61, v63
	v_cvt_pk_fp8_f32 v48, v69, v71
	v_cvt_pk_fp8_f32 v49, v77, v79
	v_cvt_pk_fp8_f32 v46, v57, v59 op_sel:[0,0,1]
	v_cvt_pk_fp8_f32 v47, v65, v67 op_sel:[0,0,1]
	v_cvt_pk_fp8_f32 v48, v73, v75 op_sel:[0,0,1]
	v_cvt_pk_fp8_f32 v49, v81, v83 op_sel:[0,0,1]
	global_store_dwordx4 v[50:51], v[46:49], off nt
	s_waitcnt lgkmcnt(0)

; #define LAS __attribute__((address_space(3)))
; __device__ __forceinline__ void tr_item8(const float* W, int ld, int K, int nblk, int item, unsigned char* WT, bool gu, float scale, LAS float* scr, int lane) {
;     const int kb = item / nblk, nb = item % nblk, k0 = 64 * kb, n0 = 32 * nb;
;     int drow0 = n0;
;     if (gu) { const int bj = n0 / FF, j = n0 - bj * FF; drow0 = 256 * (j / 128) + 128 * bj + (j % 128); }
;     { float t_[32];
; #pragma unroll
;       for (int i = 0; i < 32; ++i) t_[i] = W[(size_t)(k0 + 2 * i + (lane >> 5)) * ld + n0 + (lane & 31)];
; #pragma unroll
;       for (int i = 0; i < 32; ++i) scr[(2 * i + (lane >> 5)) * 33 + (lane & 31)] = t_[i] * scale; }
; __device__ __forceinline__ void convert_items(Frame& F, const Args& a, int lo, int hi, int w, int nw) {
;     ...
;         if (r < I_GU) { tr_item8(a.in[14], 2 * FF, D, 224, r, F.ws + WS_WGU, true, WSC_GU, scr, lane); continue; } r -= I_GU;
.LBB0_45:
	s_andn2_b64 vcc, exec, s[10:11]
	s_cbranch_vccnz .LBB0_47
	s_add_i32 s0, s14, 0xf300
	s_bfe_u32 s10, s0, 0xb0005
	s_mulk_i32 s10, 0x2493
	s_lshr_b32 s10, s10, 16
	s_mul_i32 s11, s10, 0xe0
	s_sub_i32 s0, s0, s11
	s_lshl_b32 s11, s0, 5
	s_and_b32 s12, s0, 0xffff
	s_cmpk_gt_u32 s12, 0x6f
	s_cselect_b32 s26, 0xfffff200, 0
	s_cselect_b32 s27, 0x80, 0
	s_lshl_b32 s0, s0, 7
	s_lshl_b32 s10, s10, 6
	s_and_b32 s0, s0, 0x3ff80
	v_add_u32_e32 v64, s10, v28
	v_lshl_add_u64 v[46:47], v[4:5], 0, s[0:1]
	v_mad_i64_i32 v[48:49], s[12:13], v64, s21, v[46:47]
	v_add_u32_e32 v50, 2, v64
	v_add_u32_e32 v52, 4, v64
	v_add_u32_e32 v54, 6, v64
	v_add_u32_e32 v56, 8, v64
	v_add_u32_e32 v58, 10, v64
	v_add_u32_e32 v60, 12, v64
	v_add_u32_e32 v62, 14, v64
	v_mad_i64_i32 v[50:51], s[12:13], v50, s21, v[46:47]
	v_mad_i64_i32 v[52:53], s[12:13], v52, s21, v[46:47]
	v_mad_i64_i32 v[54:55], s[12:13], v54, s21, v[46:47]
	v_mad_i64_i32 v[56:57], s[12:13], v56, s21, v[46:47]
	v_mad_i64_i32 v[58:59], s[12:13], v58, s21, v[46:47]
	v_mad_i64_i32 v[60:61], s[12:13], v60, s21, v[46:47]
	v_mad_i64_i32 v[62:63], s[12:13], v62, s21, v[46:47]
	global_load_dword v65, v[48:49], off nt
	global_load_dword v66, v[50:51], off nt
	global_load_dword v67, v[52:53], off nt
	global_load_dword v68, v[54:55], off nt
	global_load_dword v69, v[56:57], off nt
	global_load_dword v70, v[58:59], off nt
	global_load_dword v71, v[60:61], off nt
	global_load_dword v72, v[62:63], off nt
	v_add_u32_e32 v48, 16, v64
	v_mad_i64_i32 v[48:49], s[12:13], v48, s21, v[46:47]
	v_add_u32_e32 v50, 18, v64
	v_add_u32_e32 v52, 20, v64
	v_add_u32_e32 v54, 22, v64
	v_add_u32_e32 v56, 24, v64
	v_add_u32_e32 v58, 26, v64
	v_add_u32_e32 v60, 28, v64
	v_add_u32_e32 v62, 30, v64
	v_mad_i64_i32 v[50:51], s[12:13], v50, s21, v[46:47]
	v_mad_i64_i32 v[52:53], s[12:13], v52, s21, v[46:47]
	v_mad_i64_i32 v[54:55], s[12:13], v54, s21, v[46:47]
	v_mad_i64_i32 v[56:57], s[12:13], v56, s21, v[46:47]
	v_mad_i64_i32 v[58:59], s[12:13], v58, s21, v[46:47]
	v_mad_i64_i32 v[60:61], s[12:13], v60, s21, v[46:47]
	v_mad_i64_i32 v[62:63], s[12:13], v62, s21, v[46:47]
	global_load_dword v73, v[48:49], off nt
	global_load_dword v74, v[50:51], off nt
	global_load_dword v75, v[52:53], off nt
	global_load_dword v76, v[54:55], off nt
	global_load_dword v77, v[56:57], off nt
	global_load_dword v78, v[58:59], off nt
	global_load_dword v79, v[60:61], off nt
	global_load_dword v80, v[62:63], off nt
	v_add_u32_e32 v48, 32, v64
	v_add_u32_e32 v50, 34, v64
	v_add_u32_e32 v52, 36, v64
	v_add_u32_e32 v54, 38, v64
	v_add_u32_e32 v60, 44, v64
	v_mad_i64_i32 v[48:49], s[12:13], v48, s21, v[46:47]
	v_mad_i64_i32 v[50:51], s[12:13], v50, s21, v[46:47]
	v_mad_i64_i32 v[52:53], s[12:13], v52, s21, v[46:47]
	v_mad_i64_i32 v[54:55], s[12:13], v54, s21, v[46:47]
	v_add_u32_e32 v56, 40, v64
	v_add_u32_e32 v58, 42, v64
	v_mad_i64_i32 v[60:61], s[12:13], v60, s21, v[46:47]
	v_add_u32_e32 v62, 46, v64
	v_mad_i64_i32 v[56:57], s[12:13], v56, s21, v[46:47]
	v_mad_i64_i32 v[58:59], s[12:13], v58, s21, v[46:47]
	v_mad_i64_i32 v[62:63], s[12:13], v62, s21, v[46:47]
	global_load_dword v81, v[48:49], off nt
	global_load_dword v82, v[50:51], off nt
	global_load_dword v83, v[52:53], off nt
	global_load_dword v84, v[54:55], off nt
	global_load_dword v85, v[56:57], off nt
	global_load_dword v86, v[58:59], off nt
	s_nop 0
	global_load_dword v60, v[60:61], off nt
	s_nop 0
	global_load_dword v61, v[62:63], off nt
	v_add_u32_e32 v48, 48, v64
	v_add_u32_e32 v50, 50, v64
	v_add_u32_e32 v52, 52, v64
	v_add_u32_e32 v54, 54, v64
	v_mad_i64_i32 v[48:49], s[12:13], v48, s21, v[46:47]
	v_mad_i64_i32 v[50:51], s[12:13], v50, s21, v[46:47]
	v_mad_i64_i32 v[52:53], s[12:13], v52, s21, v[46:47]
	v_mad_i64_i32 v[54:55], s[12:13], v54, s21, v[46:47]
	v_add_u32_e32 v56, 56, v64
	v_add_u32_e32 v58, 58, v64
	v_mad_i64_i32 v[56:57], s[12:13], v56, s21, v[46:47]
	v_mad_i64_i32 v[58:59], s[12:13], v58, s21, v[46:47]
	global_load_dword v62, v[48:49], off nt
	s_nop 0
	global_load_dword v50, v[50:51], off nt
	s_nop 0
	global_load_dword v51, v[52:53], off nt
	s_nop 0
	global_load_dword v52, v[54:55], off nt
	global_load_dword v53, v[56:57], off nt
	s_nop 0
	global_load_dword v54, v[58:59], off nt
	v_add_u32_e32 v48, 60, v64
	v_add_u32_e32 v55, 62, v64
	v_mad_i64_i32 v[48:49], s[12:13], v48, s21, v[46:47]
	v_mad_i64_i32 v[46:47], s[12:13], v55, s21, v[46:47]
	global_load_dword v48, v[48:49], off nt
	s_nop 0
	global_load_dword v46, v[46:47], off nt
	s_waitcnt vmcnt(31)
	v_mul_f32_e32 v47, 0x42800000, v65
	s_waitcnt vmcnt(30)
	v_mul_f32_e32 v49, 0x42800000, v66
	ds_write2_b32 v29, v47, v49 offset1:66
	s_waitcnt vmcnt(29)
	v_mul_f32_e32 v47, 0x42800000, v67
	s_waitcnt vmcnt(28)
	v_mul_f32_e32 v49, 0x42800000, v68
	ds_write2_b32 v29, v47, v49 offset0:132 offset1:198
	s_waitcnt vmcnt(27)
; __device__ __forceinline__ unsigned cvt_pk4_fp8(float a, float b, float c, float d) { int w = 0; w = __builtin_amdgcn_cvt_pk_fp8_f32(a, b, w, false); w = __builtin_amdgcn_cvt_pk_fp8_f32(c, d, w, true); return (unsigned)w; }
; #define GAS __attribute__((address_space(1)))
; #define LAS __attribute__((address_space(3)))
; #define LDS_WAIT() asm volatile("s_waitcnt lgkmcnt(0)" ::: "memory")
; __device__ __forceinline__ void tr_item8(const float* W, int ld, int K, int nblk, int item, unsigned char* WT, bool gu, float scale, LAS float* scr, int lane) {
;     ...
;       for (int i = 0; i < 32; ++i) scr[(2 * i + (lane >> 5)) * 33 + (lane & 31)] = t_[i] * scale; }
;     LDS_WAIT(); asm volatile("" ::: "memory");
;     const int c = lane & 3;
; #pragma unroll
;     for (int j = 0; j < 2; ++j) { const int n = (lane >> 2) + 16 * j; const LAS float* sp = scr + (16 * c) * 33 + n;
;         v4u o; o.x = pg8::cvt_pk4_fp8(sp[0 * 33], sp[1 * 33], sp[2 * 33], sp[3 * 33]); o.y = pg8::cvt_pk4_fp8(sp[4 * 33], sp[5 * 33], sp[6 * 33], sp[7 * 33]);
;         o.z = pg8::cvt_pk4_fp8(sp[8 * 33], sp[9 * 33], sp[10 * 33], sp[11 * 33]); o.w = pg8::cvt_pk4_fp8(sp[12 * 33], sp[13 * 33], sp[14 * 33], sp[15 * 33]);
;         *(GAS v4u*)(WT + (size_t)(drow0 + n) * K + k0 + 16 * c) = o; }
;     LDS_WAIT(); asm volatile("" ::: "memory");
	v_mul_f32_e32 v47, 0x42800000, v69
	s_waitcnt vmcnt(26)
	v_mul_f32_e32 v49, 0x42800000, v70
	ds_write2_b32 v38, v47, v49 offset0:8 offset1:74
	s_waitcnt vmcnt(25)
	v_mul_f32_e32 v47, 0x42800000, v71
	s_waitcnt vmcnt(24)
	v_mul_f32_e32 v49, 0x42800000, v72
	ds_write2_b32 v38, v47, v49 offset0:140 offset1:206
	s_add_i32 s0, s26, s11
	s_sext_i32_i16 s11, s0
	s_bfe_u32 s11, s11, 0x70018
	s_add_i32 s11, s0, s11
	s_sext_i32_i16 s12, s11
	s_and_b32 s11, s11, 0xff80
	s_sub_i32 s0, s0, s11
	s_lshl_b32 s12, s12, 1
	s_sext_i32_i16 s0, s0
	s_waitcnt vmcnt(23)
	v_mul_f32_e32 v47, 0x42800000, v73
	s_waitcnt vmcnt(22)
	v_mul_f32_e32 v49, 0x42800000, v74
	ds_write2_b32 v39, v47, v49 offset0:16 offset1:82
	s_waitcnt vmcnt(21)
	v_mul_f32_e32 v47, 0x42800000, v75
	s_waitcnt vmcnt(20)
	v_mul_f32_e32 v49, 0x42800000, v76
	ds_write2_b32 v39, v47, v49 offset0:148 offset1:214
	s_waitcnt vmcnt(19)
	v_mul_f32_e32 v47, 0x42800000, v77
	s_waitcnt vmcnt(18)
	v_mul_f32_e32 v49, 0x42800000, v78
	ds_write2_b32 v40, v47, v49 offset0:24 offset1:90
	s_waitcnt vmcnt(17)
	v_mul_f32_e32 v47, 0x42800000, v79
	s_waitcnt vmcnt(16)
	v_mul_f32_e32 v49, 0x42800000, v80
	ds_write2_b32 v40, v47, v49 offset0:156 offset1:222
	s_and_b32 s12, s12, 0xffffff00
	s_add_i32 s0, s27, s0
	s_add_i32 s0, s0, s12
	s_mov_b32 s11, s1
	s_waitcnt vmcnt(15)
	v_mul_f32_e32 v47, 0x42800000, v81
	s_waitcnt vmcnt(14)
	v_mul_f32_e32 v49, 0x42800000, v82
	ds_write2_b32 v41, v47, v49 offset0:32 offset1:98
	s_waitcnt vmcnt(13)
	v_mul_f32_e32 v47, 0x42800000, v83
	s_waitcnt vmcnt(12)
	v_mul_f32_e32 v49, 0x42800000, v84
	ds_write2_b32 v41, v47, v49 offset0:164 offset1:230
	s_waitcnt vmcnt(11)
	v_mul_f32_e32 v47, 0x42800000, v85
	s_waitcnt vmcnt(10)
	v_mul_f32_e32 v49, 0x42800000, v86
	ds_write2_b32 v42, v47, v49 offset0:40 offset1:106
	s_waitcnt vmcnt(9)
	v_mul_f32_e32 v47, 0x42800000, v60
	s_waitcnt vmcnt(8)
	v_mul_f32_e32 v49, 0x42800000, v61
	ds_write2_b32 v42, v47, v49 offset0:172 offset1:238
	v_add_u32_e32 v84, s0, v30
	v_ashrrev_i32_e32 v85, 31, v84
	v_lshlrev_b64 v[84:85], 10, v[84:85]
	s_waitcnt vmcnt(7)
	v_mul_f32_e32 v47, 0x42800000, v62
	s_waitcnt vmcnt(6)
	v_mul_f32_e32 v49, 0x42800000, v50
	ds_write2_b32 v43, v47, v49 offset0:48 offset1:114
	s_waitcnt vmcnt(5)
	v_mul_f32_e32 v47, 0x42800000, v51
	s_waitcnt vmcnt(4)
	v_mul_f32_e32 v49, 0x42800000, v52
	ds_write2_b32 v43, v47, v49 offset0:180 offset1:246
	s_waitcnt vmcnt(3)
	v_mul_f32_e32 v47, 0x42800000, v53
	s_waitcnt vmcnt(2)
	v_mul_f32_e32 v49, 0x42800000, v54
	ds_write2_b32 v44, v47, v49 offset0:56 offset1:122
	v_mov_b32_e32 v49, 0
	v_lshl_add_u64 v[50:51], v[18:19], 0, s[10:11]
	s_waitcnt vmcnt(1)
	v_mul_f32_e32 v47, 0x42800000, v48
	s_waitcnt vmcnt(0)
	v_mul_f32_e32 v46, 0x42800000, v46
	ds_write2_b32 v44, v47, v46 offset0:188 offset1:254
	s_waitcnt lgkmcnt(0)
	ds_read2_b32 v[52:53], v31 offset1:16
	ds_read2_b32 v[54:55], v31 offset0:33 offset1:49
	ds_read2_b32 v[56:57], v31 offset0:66 offset1:82
	ds_read2_b32 v[58:59], v31 offset0:99 offset1:115
	ds_read2_b32 v[60:61], v31 offset0:132 offset1:148
	ds_read2_b32 v[62:63], v31 offset0:165 offset1:181
	ds_read2_b32 v[64:65], v31 offset0:198 offset1:214
	ds_read2_b32 v[66:67], v31 offset0:231 offset1:247
	ds_read2_b32 v[68:69], v45 offset0:8 offset1:24
	ds_read2_b32 v[70:71], v45 offset0:41 offset1:57
	ds_read2_b32 v[72:73], v45 offset0:74 offset1:90
	ds_read2_b32 v[74:75], v45 offset0:107 offset1:123
	ds_read2_b32 v[76:77], v45 offset0:140 offset1:156
	ds_read2_b32 v[78:79], v45 offset0:173 offset1:189
	v_mov_b32_e32 v46, 0
	v_mov_b32_e32 v47, 0
	v_mov_b32_e32 v48, 0
	ds_read2_b32 v[80:81], v45 offset0:206 offset1:222
	ds_read2_b32 v[82:83], v45 offset0:239 offset1:255
	s_waitcnt lgkmcnt(14)
	v_cvt_pk_fp8_f32 v46, v52, v54
	s_waitcnt lgkmcnt(10)
	v_cvt_pk_fp8_f32 v47, v60, v62
	s_waitcnt lgkmcnt(6)
	v_cvt_pk_fp8_f32 v48, v68, v70
	s_waitcnt lgkmcnt(2)
	v_cvt_pk_fp8_f32 v49, v76, v78
	v_cvt_pk_fp8_f32 v46, v56, v58 op_sel:[0,0,1]
	v_cvt_pk_fp8_f32 v47, v64, v66 op_sel:[0,0,1]
	v_cvt_pk_fp8_f32 v48, v72, v74 op_sel:[0,0,1]
	s_waitcnt lgkmcnt(0)
	v_cvt_pk_fp8_f32 v49, v80, v82 op_sel:[0,0,1]
	v_lshl_add_u64 v[84:85], v[50:51], 0, v[84:85]
	v_add_u32_e32 v52, s0, v32
	global_store_dwordx4 v[84:85], v[46:49], off nt
	s_nop 1
	v_mov_b32_e32 v46, 0
	v_mov_b32_e32 v47, 0
	v_mov_b32_e32 v48, 0
	v_mov_b32_e32 v49, 0
	v_cvt_pk_fp8_f32 v46, v53, v55
	v_cvt_pk_fp8_f32 v47, v61, v63
	v_cvt_pk_fp8_f32 v48, v69, v71
	v_cvt_pk_fp8_f32 v49, v77, v79
	v_cvt_pk_fp8_f32 v46, v57, v59 op_sel:[0,0,1]
	v_cvt_pk_fp8_f32 v47, v65, v67 op_sel:[0,0,1]
	v_cvt_pk_fp8_f32 v48, v73, v75 op_sel:[0,0,1]
	v_cvt_pk_fp8_f32 v49, v81, v83 op_sel:[0,0,1]
	v_ashrrev_i32_e32 v53, 31, v52
	v_lshlrev_b64 v[52:53], 10, v[52:53]
	v_lshl_add_u64 v[50:51], v[50:51], 0, v[52:53]
	global_store_dwordx4 v[50:51], v[46:49], off nt
	s_waitcnt lgkmcnt(0)

; #define LAS __attribute__((address_space(3)))
; __device__ __forceinline__ void tr_item(const float* W, int ld, int K, int nblk, int item, bf16* WT, bool gu, LAS float* scr, int lane) {
;     const int kb = item / nblk, nb = item % nblk, k0 = 64 * kb, n0 = 32 * nb;
;     int drow0 = n0;
;     if (gu) { const int bj = n0 / FF, j = n0 - bj * FF; drow0 = 256 * (j / 128) + 128 * bj + (j % 128); }
;     { float t_[32];
; #pragma unroll
;       for (int i = 0; i < 32; ++i) t_[i] = W[(size_t)(k0 + 2 * i + (lane >> 5)) * ld + n0 + (lane & 31)];
; #pragma unroll
;       for (int i = 0; i < 32; ++i) scr[(2 * i + (lane >> 5)) * 33 + (lane & 31)] = t_[i]; }
; __device__ __forceinline__ void convert_items(Frame& F, const Args& a, int lo, int hi, int w, int nw) {
;     ...
;         if (r < I_SO) { tr_item(a.in[12], D, D, 32, r, (bf16*)(F.ws + WS_WSWAOUT), false, scr, lane); continue; } r -= I_SO;
.LBB0_48:
	s_andn2_b64 vcc, exec, s[10:11]
	s_cbranch_vccnz .LBB0_50
	s_add_i32 s0, s18, 0x2000
	s_and_b32 s11, s0, 0x1ffc0
	s_and_b32 s10, s16, 0x3e0
	v_add_u32_e32 v46, s11, v28
	s_lshl_b32 s0, s10, 2
	v_ashrrev_i32_e32 v47, 31, v46
	v_lshl_add_u64 v[48:49], v[6:7], 0, s[0:1]
	v_lshlrev_b64 v[46:47], 12, v[46:47]
	v_lshl_add_u64 v[46:47], v[48:49], 0, v[46:47]
	v_add_co_u32_e32 v48, vcc, 0x2000, v46
	s_lshl_b32 s0, s11, 1
	s_nop 0
	v_addc_co_u32_e32 v49, vcc, 0, v47, vcc
	v_add_co_u32_e32 v50, vcc, 0x4000, v46
	s_nop 1
	v_addc_co_u32_e32 v51, vcc, 0, v47, vcc
	v_add_co_u32_e32 v52, vcc, 0x6000, v46
	s_nop 1
	v_addc_co_u32_e32 v53, vcc, 0, v47, vcc
	v_add_co_u32_e32 v54, vcc, 0x8000, v46
	s_nop 1
	v_addc_co_u32_e32 v55, vcc, 0, v47, vcc
	v_add_co_u32_e32 v56, vcc, 0xa000, v46
	s_nop 1
	v_addc_co_u32_e32 v57, vcc, 0, v47, vcc
	v_add_co_u32_e32 v58, vcc, 0xc000, v46
	s_nop 1
	v_addc_co_u32_e32 v59, vcc, 0, v47, vcc
	v_add_co_u32_e32 v60, vcc, 0xe000, v46
	s_nop 1
	v_addc_co_u32_e32 v61, vcc, 0, v47, vcc
	global_load_dword v64, v[46:47], off nt
	global_load_dword v65, v[48:49], off nt
	global_load_dword v66, v[50:51], off nt
	global_load_dword v67, v[52:53], off nt
	global_load_dword v68, v[54:55], off nt
	global_load_dword v69, v[56:57], off nt
	global_load_dword v70, v[58:59], off nt
	global_load_dword v71, v[60:61], off nt
	v_add_co_u32_e32 v48, vcc, 0x10000, v46
	s_nop 1
	v_addc_co_u32_e32 v49, vcc, 0, v47, vcc
	v_add_co_u32_e32 v50, vcc, 0x12000, v46
	s_nop 1
	v_addc_co_u32_e32 v51, vcc, 0, v47, vcc
	v_add_co_u32_e32 v52, vcc, 0x14000, v46
	s_nop 1
	v_addc_co_u32_e32 v53, vcc, 0, v47, vcc
	v_add_co_u32_e32 v54, vcc, 0x16000, v46
	s_nop 1
	v_addc_co_u32_e32 v55, vcc, 0, v47, vcc
	v_add_co_u32_e32 v56, vcc, 0x18000, v46
	s_nop 1
	v_addc_co_u32_e32 v57, vcc, 0, v47, vcc
	v_add_co_u32_e32 v58, vcc, 0x1a000, v46
	s_nop 1
	v_addc_co_u32_e32 v59, vcc, 0, v47, vcc
	v_add_co_u32_e32 v60, vcc, 0x1c000, v46
	s_nop 1
	v_addc_co_u32_e32 v61, vcc, 0, v47, vcc
	v_add_co_u32_e32 v62, vcc, 0x1e000, v46
	s_nop 1
	v_addc_co_u32_e32 v63, vcc, 0, v47, vcc
	global_load_dword v72, v[48:49], off nt
	global_load_dword v73, v[50:51], off nt
	global_load_dword v74, v[52:53], off nt
	global_load_dword v75, v[54:55], off nt
	global_load_dword v76, v[56:57], off nt
	global_load_dword v77, v[58:59], off nt
	global_load_dword v78, v[60:61], off nt
	global_load_dword v79, v[62:63], off nt
	v_add_co_u32_e32 v48, vcc, 0x20000, v46
	s_nop 1
	v_addc_co_u32_e32 v49, vcc, 0, v47, vcc
	v_add_co_u32_e32 v50, vcc, 0x22000, v46
	s_nop 1
	v_addc_co_u32_e32 v51, vcc, 0, v47, vcc
	v_add_co_u32_e32 v52, vcc, 0x24000, v46
	s_nop 1
	v_addc_co_u32_e32 v53, vcc, 0, v47, vcc
	v_add_co_u32_e32 v54, vcc, 0x26000, v46
	s_nop 1
	v_addc_co_u32_e32 v55, vcc, 0, v47, vcc
	v_add_co_u32_e32 v56, vcc, 0x28000, v46
	s_nop 1
	v_addc_co_u32_e32 v57, vcc, 0, v47, vcc
	v_add_co_u32_e32 v58, vcc, 0x2a000, v46
	s_nop 1
	v_addc_co_u32_e32 v59, vcc, 0, v47, vcc
	v_add_co_u32_e32 v60, vcc, 0x2c000, v46
	s_nop 1
	v_addc_co_u32_e32 v61, vcc, 0, v47, vcc
	v_add_co_u32_e32 v62, vcc, 0x2e000, v46
	s_nop 1
	v_addc_co_u32_e32 v63, vcc, 0, v47, vcc
	global_load_dword v80, v[48:49], off nt
	global_load_dword v81, v[50:51], off nt
	global_load_dword v82, v[52:53], off nt
	global_load_dword v83, v[54:55], off nt
	global_load_dword v84, v[56:57], off nt
	global_load_dword v85, v[58:59], off nt
	global_load_dword v86, v[60:61], off nt
	s_nop 0
	global_load_dword v62, v[62:63], off nt
	v_add_co_u32_e32 v48, vcc, 0x30000, v46
	s_nop 1
	v_addc_co_u32_e32 v49, vcc, 0, v47, vcc
	v_add_co_u32_e32 v50, vcc, 0x32000, v46
	s_nop 1
	v_addc_co_u32_e32 v51, vcc, 0, v47, vcc
	v_add_co_u32_e32 v52, vcc, 0x34000, v46
	s_nop 1
	v_addc_co_u32_e32 v53, vcc, 0, v47, vcc
	v_add_co_u32_e32 v54, vcc, 0x36000, v46
	s_nop 1
	v_addc_co_u32_e32 v55, vcc, 0, v47, vcc
	v_add_co_u32_e32 v56, vcc, 0x38000, v46
	s_nop 1
	v_addc_co_u32_e32 v57, vcc, 0, v47, vcc
	v_add_co_u32_e32 v58, vcc, 0x3a000, v46
	s_nop 1
	v_addc_co_u32_e32 v59, vcc, 0, v47, vcc
	v_add_co_u32_e32 v60, vcc, 0x3c000, v46
	s_nop 1
	v_addc_co_u32_e32 v61, vcc, 0, v47, vcc
	v_add_co_u32_e32 v46, vcc, 0x3e000, v46
	s_nop 1
	v_addc_co_u32_e32 v47, vcc, 0, v47, vcc
	global_load_dword v48, v[48:49], off nt
	s_nop 0
	global_load_dword v49, v[50:51], off nt
	s_nop 0
	global_load_dword v50, v[52:53], off nt
	global_load_dword v51, v[54:55], off nt
	s_nop 0
	global_load_dword v52, v[56:57], off nt
	global_load_dword v53, v[58:59], off nt
	global_load_dword v54, v[60:61], off nt
	s_nop 0
	global_load_dword v46, v[46:47], off nt
	s_waitcnt vmcnt(30)
	ds_write2_b32 v29, v64, v65 offset1:66
	s_waitcnt vmcnt(28)
	ds_write2_b32 v29, v66, v67 offset0:132 offset1:198
	s_waitcnt vmcnt(26)
	ds_write2_b32 v38, v68, v69 offset0:8 offset1:74
	s_waitcnt vmcnt(24)
	ds_write2_b32 v38, v70, v71 offset0:140 offset1:206
	s_waitcnt vmcnt(22)
	ds_write2_b32 v39, v72, v73 offset0:16 offset1:82
	s_waitcnt vmcnt(20)
	ds_write2_b32 v39, v74, v75 offset0:148 offset1:214
	s_waitcnt vmcnt(18)
	ds_write2_b32 v40, v76, v77 offset0:24 offset1:90
	s_waitcnt vmcnt(16)
	ds_write2_b32 v40, v78, v79 offset0:156 offset1:222
	s_waitcnt vmcnt(14)
	ds_write2_b32 v41, v80, v81 offset0:32 offset1:98
	s_waitcnt vmcnt(12)
	ds_write2_b32 v41, v82, v83 offset0:164 offset1:230
	s_waitcnt vmcnt(10)
; #define GAS __attribute__((address_space(1)))
; #define LAS __attribute__((address_space(3)))
; #define LDS_WAIT() asm volatile("s_waitcnt lgkmcnt(0)" ::: "memory")
; __device__ __forceinline__ unsigned pk2(float lo, float hi) { return f2bf(lo) | (f2bf(hi) << 16); }
; __device__ __forceinline__ void tr_item(const float* W, int ld, int K, int nblk, int item, bf16* WT, bool gu, LAS float* scr, int lane) {
;     ...
;       for (int i = 0; i < 32; ++i) scr[(2 * i + (lane >> 5)) * 33 + (lane & 31)] = t_[i]; }
;     LDS_WAIT(); asm volatile("" ::: "memory");
;     const int c = lane & 7;
; #pragma unroll
;     for (int j = 0; j < 4; ++j) { const int n = (lane >> 3) + 8 * j; const LAS float* s = scr + (8 * c) * 33 + n;
;         v4u o; o.x = pk2(s[0 * 33], s[1 * 33]); o.y = pk2(s[2 * 33], s[3 * 33]); o.z = pk2(s[4 * 33], s[5 * 33]); o.w = pk2(s[6 * 33], s[7 * 33]);
;         *(GAS v4u*)(WT + (size_t)(drow0 + n) * K + k0 + 8 * c) = o; }
;     LDS_WAIT(); asm volatile("" ::: "memory");
	ds_write2_b32 v42, v84, v85 offset0:40 offset1:106
	s_waitcnt vmcnt(8)
	ds_write2_b32 v42, v86, v62 offset0:172 offset1:238
	s_waitcnt vmcnt(6)
	ds_write2_b32 v43, v48, v49 offset0:48 offset1:114
	s_waitcnt vmcnt(4)
	ds_write2_b32 v43, v50, v51 offset0:180 offset1:246
	s_waitcnt vmcnt(2)
	ds_write2_b32 v44, v52, v53 offset0:56 offset1:122
	s_waitcnt vmcnt(0)
	ds_write2_b32 v44, v54, v46 offset0:188 offset1:254
	s_waitcnt lgkmcnt(0)
	ds_read2_b32 v[50:51], v34 offset1:8
	ds_read2_b32 v[54:55], v34 offset0:33 offset1:41
	ds_read2_b32 v[56:57], v34 offset0:66 offset1:74
	ds_read2_b32 v[58:59], v34 offset0:99 offset1:107
	ds_read2_b32 v[60:61], v34 offset0:132 offset1:140
	s_waitcnt lgkmcnt(4)
	v_bfe_u32 v46, v50, 16, 1
	v_add3_u32 v46, v50, v46, s22
	s_waitcnt lgkmcnt(3)
	v_bfe_u32 v47, v54, 16, 1
	v_lshrrev_b32_e32 v46, 16, v46
	v_add3_u32 v47, v54, v47, s22
	ds_read2_b32 v[62:63], v34 offset0:165 offset1:173
	v_and_or_b32 v46, v47, s23, v46
	s_waitcnt lgkmcnt(3)
	v_bfe_u32 v47, v56, 16, 1
	v_add3_u32 v47, v56, v47, s22
	s_waitcnt lgkmcnt(2)
	v_bfe_u32 v48, v58, 16, 1
	ds_read2_b32 v[64:65], v34 offset0:198 offset1:206
	v_lshrrev_b32_e32 v47, 16, v47
	v_add3_u32 v48, v58, v48, s22
	ds_read2_b32 v[66:67], v34 offset0:231 offset1:239
	v_and_or_b32 v47, v48, s23, v47
	s_waitcnt lgkmcnt(3)
	v_bfe_u32 v48, v60, 16, 1
	v_add3_u32 v48, v60, v48, s22
	s_waitcnt lgkmcnt(2)
	v_bfe_u32 v49, v62, 16, 1
	v_lshrrev_b32_e32 v48, 16, v48
	v_add3_u32 v49, v62, v49, s22
	v_and_or_b32 v48, v49, s23, v48
	s_waitcnt lgkmcnt(1)
	v_bfe_u32 v49, v64, 16, 1
	v_add_u32_e32 v68, s10, v33
	v_add3_u32 v49, v64, v49, s22
	s_waitcnt lgkmcnt(0)
	v_bfe_u32 v50, v66, 16, 1
	v_ashrrev_i32_e32 v69, 31, v68
	v_lshl_add_u64 v[52:53], v[20:21], 0, s[0:1]
	v_lshrrev_b32_e32 v49, 16, v49
	v_add3_u32 v50, v66, v50, s22
	v_lshlrev_b64 v[68:69], 11, v[68:69]
	v_and_or_b32 v49, v50, s23, v49
	v_lshl_add_u64 v[68:69], v[52:53], 0, v[68:69]
	global_store_dwordx4 v[68:69], v[46:49], off nt
	v_bfe_u32 v50, v67, 16, 1
	v_add3_u32 v50, v67, v50, s22
	v_bfe_u32 v46, v51, 16, 1
	v_add3_u32 v46, v51, v46, s22
	v_bfe_u32 v47, v55, 16, 1
	v_lshrrev_b32_e32 v46, 16, v46
	v_add3_u32 v47, v55, v47, s22
	v_and_or_b32 v46, v47, s23, v46
	v_bfe_u32 v47, v57, 16, 1
	v_add3_u32 v47, v57, v47, s22
	v_bfe_u32 v48, v59, 16, 1
	v_lshrrev_b32_e32 v47, 16, v47
	v_add3_u32 v48, v59, v48, s22
	v_and_or_b32 v47, v48, s23, v47
	v_bfe_u32 v48, v61, 16, 1
	v_add3_u32 v48, v61, v48, s22
	v_bfe_u32 v49, v63, 16, 1
	v_lshrrev_b32_e32 v48, 16, v48
	v_add3_u32 v49, v63, v49, s22
	v_and_or_b32 v48, v49, s23, v48
	v_bfe_u32 v49, v65, 16, 1
	v_add3_u32 v49, v65, v49, s22
	v_lshrrev_b32_e32 v49, 16, v49
	v_and_or_b32 v49, v50, s23, v49
	v_add_u32_e32 v50, s10, v35
	v_ashrrev_i32_e32 v51, 31, v50
	v_lshlrev_b64 v[50:51], 11, v[50:51]
	ds_read2_b32 v[54:55], v34 offset0:16 offset1:24
	v_lshl_add_u64 v[50:51], v[52:53], 0, v[50:51]
	global_store_dwordx4 v[50:51], v[46:49], off nt
	ds_read2_b32 v[50:51], v34 offset0:49 offset1:57
	ds_read2_b32 v[56:57], v34 offset0:82 offset1:90
	ds_read2_b32 v[58:59], v34 offset0:115 offset1:123
	s_waitcnt lgkmcnt(3)
	v_bfe_u32 v46, v54, 16, 1
	v_add3_u32 v46, v54, v46, s22
	s_waitcnt lgkmcnt(2)
	v_bfe_u32 v47, v50, 16, 1
	ds_read2_b32 v[60:61], v34 offset0:148 offset1:156
	v_lshrrev_b32_e32 v46, 16, v46
	v_add3_u32 v47, v50, v47, s22
	ds_read2_b32 v[62:63], v34 offset0:181 offset1:189
	v_and_or_b32 v46, v47, s23, v46
	s_waitcnt lgkmcnt(3)
	v_bfe_u32 v47, v56, 16, 1
	v_add3_u32 v47, v56, v47, s22
	s_waitcnt lgkmcnt(2)
	v_bfe_u32 v48, v58, 16, 1
	ds_read2_b32 v[64:65], v34 offset0:214 offset1:222
	v_lshrrev_b32_e32 v47, 16, v47
	v_add3_u32 v48, v58, v48, s22
	ds_read2_b32 v[66:67], v34 offset0:247 offset1:255
	v_and_or_b32 v47, v48, s23, v47
	s_waitcnt lgkmcnt(3)
	v_bfe_u32 v48, v60, 16, 1
	v_add3_u32 v48, v60, v48, s22
	s_waitcnt lgkmcnt(2)
	v_bfe_u32 v49, v62, 16, 1
	v_lshrrev_b32_e32 v48, 16, v48
	v_add3_u32 v49, v62, v49, s22
	v_and_or_b32 v48, v49, s23, v48
	s_waitcnt lgkmcnt(1)
	v_bfe_u32 v49, v64, 16, 1
	v_add_u32_e32 v68, s10, v36
	v_add3_u32 v49, v64, v49, s22
	s_waitcnt lgkmcnt(0)
	v_bfe_u32 v50, v66, 16, 1
	v_ashrrev_i32_e32 v69, 31, v68
	v_lshrrev_b32_e32 v49, 16, v49
	v_add3_u32 v50, v66, v50, s22
	v_lshlrev_b64 v[68:69], 11, v[68:69]
	v_and_or_b32 v49, v50, s23, v49
	v_lshl_add_u64 v[68:69], v[52:53], 0, v[68:69]
	global_store_dwordx4 v[68:69], v[46:49], off nt
	v_bfe_u32 v50, v67, 16, 1
	v_add3_u32 v50, v67, v50, s22
	v_bfe_u32 v46, v55, 16, 1
	v_add3_u32 v46, v55, v46, s22
	v_bfe_u32 v47, v51, 16, 1
	v_lshrrev_b32_e32 v46, 16, v46
	v_add3_u32 v47, v51, v47, s22
	v_and_or_b32 v46, v47, s23, v46
	v_bfe_u32 v47, v57, 16, 1
	v_add3_u32 v47, v57, v47, s22
	v_bfe_u32 v48, v59, 16, 1
	v_lshrrev_b32_e32 v47, 16, v47
	v_add3_u32 v48, v59, v48, s22
	v_and_or_b32 v47, v48, s23, v47
	v_bfe_u32 v48, v61, 16, 1
	v_add3_u32 v48, v61, v48, s22
	v_bfe_u32 v49, v63, 16, 1
	v_lshrrev_b32_e32 v48, 16, v48
	v_add3_u32 v49, v63, v49, s22
	v_and_or_b32 v48, v49, s23, v48
	v_bfe_u32 v49, v65, 16, 1
	v_add3_u32 v49, v65, v49, s22
	v_lshrrev_b32_e32 v49, 16, v49
	v_and_or_b32 v49, v50, s23, v49
	v_add_u32_e32 v50, s10, v37
	v_ashrrev_i32_e32 v51, 31, v50
	v_lshlrev_b64 v[50:51], 11, v[50:51]
	v_lshl_add_u64 v[50:51], v[52:53], 0, v[50:51]
	global_store_dwordx4 v[50:51], v[46:49], off nt
	s_waitcnt lgkmcnt(0)

; #define LAS __attribute__((address_space(3)))
; __device__ __forceinline__ void tr_item(const float* W, int ld, int K, int nblk, int item, bf16* WT, bool gu, LAS float* scr, int lane) {
;     const int kb = item / nblk, nb = item % nblk, k0 = 64 * kb, n0 = 32 * nb;
;     int drow0 = n0;
;     if (gu) { const int bj = n0 / FF, j = n0 - bj * FF; drow0 = 256 * (j / 128) + 128 * bj + (j % 128); }
;     { float t_[32];
; #pragma unroll
;       for (int i = 0; i < 32; ++i) t_[i] = W[(size_t)(k0 + 2 * i + (lane >> 5)) * ld + n0 + (lane & 31)];
; #pragma unroll
;       for (int i = 0; i < 32; ++i) scr[(2 * i + (lane >> 5)) * 33 + (lane & 31)] = t_[i]; }
; __device__ __forceinline__ void convert_items(Frame& F, const Args& a, int lo, int hi, int w, int nw) {
;     ...
;         if (r < I_SI) { tr_item(a.in[10], D + 512, D, 48, r, (bf16*)(F.ws + WS_WSWAIN), false, scr, lane); continue; } r -= I_SI;
.LBB0_51:
	s_andn2_b64 vcc, exec, s[10:11]
	s_cbranch_vccnz .LBB0_53
	s_add_i32 s0, s14, 0xf800
	s_and_b32 s10, s0, 0xffff
	s_mul_i32 s10, s10, 0xaaab
	s_lshr_b32 s11, s10, 21
	s_mul_i32 s10, s11, 48
	s_sub_i32 s0, s0, s10
	s_lshl_b32 s0, s0, 5
	s_and_b32 s10, s0, 0xffe0
	v_lshl_add_u32 v64, s11, 6, v28
	s_lshl_b32 s0, s10, 2
	v_lshl_add_u64 v[46:47], v[8:9], 0, s[0:1]
	v_add_u32_e32 v50, 2, v64
	v_add_u32_e32 v52, 4, v64
	v_add_u32_e32 v54, 6, v64
	v_add_u32_e32 v56, 8, v64
	v_add_u32_e32 v58, 10, v64
	v_add_u32_e32 v60, 12, v64
	v_add_u32_e32 v62, 14, v64
	v_mad_i64_i32 v[48:49], s[12:13], v64, s24, v[46:47]
	v_mad_i64_i32 v[50:51], s[12:13], v50, s24, v[46:47]
	v_mad_i64_i32 v[52:53], s[12:13], v52, s24, v[46:47]
	v_mad_i64_i32 v[54:55], s[12:13], v54, s24, v[46:47]
	v_mad_i64_i32 v[56:57], s[12:13], v56, s24, v[46:47]
	v_mad_i64_i32 v[58:59], s[12:13], v58, s24, v[46:47]
	v_mad_i64_i32 v[60:61], s[12:13], v60, s24, v[46:47]
	v_mad_i64_i32 v[62:63], s[12:13], v62, s24, v[46:47]
	global_load_dword v65, v[48:49], off nt
	global_load_dword v66, v[50:51], off nt
	global_load_dword v67, v[52:53], off nt
	global_load_dword v68, v[54:55], off nt
	global_load_dword v69, v[56:57], off nt
	global_load_dword v70, v[58:59], off nt
	global_load_dword v71, v[60:61], off nt
	global_load_dword v72, v[62:63], off nt
	v_add_u32_e32 v48, 16, v64
	v_add_u32_e32 v50, 18, v64
	v_add_u32_e32 v52, 20, v64
	v_add_u32_e32 v54, 22, v64
	v_add_u32_e32 v56, 24, v64
	v_add_u32_e32 v58, 26, v64
	v_add_u32_e32 v60, 28, v64
	v_add_u32_e32 v62, 30, v64
	v_mad_i64_i32 v[48:49], s[12:13], v48, s24, v[46:47]
	v_mad_i64_i32 v[50:51], s[12:13], v50, s24, v[46:47]
	v_mad_i64_i32 v[52:53], s[12:13], v52, s24, v[46:47]
	v_mad_i64_i32 v[54:55], s[12:13], v54, s24, v[46:47]
	v_mad_i64_i32 v[56:57], s[12:13], v56, s24, v[46:47]
	v_mad_i64_i32 v[58:59], s[12:13], v58, s24, v[46:47]
	v_mad_i64_i32 v[60:61], s[12:13], v60, s24, v[46:47]
	v_mad_i64_i32 v[62:63], s[12:13], v62, s24, v[46:47]
	global_load_dword v73, v[48:49], off nt
	global_load_dword v74, v[50:51], off nt
	global_load_dword v75, v[52:53], off nt
	global_load_dword v76, v[54:55], off nt
	global_load_dword v77, v[56:57], off nt
	global_load_dword v78, v[58:59], off nt
	global_load_dword v79, v[60:61], off nt
	global_load_dword v80, v[62:63], off nt
	v_add_u32_e32 v48, 32, v64
	v_add_u32_e32 v50, 34, v64
	v_add_u32_e32 v52, 36, v64
	v_add_u32_e32 v54, 38, v64
	v_add_u32_e32 v56, 40, v64
	v_add_u32_e32 v58, 42, v64
	v_add_u32_e32 v60, 44, v64
	v_add_u32_e32 v62, 46, v64
	v_mad_i64_i32 v[48:49], s[12:13], v48, s24, v[46:47]
	v_mad_i64_i32 v[50:51], s[12:13], v50, s24, v[46:47]
	v_mad_i64_i32 v[52:53], s[12:13], v52, s24, v[46:47]
	v_mad_i64_i32 v[54:55], s[12:13], v54, s24, v[46:47]
	v_mad_i64_i32 v[56:57], s[12:13], v56, s24, v[46:47]
	v_mad_i64_i32 v[58:59], s[12:13], v58, s24, v[46:47]
	v_mad_i64_i32 v[60:61], s[12:13], v60, s24, v[46:47]
	v_mad_i64_i32 v[62:63], s[12:13], v62, s24, v[46:47]
	global_load_dword v81, v[48:49], off nt
	global_load_dword v82, v[50:51], off nt
	global_load_dword v83, v[52:53], off nt
	global_load_dword v84, v[54:55], off nt
	global_load_dword v85, v[56:57], off nt
	global_load_dword v86, v[58:59], off nt
	global_load_dword v87, v[60:61], off nt
	s_nop 0
	global_load_dword v62, v[62:63], off nt
	v_add_u32_e32 v48, 48, v64
	v_add_u32_e32 v50, 50, v64
	v_add_u32_e32 v52, 52, v64
	v_add_u32_e32 v54, 54, v64
	v_add_u32_e32 v56, 56, v64
	v_add_u32_e32 v58, 58, v64
	v_add_u32_e32 v60, 60, v64
	v_add_u32_e32 v63, 62, v64
	v_mad_i64_i32 v[48:49], s[12:13], v48, s24, v[46:47]
	v_mad_i64_i32 v[50:51], s[12:13], v50, s24, v[46:47]
	v_mad_i64_i32 v[52:53], s[12:13], v52, s24, v[46:47]
	v_mad_i64_i32 v[54:55], s[12:13], v54, s24, v[46:47]
	v_mad_i64_i32 v[56:57], s[12:13], v56, s24, v[46:47]
	v_mad_i64_i32 v[58:59], s[12:13], v58, s24, v[46:47]
	v_mad_i64_i32 v[60:61], s[12:13], v60, s24, v[46:47]
	v_mad_i64_i32 v[46:47], s[12:13], v63, s24, v[46:47]
	global_load_dword v48, v[48:49], off nt
	s_nop 0
	global_load_dword v49, v[50:51], off nt
	s_nop 0
	global_load_dword v50, v[52:53], off nt
	global_load_dword v51, v[54:55], off nt
	s_nop 0
	global_load_dword v52, v[56:57], off nt
	global_load_dword v53, v[58:59], off nt
	global_load_dword v54, v[60:61], off nt
	s_nop 0
	global_load_dword v46, v[46:47], off nt
	s_waitcnt vmcnt(30)
	ds_write2_b32 v29, v65, v66 offset1:66
	s_waitcnt vmcnt(28)
	ds_write2_b32 v29, v67, v68 offset0:132 offset1:198
	s_waitcnt vmcnt(26)
	ds_write2_b32 v38, v69, v70 offset0:8 offset1:74
	s_waitcnt vmcnt(24)
	ds_write2_b32 v38, v71, v72 offset0:140 offset1:206
	s_waitcnt vmcnt(22)
	ds_write2_b32 v39, v73, v74 offset0:16 offset1:82
	s_waitcnt vmcnt(20)
	ds_write2_b32 v39, v75, v76 offset0:148 offset1:214
	s_waitcnt vmcnt(18)
	ds_write2_b32 v40, v77, v78 offset0:24 offset1:90
	s_waitcnt vmcnt(16)
	ds_write2_b32 v40, v79, v80 offset0:156 offset1:222
	s_waitcnt vmcnt(14)
	ds_write2_b32 v41, v81, v82 offset0:32 offset1:98
	s_waitcnt vmcnt(12)
	ds_write2_b32 v41, v83, v84 offset0:164 offset1:230
	s_waitcnt vmcnt(10)
	ds_write2_b32 v42, v85, v86 offset0:40 offset1:106
	s_waitcnt vmcnt(8)
	ds_write2_b32 v42, v87, v62 offset0:172 offset1:238
	s_waitcnt vmcnt(6)
; #define GAS __attribute__((address_space(1)))
; #define LAS __attribute__((address_space(3)))
; #define LDS_WAIT() asm volatile("s_waitcnt lgkmcnt(0)" ::: "memory")
; __device__ __forceinline__ unsigned pk2(float lo, float hi) { return f2bf(lo) | (f2bf(hi) << 16); }
; __device__ __forceinline__ void tr_item(const float* W, int ld, int K, int nblk, int item, bf16* WT, bool gu, LAS float* scr, int lane) {
;     ...
;       for (int i = 0; i < 32; ++i) scr[(2 * i + (lane >> 5)) * 33 + (lane & 31)] = t_[i]; }
;     LDS_WAIT(); asm volatile("" ::: "memory");
;     const int c = lane & 7;
; #pragma unroll
;     for (int j = 0; j < 4; ++j) { const int n = (lane >> 3) + 8 * j; const LAS float* s = scr + (8 * c) * 33 + n;
;         v4u o; o.x = pk2(s[0 * 33], s[1 * 33]); o.y = pk2(s[2 * 33], s[3 * 33]); o.z = pk2(s[4 * 33], s[5 * 33]); o.w = pk2(s[6 * 33], s[7 * 33]);
;         *(GAS v4u*)(WT + (size_t)(drow0 + n) * K + k0 + 8 * c) = o; }
;     LDS_WAIT(); asm volatile("" ::: "memory");
	ds_write2_b32 v43, v48, v49 offset0:48 offset1:114
	s_waitcnt vmcnt(4)
	ds_write2_b32 v43, v50, v51 offset0:180 offset1:246
	s_waitcnt vmcnt(2)
	ds_write2_b32 v44, v52, v53 offset0:56 offset1:122
	s_waitcnt vmcnt(0)
	ds_write2_b32 v44, v54, v46 offset0:188 offset1:254
	s_waitcnt lgkmcnt(0)
	ds_read2_b32 v[50:51], v34 offset1:8
	ds_read2_b32 v[54:55], v34 offset0:33 offset1:41
	ds_read2_b32 v[56:57], v34 offset0:66 offset1:74
	ds_read2_b32 v[58:59], v34 offset0:99 offset1:107
	ds_read2_b32 v[60:61], v34 offset0:132 offset1:140
	s_waitcnt lgkmcnt(4)
	v_bfe_u32 v46, v50, 16, 1
	v_add3_u32 v46, v50, v46, s22
	s_waitcnt lgkmcnt(3)
	v_bfe_u32 v47, v54, 16, 1
	v_lshrrev_b32_e32 v46, 16, v46
	v_add3_u32 v47, v54, v47, s22
	ds_read2_b32 v[62:63], v34 offset0:165 offset1:173
	v_and_or_b32 v46, v47, s23, v46
	s_waitcnt lgkmcnt(3)
	v_bfe_u32 v47, v56, 16, 1
	v_add3_u32 v47, v56, v47, s22
	s_waitcnt lgkmcnt(2)
	v_bfe_u32 v48, v58, 16, 1
	ds_read2_b32 v[64:65], v34 offset0:198 offset1:206
	v_lshrrev_b32_e32 v47, 16, v47
	v_add3_u32 v48, v58, v48, s22
	ds_read2_b32 v[66:67], v34 offset0:231 offset1:239
	v_and_or_b32 v47, v48, s23, v47
	s_waitcnt lgkmcnt(3)
	v_bfe_u32 v48, v60, 16, 1
	v_add3_u32 v48, v60, v48, s22
	s_waitcnt lgkmcnt(2)
	v_bfe_u32 v49, v62, 16, 1
	v_lshrrev_b32_e32 v48, 16, v48
	v_add3_u32 v49, v62, v49, s22
	v_and_or_b32 v48, v49, s23, v48
	s_waitcnt lgkmcnt(1)
	v_bfe_u32 v49, v64, 16, 1
	v_add_u32_e32 v68, s10, v33
	s_lshl_b32 s0, s11, 7
	v_add3_u32 v49, v64, v49, s22
	s_waitcnt lgkmcnt(0)
	v_bfe_u32 v50, v66, 16, 1
	v_ashrrev_i32_e32 v69, 31, v68
	v_lshl_add_u64 v[52:53], v[22:23], 0, s[0:1]
	v_lshrrev_b32_e32 v49, 16, v49
	v_add3_u32 v50, v66, v50, s22
	v_lshlrev_b64 v[68:69], 11, v[68:69]
	v_and_or_b32 v49, v50, s23, v49
	v_lshl_add_u64 v[68:69], v[52:53], 0, v[68:69]
	global_store_dwordx4 v[68:69], v[46:49], off nt
	v_bfe_u32 v50, v67, 16, 1
	v_add3_u32 v50, v67, v50, s22
	v_bfe_u32 v46, v51, 16, 1
	v_add3_u32 v46, v51, v46, s22
	v_bfe_u32 v47, v55, 16, 1
	v_lshrrev_b32_e32 v46, 16, v46
	v_add3_u32 v47, v55, v47, s22
	v_and_or_b32 v46, v47, s23, v46
	v_bfe_u32 v47, v57, 16, 1
	v_add3_u32 v47, v57, v47, s22
	v_bfe_u32 v48, v59, 16, 1
	v_lshrrev_b32_e32 v47, 16, v47
	v_add3_u32 v48, v59, v48, s22
	v_and_or_b32 v47, v48, s23, v47
	v_bfe_u32 v48, v61, 16, 1
	v_add3_u32 v48, v61, v48, s22
	v_bfe_u32 v49, v63, 16, 1
	v_lshrrev_b32_e32 v48, 16, v48
	v_add3_u32 v49, v63, v49, s22
	v_and_or_b32 v48, v49, s23, v48
	v_bfe_u32 v49, v65, 16, 1
	v_add3_u32 v49, v65, v49, s22
	v_lshrrev_b32_e32 v49, 16, v49
	v_and_or_b32 v49, v50, s23, v49
	v_add_u32_e32 v50, s10, v35
	v_ashrrev_i32_e32 v51, 31, v50
	v_lshlrev_b64 v[50:51], 11, v[50:51]
	ds_read2_b32 v[54:55], v34 offset0:16 offset1:24
	v_lshl_add_u64 v[50:51], v[52:53], 0, v[50:51]
	global_store_dwordx4 v[50:51], v[46:49], off nt
	ds_read2_b32 v[50:51], v34 offset0:49 offset1:57
	ds_read2_b32 v[56:57], v34 offset0:82 offset1:90
	ds_read2_b32 v[58:59], v34 offset0:115 offset1:123
	s_waitcnt lgkmcnt(3)
	v_bfe_u32 v46, v54, 16, 1
	v_add3_u32 v46, v54, v46, s22
	s_waitcnt lgkmcnt(2)
	v_bfe_u32 v47, v50, 16, 1
	ds_read2_b32 v[60:61], v34 offset0:148 offset1:156
	v_lshrrev_b32_e32 v46, 16, v46
	v_add3_u32 v47, v50, v47, s22
	ds_read2_b32 v[62:63], v34 offset0:181 offset1:189
	v_and_or_b32 v46, v47, s23, v46
	s_waitcnt lgkmcnt(3)
	v_bfe_u32 v47, v56, 16, 1
	v_add3_u32 v47, v56, v47, s22
	s_waitcnt lgkmcnt(2)
	v_bfe_u32 v48, v58, 16, 1
	ds_read2_b32 v[64:65], v34 offset0:214 offset1:222
	v_lshrrev_b32_e32 v47, 16, v47
	v_add3_u32 v48, v58, v48, s22
	ds_read2_b32 v[66:67], v34 offset0:247 offset1:255
	v_and_or_b32 v47, v48, s23, v47
	s_waitcnt lgkmcnt(3)
	v_bfe_u32 v48, v60, 16, 1
	v_add3_u32 v48, v60, v48, s22
	s_waitcnt lgkmcnt(2)
	v_bfe_u32 v49, v62, 16, 1
	v_lshrrev_b32_e32 v48, 16, v48
	v_add3_u32 v49, v62, v49, s22
	v_and_or_b32 v48, v49, s23, v48
	s_waitcnt lgkmcnt(1)
	v_bfe_u32 v49, v64, 16, 1
	v_add_u32_e32 v68, s10, v36
	v_add3_u32 v49, v64, v49, s22
	s_waitcnt lgkmcnt(0)
	v_bfe_u32 v50, v66, 16, 1
	v_ashrrev_i32_e32 v69, 31, v68
	v_lshrrev_b32_e32 v49, 16, v49
	v_add3_u32 v50, v66, v50, s22
	v_lshlrev_b64 v[68:69], 11, v[68:69]
	v_and_or_b32 v49, v50, s23, v49
	v_lshl_add_u64 v[68:69], v[52:53], 0, v[68:69]
	global_store_dwordx4 v[68:69], v[46:49], off nt
	v_bfe_u32 v50, v67, 16, 1
	v_add3_u32 v50, v67, v50, s22
	v_bfe_u32 v46, v55, 16, 1
	v_add3_u32 v46, v55, v46, s22
	v_bfe_u32 v47, v51, 16, 1
	v_lshrrev_b32_e32 v46, 16, v46
	v_add3_u32 v47, v51, v47, s22
	v_and_or_b32 v46, v47, s23, v46
	v_bfe_u32 v47, v57, 16, 1
	v_add3_u32 v47, v57, v47, s22
	v_bfe_u32 v48, v59, 16, 1
	v_lshrrev_b32_e32 v47, 16, v47
	v_add3_u32 v48, v59, v48, s22
	v_and_or_b32 v47, v48, s23, v47
	v_bfe_u32 v48, v61, 16, 1
	v_add3_u32 v48, v61, v48, s22
	v_bfe_u32 v49, v63, 16, 1
	v_lshrrev_b32_e32 v48, 16, v48
	v_add3_u32 v49, v63, v49, s22
	v_and_or_b32 v48, v49, s23, v48
	v_bfe_u32 v49, v65, 16, 1
	v_add3_u32 v49, v65, v49, s22
	v_lshrrev_b32_e32 v49, 16, v49
	v_and_or_b32 v49, v50, s23, v49
	v_add_u32_e32 v50, s10, v37
	v_ashrrev_i32_e32 v51, 31, v50
	v_lshlrev_b64 v[50:51], 11, v[50:51]
	v_lshl_add_u64 v[50:51], v[52:53], 0, v[50:51]
	global_store_dwordx4 v[50:51], v[46:49], off nt
	s_waitcnt lgkmcnt(0)

; #define LAS __attribute__((address_space(3)))
; __device__ __forceinline__ void tr_item(const float* W, int ld, int K, int nblk, int item, bf16* WT, bool gu, LAS float* scr, int lane) {
;     const int kb = item / nblk, nb = item % nblk, k0 = 64 * kb, n0 = 32 * nb;
;     int drow0 = n0;
;     if (gu) { const int bj = n0 / FF, j = n0 - bj * FF; drow0 = 256 * (j / 128) + 128 * bj + (j % 128); }
;     { float t_[32];
; #pragma unroll
;       for (int i = 0; i < 32; ++i) t_[i] = W[(size_t)(k0 + 2 * i + (lane >> 5)) * ld + n0 + (lane & 31)];
; #pragma unroll
;       for (int i = 0; i < 32; ++i) scr[(2 * i + (lane >> 5)) * 33 + (lane & 31)] = t_[i]; }
; __device__ __forceinline__ void convert_items(Frame& F, const Args& a, int lo, int hi, int w, int nw) {
;     ...
;         if (r < I_FO) { tr_item(a.in[9], D, D, 32, r, (bf16*)(F.ws + WS_WFOXOUT), false, scr, lane); continue; } r -= I_FO;
.LBB0_54:
	s_andn2_b64 vcc, exec, s[10:11]
	s_cbranch_vccnz .LBB0_56
	s_add_i32 s0, s18, 0x2a00
	s_and_b32 s11, s0, 0x1ffc0
	s_and_b32 s10, s16, 0x3e0
	v_add_u32_e32 v46, s11, v28
	s_lshl_b32 s0, s10, 2
	v_ashrrev_i32_e32 v47, 31, v46
	v_lshl_add_u64 v[48:49], v[10:11], 0, s[0:1]
	v_lshlrev_b64 v[46:47], 12, v[46:47]
	v_lshl_add_u64 v[46:47], v[48:49], 0, v[46:47]
	v_add_co_u32_e32 v48, vcc, 0x2000, v46
	s_lshl_b32 s0, s11, 1
	s_nop 0
	v_addc_co_u32_e32 v49, vcc, 0, v47, vcc
	v_add_co_u32_e32 v50, vcc, 0x4000, v46
	s_nop 1
	v_addc_co_u32_e32 v51, vcc, 0, v47, vcc
	v_add_co_u32_e32 v52, vcc, 0x6000, v46
	s_nop 1
	v_addc_co_u32_e32 v53, vcc, 0, v47, vcc
	v_add_co_u32_e32 v54, vcc, 0x8000, v46
	s_nop 1
	v_addc_co_u32_e32 v55, vcc, 0, v47, vcc
	v_add_co_u32_e32 v56, vcc, 0xa000, v46
	s_nop 1
	v_addc_co_u32_e32 v57, vcc, 0, v47, vcc
	v_add_co_u32_e32 v58, vcc, 0xc000, v46
	s_nop 1
	v_addc_co_u32_e32 v59, vcc, 0, v47, vcc
	v_add_co_u32_e32 v60, vcc, 0xe000, v46
	s_nop 1
	v_addc_co_u32_e32 v61, vcc, 0, v47, vcc
	global_load_dword v64, v[46:47], off nt
	global_load_dword v65, v[48:49], off nt
	global_load_dword v66, v[50:51], off nt
	global_load_dword v67, v[52:53], off nt
	global_load_dword v68, v[54:55], off nt
	global_load_dword v69, v[56:57], off nt
	global_load_dword v70, v[58:59], off nt
	global_load_dword v71, v[60:61], off nt
	v_add_co_u32_e32 v48, vcc, 0x10000, v46
	s_nop 1
	v_addc_co_u32_e32 v49, vcc, 0, v47, vcc
	v_add_co_u32_e32 v50, vcc, 0x12000, v46
	s_nop 1
	v_addc_co_u32_e32 v51, vcc, 0, v47, vcc
	v_add_co_u32_e32 v52, vcc, 0x14000, v46
	s_nop 1
	v_addc_co_u32_e32 v53, vcc, 0, v47, vcc
	v_add_co_u32_e32 v54, vcc, 0x16000, v46
	s_nop 1
	v_addc_co_u32_e32 v55, vcc, 0, v47, vcc
	v_add_co_u32_e32 v56, vcc, 0x18000, v46
	s_nop 1
	v_addc_co_u32_e32 v57, vcc, 0, v47, vcc
	v_add_co_u32_e32 v58, vcc, 0x1a000, v46
	s_nop 1
	v_addc_co_u32_e32 v59, vcc, 0, v47, vcc
	v_add_co_u32_e32 v60, vcc, 0x1c000, v46
	s_nop 1
	v_addc_co_u32_e32 v61, vcc, 0, v47, vcc
	v_add_co_u32_e32 v62, vcc, 0x1e000, v46
	s_nop 1
	v_addc_co_u32_e32 v63, vcc, 0, v47, vcc
	global_load_dword v72, v[48:49], off nt
	global_load_dword v73, v[50:51], off nt
	global_load_dword v74, v[52:53], off nt
	global_load_dword v75, v[54:55], off nt
	global_load_dword v76, v[56:57], off nt
	global_load_dword v77, v[58:59], off nt
	global_load_dword v78, v[60:61], off nt
	global_load_dword v79, v[62:63], off nt
	v_add_co_u32_e32 v48, vcc, 0x20000, v46
	s_nop 1
	v_addc_co_u32_e32 v49, vcc, 0, v47, vcc
	v_add_co_u32_e32 v50, vcc, 0x22000, v46
	s_nop 1
	v_addc_co_u32_e32 v51, vcc, 0, v47, vcc
	v_add_co_u32_e32 v52, vcc, 0x24000, v46
	s_nop 1
	v_addc_co_u32_e32 v53, vcc, 0, v47, vcc
	v_add_co_u32_e32 v54, vcc, 0x26000, v46
	s_nop 1
	v_addc_co_u32_e32 v55, vcc, 0, v47, vcc
	v_add_co_u32_e32 v56, vcc, 0x28000, v46
	s_nop 1
	v_addc_co_u32_e32 v57, vcc, 0, v47, vcc
	v_add_co_u32_e32 v58, vcc, 0x2a000, v46
	s_nop 1
	v_addc_co_u32_e32 v59, vcc, 0, v47, vcc
	v_add_co_u32_e32 v60, vcc, 0x2c000, v46
	s_nop 1
	v_addc_co_u32_e32 v61, vcc, 0, v47, vcc
	v_add_co_u32_e32 v62, vcc, 0x2e000, v46
	s_nop 1
	v_addc_co_u32_e32 v63, vcc, 0, v47, vcc
	global_load_dword v80, v[48:49], off nt
	global_load_dword v81, v[50:51], off nt
	global_load_dword v82, v[52:53], off nt
	global_load_dword v83, v[54:55], off nt
	global_load_dword v84, v[56:57], off nt
	global_load_dword v85, v[58:59], off nt
	global_load_dword v86, v[60:61], off nt
	s_nop 0
	global_load_dword v62, v[62:63], off nt
	v_add_co_u32_e32 v48, vcc, 0x30000, v46
	s_nop 1
	v_addc_co_u32_e32 v49, vcc, 0, v47, vcc
	v_add_co_u32_e32 v50, vcc, 0x32000, v46
	s_nop 1
	v_addc_co_u32_e32 v51, vcc, 0, v47, vcc
	v_add_co_u32_e32 v52, vcc, 0x34000, v46
	s_nop 1
	v_addc_co_u32_e32 v53, vcc, 0, v47, vcc
	v_add_co_u32_e32 v54, vcc, 0x36000, v46
	s_nop 1
	v_addc_co_u32_e32 v55, vcc, 0, v47, vcc
	v_add_co_u32_e32 v56, vcc, 0x38000, v46
	s_nop 1
	v_addc_co_u32_e32 v57, vcc, 0, v47, vcc
	v_add_co_u32_e32 v58, vcc, 0x3a000, v46
	s_nop 1
	v_addc_co_u32_e32 v59, vcc, 0, v47, vcc
	v_add_co_u32_e32 v60, vcc, 0x3c000, v46
	s_nop 1
	v_addc_co_u32_e32 v61, vcc, 0, v47, vcc
	v_add_co_u32_e32 v46, vcc, 0x3e000, v46
	s_nop 1
	v_addc_co_u32_e32 v47, vcc, 0, v47, vcc
	global_load_dword v48, v[48:49], off nt
	s_nop 0
	global_load_dword v49, v[50:51], off nt
	s_nop 0
	global_load_dword v50, v[52:53], off nt
	global_load_dword v51, v[54:55], off nt
	s_nop 0
	global_load_dword v52, v[56:57], off nt
	global_load_dword v53, v[58:59], off nt
	global_load_dword v54, v[60:61], off nt
	s_nop 0
	global_load_dword v46, v[46:47], off nt
	s_waitcnt vmcnt(30)
	ds_write2_b32 v29, v64, v65 offset1:66
	s_waitcnt vmcnt(28)
	ds_write2_b32 v29, v66, v67 offset0:132 offset1:198
	s_waitcnt vmcnt(26)
	ds_write2_b32 v38, v68, v69 offset0:8 offset1:74
	s_waitcnt vmcnt(24)
	ds_write2_b32 v38, v70, v71 offset0:140 offset1:206
	s_waitcnt vmcnt(22)
	ds_write2_b32 v39, v72, v73 offset0:16 offset1:82
	s_waitcnt vmcnt(20)
	ds_write2_b32 v39, v74, v75 offset0:148 offset1:214
	s_waitcnt vmcnt(18)
	ds_write2_b32 v40, v76, v77 offset0:24 offset1:90
	s_waitcnt vmcnt(16)
	ds_write2_b32 v40, v78, v79 offset0:156 offset1:222
	s_waitcnt vmcnt(14)
	ds_write2_b32 v41, v80, v81 offset0:32 offset1:98
	s_waitcnt vmcnt(12)
	ds_write2_b32 v41, v82, v83 offset0:164 offset1:230
	s_waitcnt vmcnt(10)
; #define GAS __attribute__((address_space(1)))
; #define LAS __attribute__((address_space(3)))
; #define LDS_WAIT() asm volatile("s_waitcnt lgkmcnt(0)" ::: "memory")
; __device__ __forceinline__ unsigned pk2(float lo, float hi) { return f2bf(lo) | (f2bf(hi) << 16); }
; __device__ __forceinline__ void tr_item(const float* W, int ld, int K, int nblk, int item, bf16* WT, bool gu, LAS float* scr, int lane) {
;     ...
;       for (int i = 0; i < 32; ++i) scr[(2 * i + (lane >> 5)) * 33 + (lane & 31)] = t_[i]; }
;     LDS_WAIT(); asm volatile("" ::: "memory");
;     const int c = lane & 7;
; #pragma unroll
;     for (int j = 0; j < 4; ++j) { const int n = (lane >> 3) + 8 * j; const LAS float* s = scr + (8 * c) * 33 + n;
;         v4u o; o.x = pk2(s[0 * 33], s[1 * 33]); o.y = pk2(s[2 * 33], s[3 * 33]); o.z = pk2(s[4 * 33], s[5 * 33]); o.w = pk2(s[6 * 33], s[7 * 33]);
;         *(GAS v4u*)(WT + (size_t)(drow0 + n) * K + k0 + 8 * c) = o; }
;     LDS_WAIT(); asm volatile("" ::: "memory");
	ds_write2_b32 v42, v84, v85 offset0:40 offset1:106
	s_waitcnt vmcnt(8)
	ds_write2_b32 v42, v86, v62 offset0:172 offset1:238
	s_waitcnt vmcnt(6)
	ds_write2_b32 v43, v48, v49 offset0:48 offset1:114
	s_waitcnt vmcnt(4)
	ds_write2_b32 v43, v50, v51 offset0:180 offset1:246
	s_waitcnt vmcnt(2)
	ds_write2_b32 v44, v52, v53 offset0:56 offset1:122
	s_waitcnt vmcnt(0)
	ds_write2_b32 v44, v54, v46 offset0:188 offset1:254
	s_waitcnt lgkmcnt(0)
	ds_read2_b32 v[50:51], v34 offset1:8
	ds_read2_b32 v[54:55], v34 offset0:33 offset1:41
	ds_read2_b32 v[56:57], v34 offset0:66 offset1:74
	ds_read2_b32 v[58:59], v34 offset0:99 offset1:107
	ds_read2_b32 v[60:61], v34 offset0:132 offset1:140
	s_waitcnt lgkmcnt(4)
	v_bfe_u32 v46, v50, 16, 1
	v_add3_u32 v46, v50, v46, s22
	s_waitcnt lgkmcnt(3)
	v_bfe_u32 v47, v54, 16, 1
	v_lshrrev_b32_e32 v46, 16, v46
	v_add3_u32 v47, v54, v47, s22
	ds_read2_b32 v[62:63], v34 offset0:165 offset1:173
	v_and_or_b32 v46, v47, s23, v46
	s_waitcnt lgkmcnt(3)
	v_bfe_u32 v47, v56, 16, 1
	v_add3_u32 v47, v56, v47, s22
	s_waitcnt lgkmcnt(2)
	v_bfe_u32 v48, v58, 16, 1
	ds_read2_b32 v[64:65], v34 offset0:198 offset1:206
	v_lshrrev_b32_e32 v47, 16, v47
	v_add3_u32 v48, v58, v48, s22
	ds_read2_b32 v[66:67], v34 offset0:231 offset1:239
	v_and_or_b32 v47, v48, s23, v47
	s_waitcnt lgkmcnt(3)
	v_bfe_u32 v48, v60, 16, 1
	v_add3_u32 v48, v60, v48, s22
	s_waitcnt lgkmcnt(2)
	v_bfe_u32 v49, v62, 16, 1
	v_lshrrev_b32_e32 v48, 16, v48
	v_add3_u32 v49, v62, v49, s22
	v_and_or_b32 v48, v49, s23, v48
	s_waitcnt lgkmcnt(1)
	v_bfe_u32 v49, v64, 16, 1
	v_add_u32_e32 v68, s10, v33
	v_add3_u32 v49, v64, v49, s22
	s_waitcnt lgkmcnt(0)
	v_bfe_u32 v50, v66, 16, 1
	v_ashrrev_i32_e32 v69, 31, v68
	v_lshl_add_u64 v[52:53], v[24:25], 0, s[0:1]
	v_lshrrev_b32_e32 v49, 16, v49
	v_add3_u32 v50, v66, v50, s22
	v_lshlrev_b64 v[68:69], 11, v[68:69]
	v_and_or_b32 v49, v50, s23, v49
	v_lshl_add_u64 v[68:69], v[52:53], 0, v[68:69]
	global_store_dwordx4 v[68:69], v[46:49], off nt
	v_bfe_u32 v50, v67, 16, 1
	v_add3_u32 v50, v67, v50, s22
	v_bfe_u32 v46, v51, 16, 1
	v_add3_u32 v46, v51, v46, s22
	v_bfe_u32 v47, v55, 16, 1
	v_lshrrev_b32_e32 v46, 16, v46
	v_add3_u32 v47, v55, v47, s22
	v_and_or_b32 v46, v47, s23, v46
	v_bfe_u32 v47, v57, 16, 1
	v_add3_u32 v47, v57, v47, s22
	v_bfe_u32 v48, v59, 16, 1
	v_lshrrev_b32_e32 v47, 16, v47
	v_add3_u32 v48, v59, v48, s22
	v_and_or_b32 v47, v48, s23, v47
	v_bfe_u32 v48, v61, 16, 1
	v_add3_u32 v48, v61, v48, s22
	v_bfe_u32 v49, v63, 16, 1
	v_lshrrev_b32_e32 v48, 16, v48
	v_add3_u32 v49, v63, v49, s22
	v_and_or_b32 v48, v49, s23, v48
	v_bfe_u32 v49, v65, 16, 1
	v_add3_u32 v49, v65, v49, s22
	v_lshrrev_b32_e32 v49, 16, v49
	v_and_or_b32 v49, v50, s23, v49
	v_add_u32_e32 v50, s10, v35
	v_ashrrev_i32_e32 v51, 31, v50
	v_lshlrev_b64 v[50:51], 11, v[50:51]
	ds_read2_b32 v[54:55], v34 offset0:16 offset1:24
	v_lshl_add_u64 v[50:51], v[52:53], 0, v[50:51]
	global_store_dwordx4 v[50:51], v[46:49], off nt
	ds_read2_b32 v[50:51], v34 offset0:49 offset1:57
	ds_read2_b32 v[56:57], v34 offset0:82 offset1:90
	ds_read2_b32 v[58:59], v34 offset0:115 offset1:123
	s_waitcnt lgkmcnt(3)
	v_bfe_u32 v46, v54, 16, 1
	v_add3_u32 v46, v54, v46, s22
	s_waitcnt lgkmcnt(2)
	v_bfe_u32 v47, v50, 16, 1
	ds_read2_b32 v[60:61], v34 offset0:148 offset1:156
	v_lshrrev_b32_e32 v46, 16, v46
	v_add3_u32 v47, v50, v47, s22
	ds_read2_b32 v[62:63], v34 offset0:181 offset1:189
	v_and_or_b32 v46, v47, s23, v46
	s_waitcnt lgkmcnt(3)
	v_bfe_u32 v47, v56, 16, 1
	v_add3_u32 v47, v56, v47, s22
	s_waitcnt lgkmcnt(2)
	v_bfe_u32 v48, v58, 16, 1
	ds_read2_b32 v[64:65], v34 offset0:214 offset1:222
	v_lshrrev_b32_e32 v47, 16, v47
	v_add3_u32 v48, v58, v48, s22
	ds_read2_b32 v[66:67], v34 offset0:247 offset1:255
	v_and_or_b32 v47, v48, s23, v47
	s_waitcnt lgkmcnt(3)
	v_bfe_u32 v48, v60, 16, 1
	v_add3_u32 v48, v60, v48, s22
	s_waitcnt lgkmcnt(2)
	v_bfe_u32 v49, v62, 16, 1
	v_lshrrev_b32_e32 v48, 16, v48
	v_add3_u32 v49, v62, v49, s22
	v_and_or_b32 v48, v49, s23, v48
	s_waitcnt lgkmcnt(1)
	v_bfe_u32 v49, v64, 16, 1
	v_add_u32_e32 v68, s10, v36
	v_add3_u32 v49, v64, v49, s22
	s_waitcnt lgkmcnt(0)
	v_bfe_u32 v50, v66, 16, 1
	v_ashrrev_i32_e32 v69, 31, v68
	v_lshrrev_b32_e32 v49, 16, v49
	v_add3_u32 v50, v66, v50, s22
	v_lshlrev_b64 v[68:69], 11, v[68:69]
	v_and_or_b32 v49, v50, s23, v49
	v_lshl_add_u64 v[68:69], v[52:53], 0, v[68:69]
	global_store_dwordx4 v[68:69], v[46:49], off nt
	v_bfe_u32 v50, v67, 16, 1
	v_add3_u32 v50, v67, v50, s22
	v_bfe_u32 v46, v55, 16, 1
	v_add3_u32 v46, v55, v46, s22
	v_bfe_u32 v47, v51, 16, 1
	v_lshrrev_b32_e32 v46, 16, v46
	v_add3_u32 v47, v51, v47, s22
	v_and_or_b32 v46, v47, s23, v46
	v_bfe_u32 v47, v57, 16, 1
	v_add3_u32 v47, v57, v47, s22
	v_bfe_u32 v48, v59, 16, 1
	v_lshrrev_b32_e32 v47, 16, v47
	v_add3_u32 v48, v59, v48, s22
	v_and_or_b32 v47, v48, s23, v47
	v_bfe_u32 v48, v61, 16, 1
	v_add3_u32 v48, v61, v48, s22
	v_bfe_u32 v49, v63, 16, 1
	v_lshrrev_b32_e32 v48, 16, v48
	v_add3_u32 v49, v63, v49, s22
	v_and_or_b32 v48, v49, s23, v48
	v_bfe_u32 v49, v65, 16, 1
	v_add3_u32 v49, v65, v49, s22
	v_lshrrev_b32_e32 v49, 16, v49
	v_and_or_b32 v49, v50, s23, v49
	v_add_u32_e32 v50, s10, v37
	v_ashrrev_i32_e32 v51, 31, v50
	v_lshlrev_b64 v[50:51], 11, v[50:51]
	v_lshl_add_u64 v[50:51], v[52:53], 0, v[50:51]
	global_store_dwordx4 v[50:51], v[46:49], off nt
	s_waitcnt lgkmcnt(0)

; #define LAS __attribute__((address_space(3)))
; __device__ __forceinline__ void tr_item(const float* W, int ld, int K, int nblk, int item, bf16* WT, bool gu, LAS float* scr, int lane) {
;     const int kb = item / nblk, nb = item % nblk, k0 = 64 * kb, n0 = 32 * nb;
;     int drow0 = n0;
;     if (gu) { const int bj = n0 / FF, j = n0 - bj * FF; drow0 = 256 * (j / 128) + 128 * bj + (j % 128); }
;     { float t_[32];
; #pragma unroll
;       for (int i = 0; i < 32; ++i) t_[i] = W[(size_t)(k0 + 2 * i + (lane >> 5)) * ld + n0 + (lane & 31)];
; #pragma unroll
;       for (int i = 0; i < 32; ++i) scr[(2 * i + (lane >> 5)) * 33 + (lane & 31)] = t_[i]; }
; __device__ __forceinline__ void convert_items(Frame& F, const Args& a, int lo, int hi, int w, int nw) {
;     ...
;         if (r < I_FI) { tr_item(a.in[7], 3 * D + 16, D, 96, r, (bf16*)(F.ws + WS_WFOXIN), false, scr, lane); continue; } r -= I_FI;
.LBB0_57:
	s_andn2_b64 vcc, exec, s[10:11]
	s_cbranch_vccnz .LBB0_34
	s_mul_hi_i32 s0, s14, 0x2aaaaaab
	s_lshr_b32 s10, s0, 31
	s_ashr_i32 s0, s0, 4
	s_add_i32 s0, s0, s10
	s_lshl_b32 s12, s0, 6
	s_mulk_i32 s0, 0xf400
	s_add_i32 s10, s16, s0
	v_add_u32_e32 v64, s12, v28
	s_ashr_i32 s11, s10, 31
	v_lshl_add_u64 v[46:47], s[10:11], 2, v[12:13]
	v_add_u32_e32 v50, 2, v64
	v_add_u32_e32 v52, 4, v64
	v_add_u32_e32 v54, 6, v64
	v_add_u32_e32 v56, 8, v64
	v_add_u32_e32 v58, 10, v64
	v_add_u32_e32 v60, 12, v64
	v_add_u32_e32 v62, 14, v64
	v_mad_i64_i32 v[48:49], s[26:27], v64, s25, v[46:47]
	v_mad_i64_i32 v[50:51], s[26:27], v50, s25, v[46:47]
	v_mad_i64_i32 v[52:53], s[26:27], v52, s25, v[46:47]
	v_mad_i64_i32 v[54:55], s[26:27], v54, s25, v[46:47]
	v_mad_i64_i32 v[56:57], s[26:27], v56, s25, v[46:47]
	v_mad_i64_i32 v[58:59], s[26:27], v58, s25, v[46:47]
	v_mad_i64_i32 v[60:61], s[26:27], v60, s25, v[46:47]
	v_mad_i64_i32 v[62:63], s[26:27], v62, s25, v[46:47]
	global_load_dword v65, v[48:49], off nt
	global_load_dword v66, v[50:51], off nt
	global_load_dword v67, v[52:53], off nt
	global_load_dword v68, v[54:55], off nt
	global_load_dword v69, v[56:57], off nt
	global_load_dword v70, v[58:59], off nt
	global_load_dword v71, v[60:61], off nt
	global_load_dword v72, v[62:63], off nt
	v_add_u32_e32 v48, 16, v64
	v_add_u32_e32 v50, 18, v64
	v_add_u32_e32 v52, 20, v64
	v_add_u32_e32 v54, 22, v64
	v_add_u32_e32 v56, 24, v64
	v_add_u32_e32 v58, 26, v64
	v_add_u32_e32 v60, 28, v64
	v_add_u32_e32 v62, 30, v64
	v_mad_i64_i32 v[48:49], s[26:27], v48, s25, v[46:47]
	v_mad_i64_i32 v[50:51], s[26:27], v50, s25, v[46:47]
	v_mad_i64_i32 v[52:53], s[26:27], v52, s25, v[46:47]
	v_mad_i64_i32 v[54:55], s[26:27], v54, s25, v[46:47]
	v_mad_i64_i32 v[56:57], s[26:27], v56, s25, v[46:47]
	v_mad_i64_i32 v[58:59], s[26:27], v58, s25, v[46:47]
	v_mad_i64_i32 v[60:61], s[26:27], v60, s25, v[46:47]
	v_mad_i64_i32 v[62:63], s[26:27], v62, s25, v[46:47]
	global_load_dword v73, v[48:49], off nt
	global_load_dword v74, v[50:51], off nt
	global_load_dword v75, v[52:53], off nt
	global_load_dword v76, v[54:55], off nt
	global_load_dword v77, v[56:57], off nt
	global_load_dword v78, v[58:59], off nt
	global_load_dword v79, v[60:61], off nt
	global_load_dword v80, v[62:63], off nt
	v_add_u32_e32 v48, 32, v64
	v_add_u32_e32 v50, 34, v64
	v_add_u32_e32 v52, 36, v64
	v_add_u32_e32 v54, 38, v64
	v_add_u32_e32 v56, 40, v64
	v_add_u32_e32 v58, 42, v64
	v_add_u32_e32 v60, 44, v64
	v_add_u32_e32 v62, 46, v64
	v_mad_i64_i32 v[48:49], s[26:27], v48, s25, v[46:47]
	v_mad_i64_i32 v[50:51], s[26:27], v50, s25, v[46:47]
	v_mad_i64_i32 v[52:53], s[26:27], v52, s25, v[46:47]
	v_mad_i64_i32 v[54:55], s[26:27], v54, s25, v[46:47]
	v_mad_i64_i32 v[56:57], s[26:27], v56, s25, v[46:47]
	v_mad_i64_i32 v[58:59], s[26:27], v58, s25, v[46:47]
	v_mad_i64_i32 v[60:61], s[26:27], v60, s25, v[46:47]
	v_mad_i64_i32 v[62:63], s[26:27], v62, s25, v[46:47]
	global_load_dword v81, v[48:49], off nt
	global_load_dword v82, v[50:51], off nt
	global_load_dword v83, v[52:53], off nt
	global_load_dword v84, v[54:55], off nt
	global_load_dword v85, v[56:57], off nt
	global_load_dword v86, v[58:59], off nt
	global_load_dword v87, v[60:61], off nt
	s_nop 0
	global_load_dword v62, v[62:63], off nt
	v_add_u32_e32 v48, 48, v64
	v_add_u32_e32 v50, 50, v64
	v_add_u32_e32 v52, 52, v64
	v_add_u32_e32 v54, 54, v64
	v_add_u32_e32 v56, 56, v64
	v_add_u32_e32 v58, 58, v64
	v_add_u32_e32 v60, 60, v64
	v_add_u32_e32 v63, 62, v64
	v_mad_i64_i32 v[48:49], s[26:27], v48, s25, v[46:47]
	v_mad_i64_i32 v[50:51], s[26:27], v50, s25, v[46:47]
	v_mad_i64_i32 v[52:53], s[26:27], v52, s25, v[46:47]
	v_mad_i64_i32 v[54:55], s[26:27], v54, s25, v[46:47]
	v_mad_i64_i32 v[56:57], s[26:27], v56, s25, v[46:47]
	v_mad_i64_i32 v[58:59], s[26:27], v58, s25, v[46:47]
	v_mad_i64_i32 v[60:61], s[26:27], v60, s25, v[46:47]
	v_mad_i64_i32 v[46:47], s[26:27], v63, s25, v[46:47]
	global_load_dword v48, v[48:49], off nt
	s_nop 0
	global_load_dword v49, v[50:51], off nt
	s_nop 0
	global_load_dword v50, v[52:53], off nt
	global_load_dword v51, v[54:55], off nt
	s_nop 0
	global_load_dword v52, v[56:57], off nt
	global_load_dword v53, v[58:59], off nt
	global_load_dword v54, v[60:61], off nt
	s_nop 0
	global_load_dword v46, v[46:47], off nt
	s_waitcnt vmcnt(30)
	ds_write2_b32 v29, v65, v66 offset1:66
	s_waitcnt vmcnt(28)
	ds_write2_b32 v29, v67, v68 offset0:132 offset1:198
	s_waitcnt vmcnt(26)
	ds_write2_b32 v38, v69, v70 offset0:8 offset1:74
	s_waitcnt vmcnt(24)
	ds_write2_b32 v38, v71, v72 offset0:140 offset1:206
	s_waitcnt vmcnt(22)
	ds_write2_b32 v39, v73, v74 offset0:16 offset1:82
	s_waitcnt vmcnt(20)
	ds_write2_b32 v39, v75, v76 offset0:148 offset1:214
	s_waitcnt vmcnt(18)
	ds_write2_b32 v40, v77, v78 offset0:24 offset1:90
	s_waitcnt vmcnt(16)
	ds_write2_b32 v40, v79, v80 offset0:156 offset1:222
	s_waitcnt vmcnt(14)
	ds_write2_b32 v41, v81, v82 offset0:32 offset1:98
	s_waitcnt vmcnt(12)
	ds_write2_b32 v41, v83, v84 offset0:164 offset1:230
	s_waitcnt vmcnt(10)
	ds_write2_b32 v42, v85, v86 offset0:40 offset1:106
	s_waitcnt vmcnt(8)
	ds_write2_b32 v42, v87, v62 offset0:172 offset1:238
	s_waitcnt vmcnt(6)
; #define GAS __attribute__((address_space(1)))
; #define LAS __attribute__((address_space(3)))
; #define LDS_WAIT() asm volatile("s_waitcnt lgkmcnt(0)" ::: "memory")
; __device__ __forceinline__ unsigned pk2(float lo, float hi) { return f2bf(lo) | (f2bf(hi) << 16); }
; __device__ __forceinline__ void tr_item(const float* W, int ld, int K, int nblk, int item, bf16* WT, bool gu, LAS float* scr, int lane) {
;     ...
;       for (int i = 0; i < 32; ++i) scr[(2 * i + (lane >> 5)) * 33 + (lane & 31)] = t_[i]; }
;     LDS_WAIT(); asm volatile("" ::: "memory");
;     const int c = lane & 7;
; #pragma unroll
;     for (int j = 0; j < 4; ++j) { const int n = (lane >> 3) + 8 * j; const LAS float* s = scr + (8 * c) * 33 + n;
;         v4u o; o.x = pk2(s[0 * 33], s[1 * 33]); o.y = pk2(s[2 * 33], s[3 * 33]); o.z = pk2(s[4 * 33], s[5 * 33]); o.w = pk2(s[6 * 33], s[7 * 33]);
;         *(GAS v4u*)(WT + (size_t)(drow0 + n) * K + k0 + 8 * c) = o; }
;     LDS_WAIT(); asm volatile("" ::: "memory");
; __device__ __forceinline__ void convert_items(Frame& F, const Args& a, int lo, int hi, int w, int nw) {
;     ...
;     for (int it = lo + w; it < hi; it += nw) {
	ds_write2_b32 v43, v48, v49 offset0:48 offset1:114
	s_waitcnt vmcnt(4)
	ds_write2_b32 v43, v50, v51 offset0:180 offset1:246
	s_waitcnt vmcnt(2)
	ds_write2_b32 v44, v52, v53 offset0:56 offset1:122
	s_waitcnt vmcnt(0)
	ds_write2_b32 v44, v54, v46 offset0:188 offset1:254
	s_waitcnt lgkmcnt(0)
	ds_read2_b32 v[50:51], v34 offset1:8
	ds_read2_b32 v[54:55], v34 offset0:33 offset1:41
	ds_read2_b32 v[56:57], v34 offset0:66 offset1:74
	ds_read2_b32 v[58:59], v34 offset0:99 offset1:107
	ds_read2_b32 v[60:61], v34 offset0:132 offset1:140
	s_waitcnt lgkmcnt(4)
	v_bfe_u32 v46, v50, 16, 1
	v_add3_u32 v46, v50, v46, s22
	s_waitcnt lgkmcnt(3)
	v_bfe_u32 v47, v54, 16, 1
	v_lshrrev_b32_e32 v46, 16, v46
	v_add3_u32 v47, v54, v47, s22
	ds_read2_b32 v[62:63], v34 offset0:165 offset1:173
	v_and_or_b32 v46, v47, s23, v46
	s_waitcnt lgkmcnt(3)
	v_bfe_u32 v47, v56, 16, 1
	v_add3_u32 v47, v56, v47, s22
	s_waitcnt lgkmcnt(2)
	v_bfe_u32 v48, v58, 16, 1
	ds_read2_b32 v[64:65], v34 offset0:198 offset1:206
	v_lshrrev_b32_e32 v47, 16, v47
	v_add3_u32 v48, v58, v48, s22
	ds_read2_b32 v[66:67], v34 offset0:231 offset1:239
	v_and_or_b32 v47, v48, s23, v47
	s_waitcnt lgkmcnt(3)
	v_bfe_u32 v48, v60, 16, 1
	v_add3_u32 v48, v60, v48, s22
	s_waitcnt lgkmcnt(2)
	v_bfe_u32 v49, v62, 16, 1
	v_lshrrev_b32_e32 v48, 16, v48
	v_add3_u32 v49, v62, v49, s22
	v_and_or_b32 v48, v49, s23, v48
	s_waitcnt lgkmcnt(1)
	v_bfe_u32 v49, v64, 16, 1
	v_add_u32_e32 v68, s10, v33
	s_ashr_i32 s13, s12, 31
	v_add3_u32 v49, v64, v49, s22
	s_waitcnt lgkmcnt(0)
	v_bfe_u32 v50, v66, 16, 1
	v_ashrrev_i32_e32 v69, 31, v68
	v_lshl_add_u64 v[52:53], s[12:13], 1, v[26:27]
	v_lshrrev_b32_e32 v49, 16, v49
	v_add3_u32 v50, v66, v50, s22
	v_lshlrev_b64 v[70:71], 11, v[68:69]
	v_and_or_b32 v49, v50, s23, v49
	v_lshl_add_u64 v[70:71], v[52:53], 0, v[70:71]
	global_store_dwordx4 v[70:71], v[46:49], off nt
	v_bfe_u32 v50, v67, 16, 1
	v_add3_u32 v50, v67, v50, s22
	v_bfe_u32 v46, v51, 16, 1
	v_add3_u32 v46, v51, v46, s22
	v_bfe_u32 v47, v55, 16, 1
	v_lshrrev_b32_e32 v46, 16, v46
	v_add3_u32 v47, v55, v47, s22
	v_and_or_b32 v46, v47, s23, v46
	v_bfe_u32 v47, v57, 16, 1
	v_add3_u32 v47, v57, v47, s22
	v_bfe_u32 v48, v59, 16, 1
	v_lshrrev_b32_e32 v47, 16, v47
	v_add3_u32 v48, v59, v48, s22
	v_and_or_b32 v47, v48, s23, v47
	v_bfe_u32 v48, v61, 16, 1
	v_add3_u32 v48, v61, v48, s22
	v_bfe_u32 v49, v63, 16, 1
	v_lshrrev_b32_e32 v48, 16, v48
	v_add3_u32 v49, v63, v49, s22
	v_and_or_b32 v48, v49, s23, v48
	v_bfe_u32 v49, v65, 16, 1
	v_add3_u32 v49, v65, v49, s22
	v_lshrrev_b32_e32 v49, 16, v49
	v_and_or_b32 v49, v50, s23, v49
	v_add_u32_e32 v50, 8, v68
	v_ashrrev_i32_e32 v51, 31, v50
	v_lshlrev_b64 v[50:51], 11, v[50:51]
	ds_read2_b32 v[54:55], v34 offset0:16 offset1:24
	v_lshl_add_u64 v[50:51], v[52:53], 0, v[50:51]
	global_store_dwordx4 v[50:51], v[46:49], off nt
	ds_read2_b32 v[50:51], v34 offset0:49 offset1:57
	ds_read2_b32 v[56:57], v34 offset0:82 offset1:90
	ds_read2_b32 v[58:59], v34 offset0:115 offset1:123
	s_waitcnt lgkmcnt(3)
	v_bfe_u32 v46, v54, 16, 1
	v_add3_u32 v46, v54, v46, s22
	s_waitcnt lgkmcnt(2)
	v_bfe_u32 v47, v50, 16, 1
	ds_read2_b32 v[60:61], v34 offset0:148 offset1:156
	v_lshrrev_b32_e32 v46, 16, v46
	v_add3_u32 v47, v50, v47, s22
	ds_read2_b32 v[62:63], v34 offset0:181 offset1:189
	v_and_or_b32 v46, v47, s23, v46
	s_waitcnt lgkmcnt(3)
	v_bfe_u32 v47, v56, 16, 1
	v_add3_u32 v47, v56, v47, s22
	s_waitcnt lgkmcnt(2)
	v_bfe_u32 v48, v58, 16, 1
	ds_read2_b32 v[64:65], v34 offset0:214 offset1:222
	v_lshrrev_b32_e32 v47, 16, v47
	v_add3_u32 v48, v58, v48, s22
	ds_read2_b32 v[66:67], v34 offset0:247 offset1:255
	v_and_or_b32 v47, v48, s23, v47
	s_waitcnt lgkmcnt(3)
	v_bfe_u32 v48, v60, 16, 1
	v_add3_u32 v48, v60, v48, s22
	s_waitcnt lgkmcnt(2)
	v_bfe_u32 v49, v62, 16, 1
	v_lshrrev_b32_e32 v48, 16, v48
	v_add3_u32 v49, v62, v49, s22
	v_and_or_b32 v48, v49, s23, v48
	s_waitcnt lgkmcnt(1)
	v_bfe_u32 v49, v64, 16, 1
	v_add_u32_e32 v70, 16, v68
	v_add3_u32 v49, v64, v49, s22
	s_waitcnt lgkmcnt(0)
	v_bfe_u32 v50, v66, 16, 1
	v_ashrrev_i32_e32 v71, 31, v70
	v_lshrrev_b32_e32 v49, 16, v49
	v_add3_u32 v50, v66, v50, s22
	v_lshlrev_b64 v[70:71], 11, v[70:71]
	v_and_or_b32 v49, v50, s23, v49
	v_lshl_add_u64 v[70:71], v[52:53], 0, v[70:71]
	global_store_dwordx4 v[70:71], v[46:49], off nt
	v_bfe_u32 v50, v67, 16, 1
	v_add3_u32 v50, v67, v50, s22
	v_bfe_u32 v46, v55, 16, 1
	v_add3_u32 v46, v55, v46, s22
	v_bfe_u32 v47, v51, 16, 1
	v_lshrrev_b32_e32 v46, 16, v46
	v_add3_u32 v47, v51, v47, s22
	v_and_or_b32 v46, v47, s23, v46
	v_bfe_u32 v47, v57, 16, 1
	v_add3_u32 v47, v57, v47, s22
	v_bfe_u32 v48, v59, 16, 1
	v_lshrrev_b32_e32 v47, 16, v47
	v_add3_u32 v48, v59, v48, s22
	v_and_or_b32 v47, v48, s23, v47
	v_bfe_u32 v48, v61, 16, 1
	v_add3_u32 v48, v61, v48, s22
	v_bfe_u32 v49, v63, 16, 1
	v_lshrrev_b32_e32 v48, 16, v48
	v_add3_u32 v49, v63, v49, s22
	v_and_or_b32 v48, v49, s23, v48
	v_bfe_u32 v49, v65, 16, 1
	v_add3_u32 v49, v65, v49, s22
	v_lshrrev_b32_e32 v49, 16, v49
	v_and_or_b32 v49, v50, s23, v49
	v_add_u32_e32 v50, 24, v68
	v_ashrrev_i32_e32 v51, 31, v50
	v_lshlrev_b64 v[50:51], 11, v[50:51]
	v_lshl_add_u64 v[50:51], v[52:53], 0, v[50:51]
	global_store_dwordx4 v[50:51], v[46:49], off nt
	s_waitcnt lgkmcnt(0)
	s_branch .LBB0_34

; #define LAS __attribute__((address_space(3)))
; __device__ __forceinline__ void tr_item8(const float* W, int ld, int K, int nblk, int item, unsigned char* WT, bool gu, float scale, LAS float* scr, int lane) {
;     const int kb = item / nblk, nb = item % nblk, k0 = 64 * kb, n0 = 32 * nb;
;     int drow0 = n0;
;     if (gu) { const int bj = n0 / FF, j = n0 - bj * FF; drow0 = 256 * (j / 128) + 128 * bj + (j % 128); }
;     { float t_[32];
; #pragma unroll
;       for (int i = 0; i < 32; ++i) t_[i] = W[(size_t)(k0 + 2 * i + (lane >> 5)) * ld + n0 + (lane & 31)];
; #pragma unroll
;       for (int i = 0; i < 32; ++i) scr[(2 * i + (lane >> 5)) * 33 + (lane & 31)] = t_[i] * scale; }
; __device__ __forceinline__ void convert_items(Frame& F, const Args& a, int lo, int hi, int w, int nw) {
;     ...
;     for (int it = lo + w; it < hi; it += nw) {
;         int r = it;
;         if (r < I_FI) { tr_item(a.in[7], 3 * D + 16, D, 96, r, (bf16*)(F.ws + WS_WFOXIN), false, scr, lane); continue; } r -= I_FI;
;         if (r < I_FO) { tr_item(a.in[9], D, D, 32, r, (bf16*)(F.ws + WS_WFOXOUT), false, scr, lane); continue; } r -= I_FO;
;         if (r < I_SI) { tr_item(a.in[10], D + 512, D, 48, r, (bf16*)(F.ws + WS_WSWAIN), false, scr, lane); continue; } r -= I_SI;
;         if (r < I_SO) { tr_item(a.in[12], D, D, 32, r, (bf16*)(F.ws + WS_WSWAOUT), false, scr, lane); continue; } r -= I_SO;
;         if (r < I_GU) { tr_item8(a.in[14], 2 * FF, D, 224, r, F.ws + WS_WGU, true, WSC_GU, scr, lane); continue; } r -= I_GU;
;         if (r < I_DN) { tr_item8(a.in[15], D, FF, 32, r, F.ws + WS_WDN, false, WSC_DN, scr, lane); continue; } r -= I_DN;
;         if (r < NE * I_GU) { const int e = r / I_GU, rr = r % I_GU; tr_item8(a.in[18] + (size_t)e * D * 2 * FF, 2 * FF, D, 224, rr, F.ws + WS_WMGU + (size_t)e * 2 * FF * D, true, WSC_GU, scr, lane); continue; } r -= NE * I_GU;
.LBB0_559:
	s_cmpk_gt_i32 s3, 0x5ff
	s_mov_b64 s[4:5], -1
	s_cbranch_scc0 .LBB0_581
	s_cmpk_gt_u32 s3, 0x7ff
	s_cbranch_scc0 .LBB0_578
	s_cmpk_gt_u32 s3, 0xaff
	s_cbranch_scc0 .LBB0_575
	s_cmpk_gt_u32 s3, 0xcff
	s_cbranch_scc0 .LBB0_572
	s_cmpk_gt_u32 s3, 0x1aff
	s_cbranch_scc0 .LBB0_569
	s_cmpk_gt_u32 s3, 0x21ff
	s_cbranch_scc0 .LBB0_566
	s_add_i32 s0, s3, 0xde00
	s_bfe_u32 s4, s0, 0x70009
	s_mulk_i32 s4, 0x2493
	s_lshr_b32 s4, s4, 16
	s_mulk_i32 s4, 0xe00
	s_sub_i32 s0, s0, s4
	s_bfe_u32 s4, s0, 0xb0005
	s_mulk_i32 s4, 0x2493
	s_lshr_b32 s4, s4, 16
	s_mul_i32 s5, s4, 0xe0
	s_sub_i32 s0, s0, s5
	s_lshl_b32 s5, s0, 5
	s_and_b32 s6, s0, 0xffff
	s_cmpk_gt_u32 s6, 0x6f
	s_cselect_b32 s17, 0xfffff200, 0
	s_cselect_b32 s18, 0x80, 0
	s_lshl_b32 s0, s0, 7
	s_lshl_b32 s4, s4, 6
	s_and_b32 s0, s0, 0x3ff80
	v_add_u32_e32 v64, s4, v28
	v_lshl_add_u64 v[46:47], v[24:25], 0, s[0:1]
	v_mad_i64_i32 v[48:49], s[6:7], v64, s12, v[46:47]
	v_add_u32_e32 v50, 2, v64
	v_add_u32_e32 v52, 4, v64
	v_add_u32_e32 v54, 6, v64
	v_add_u32_e32 v56, 8, v64
	v_add_u32_e32 v58, 10, v64
	v_add_u32_e32 v60, 12, v64
	v_add_u32_e32 v62, 14, v64
	v_mad_i64_i32 v[50:51], s[6:7], v50, s12, v[46:47]
	v_mad_i64_i32 v[52:53], s[6:7], v52, s12, v[46:47]
	v_mad_i64_i32 v[54:55], s[6:7], v54, s12, v[46:47]
	v_mad_i64_i32 v[56:57], s[6:7], v56, s12, v[46:47]
	v_mad_i64_i32 v[58:59], s[6:7], v58, s12, v[46:47]
	v_mad_i64_i32 v[60:61], s[6:7], v60, s12, v[46:47]
	v_mad_i64_i32 v[62:63], s[6:7], v62, s12, v[46:47]
	global_load_dword v65, v[48:49], off nt
	global_load_dword v66, v[50:51], off nt
	global_load_dword v67, v[52:53], off nt
	global_load_dword v68, v[54:55], off nt
	global_load_dword v69, v[56:57], off nt
	global_load_dword v70, v[58:59], off nt
	global_load_dword v71, v[60:61], off nt
	global_load_dword v72, v[62:63], off nt
	v_add_u32_e32 v48, 16, v64
	v_mad_i64_i32 v[48:49], s[6:7], v48, s12, v[46:47]
	v_add_u32_e32 v50, 18, v64
	v_add_u32_e32 v52, 20, v64
	v_add_u32_e32 v54, 22, v64
	v_add_u32_e32 v56, 24, v64
	v_add_u32_e32 v58, 26, v64
	v_add_u32_e32 v60, 28, v64
	v_add_u32_e32 v62, 30, v64
	v_mad_i64_i32 v[50:51], s[6:7], v50, s12, v[46:47]
	v_mad_i64_i32 v[52:53], s[6:7], v52, s12, v[46:47]
	v_mad_i64_i32 v[54:55], s[6:7], v54, s12, v[46:47]
	v_mad_i64_i32 v[56:57], s[6:7], v56, s12, v[46:47]
	v_mad_i64_i32 v[58:59], s[6:7], v58, s12, v[46:47]
	v_mad_i64_i32 v[60:61], s[6:7], v60, s12, v[46:47]
	v_mad_i64_i32 v[62:63], s[6:7], v62, s12, v[46:47]
	global_load_dword v73, v[48:49], off nt
	global_load_dword v74, v[50:51], off nt
	global_load_dword v75, v[52:53], off nt
	global_load_dword v76, v[54:55], off nt
	global_load_dword v77, v[56:57], off nt
	global_load_dword v78, v[58:59], off nt
	global_load_dword v79, v[60:61], off nt
	global_load_dword v80, v[62:63], off nt
	v_add_u32_e32 v48, 32, v64
	v_add_u32_e32 v50, 34, v64
	v_add_u32_e32 v52, 36, v64
	v_add_u32_e32 v54, 38, v64
	v_add_u32_e32 v60, 44, v64
	v_mad_i64_i32 v[48:49], s[6:7], v48, s12, v[46:47]
	v_mad_i64_i32 v[50:51], s[6:7], v50, s12, v[46:47]
	v_mad_i64_i32 v[52:53], s[6:7], v52, s12, v[46:47]
	v_mad_i64_i32 v[54:55], s[6:7], v54, s12, v[46:47]
	v_add_u32_e32 v56, 40, v64
	v_add_u32_e32 v58, 42, v64
	v_mad_i64_i32 v[60:61], s[6:7], v60, s12, v[46:47]
	v_add_u32_e32 v62, 46, v64
	v_mad_i64_i32 v[56:57], s[6:7], v56, s12, v[46:47]
	v_mad_i64_i32 v[58:59], s[6:7], v58, s12, v[46:47]
	v_mad_i64_i32 v[62:63], s[6:7], v62, s12, v[46:47]
	global_load_dword v81, v[48:49], off nt
	global_load_dword v82, v[50:51], off nt
	global_load_dword v83, v[52:53], off nt
	global_load_dword v84, v[54:55], off nt
	global_load_dword v85, v[56:57], off nt
	global_load_dword v86, v[58:59], off nt
	s_nop 0
	global_load_dword v60, v[60:61], off nt
	s_nop 0
	global_load_dword v61, v[62:63], off nt
	v_add_u32_e32 v48, 48, v64
	v_add_u32_e32 v50, 50, v64
	v_add_u32_e32 v52, 52, v64
	v_add_u32_e32 v54, 54, v64
	v_mad_i64_i32 v[48:49], s[6:7], v48, s12, v[46:47]
	v_mad_i64_i32 v[50:51], s[6:7], v50, s12, v[46:47]
	v_mad_i64_i32 v[52:53], s[6:7], v52, s12, v[46:47]
	v_mad_i64_i32 v[54:55], s[6:7], v54, s12, v[46:47]
	v_add_u32_e32 v56, 56, v64
	v_add_u32_e32 v58, 58, v64
	v_mad_i64_i32 v[56:57], s[6:7], v56, s12, v[46:47]
	v_mad_i64_i32 v[58:59], s[6:7], v58, s12, v[46:47]
	global_load_dword v62, v[48:49], off nt
	s_nop 0
	global_load_dword v50, v[50:51], off nt
	s_nop 0
	global_load_dword v51, v[52:53], off nt
	s_nop 0
	global_load_dword v52, v[54:55], off nt
	global_load_dword v53, v[56:57], off nt
	s_nop 0
	global_load_dword v54, v[58:59], off nt
	v_add_u32_e32 v48, 60, v64
	v_add_u32_e32 v55, 62, v64
	v_mad_i64_i32 v[48:49], s[6:7], v48, s12, v[46:47]
	v_mad_i64_i32 v[46:47], s[6:7], v55, s12, v[46:47]
	global_load_dword v48, v[48:49], off nt
	s_nop 0
	global_load_dword v46, v[46:47], off nt
	s_waitcnt vmcnt(0)
; __device__ __forceinline__ unsigned cvt_pk4_fp8(float a, float b, float c, float d) { int w = 0; w = __builtin_amdgcn_cvt_pk_fp8_f32(a, b, w, false); w = __builtin_amdgcn_cvt_pk_fp8_f32(c, d, w, true); return (unsigned)w; }
; #define GAS __attribute__((address_space(1)))
; #define LAS __attribute__((address_space(3)))
; #define LDS_WAIT() asm volatile("s_waitcnt lgkmcnt(0)" ::: "memory")
; __device__ __forceinline__ void tr_item8(const float* W, int ld, int K, int nblk, int item, unsigned char* WT, bool gu, float scale, LAS float* scr, int lane) {
;     ...
;       for (int i = 0; i < 32; ++i) scr[(2 * i + (lane >> 5)) * 33 + (lane & 31)] = t_[i] * scale; }
;     LDS_WAIT(); asm volatile("" ::: "memory");
;     const int c = lane & 3;
; #pragma unroll
;     for (int j = 0; j < 2; ++j) { const int n = (lane >> 2) + 16 * j; const LAS float* sp = scr + (16 * c) * 33 + n;
;         v4u o; o.x = pg8::cvt_pk4_fp8(sp[0 * 33], sp[1 * 33], sp[2 * 33], sp[3 * 33]); o.y = pg8::cvt_pk4_fp8(sp[4 * 33], sp[5 * 33], sp[6 * 33], sp[7 * 33]);
;         o.z = pg8::cvt_pk4_fp8(sp[8 * 33], sp[9 * 33], sp[10 * 33], sp[11 * 33]); o.w = pg8::cvt_pk4_fp8(sp[12 * 33], sp[13 * 33], sp[14 * 33], sp[15 * 33]);
;         *(GAS v4u*)(WT + (size_t)(drow0 + n) * K + k0 + 16 * c) = o; }
;     LDS_WAIT(); asm volatile("" ::: "memory");
	v_mul_f32_e32 v47, 0x42800000, v65
	v_mul_f32_e32 v49, 0x42800000, v66
	ds_write2_b32 v29, v47, v49 offset1:66
	v_mul_f32_e32 v47, 0x42800000, v67
	v_mul_f32_e32 v49, 0x42800000, v68
	ds_write2_b32 v29, v47, v49 offset0:132 offset1:198
	v_mul_f32_e32 v47, 0x42800000, v69
	v_mul_f32_e32 v49, 0x42800000, v70
	ds_write2_b32 v38, v47, v49 offset0:8 offset1:74
	v_mul_f32_e32 v47, 0x42800000, v71
	v_mul_f32_e32 v49, 0x42800000, v72
	ds_write2_b32 v38, v47, v49 offset0:140 offset1:206
	s_add_i32 s0, s17, s5
	s_sext_i32_i16 s5, s0
	s_bfe_u32 s5, s5, 0x70018
	s_add_i32 s5, s0, s5
	s_sext_i32_i16 s6, s5
	s_and_b32 s5, s5, 0xff80
	s_sub_i32 s0, s0, s5
	s_lshl_b32 s6, s6, 1
	s_sext_i32_i16 s0, s0
	v_mul_f32_e32 v47, 0x42800000, v73
	v_mul_f32_e32 v49, 0x42800000, v74
	ds_write2_b32 v39, v47, v49 offset0:16 offset1:82
	v_mul_f32_e32 v47, 0x42800000, v75
	v_mul_f32_e32 v49, 0x42800000, v76
	ds_write2_b32 v39, v47, v49 offset0:148 offset1:214
	v_mul_f32_e32 v47, 0x42800000, v77
	v_mul_f32_e32 v49, 0x42800000, v78
	ds_write2_b32 v40, v47, v49 offset0:24 offset1:90
	v_mul_f32_e32 v47, 0x42800000, v79
	v_mul_f32_e32 v49, 0x42800000, v80
	ds_write2_b32 v40, v47, v49 offset0:156 offset1:222
	s_and_b32 s6, s6, 0xffffff00
	s_add_i32 s0, s18, s0
	s_add_i32 s0, s0, s6
	s_mov_b32 s5, s1
	v_mul_f32_e32 v47, 0x42800000, v81
	v_mul_f32_e32 v49, 0x42800000, v82
	ds_write2_b32 v41, v47, v49 offset0:32 offset1:98
	v_mul_f32_e32 v47, 0x42800000, v83
	v_mul_f32_e32 v49, 0x42800000, v84
	ds_write2_b32 v41, v47, v49 offset0:164 offset1:230
	v_mul_f32_e32 v47, 0x42800000, v85
	v_mul_f32_e32 v49, 0x42800000, v86
	ds_write2_b32 v42, v47, v49 offset0:40 offset1:106
	v_mul_f32_e32 v47, 0x42800000, v60
	v_mul_f32_e32 v49, 0x42800000, v61
	ds_write2_b32 v42, v47, v49 offset0:172 offset1:238
	v_add_u32_e32 v84, s0, v30
	v_ashrrev_i32_e32 v85, 31, v84
	v_lshlrev_b64 v[84:85], 10, v[84:85]
	v_mul_f32_e32 v47, 0x42800000, v62
	v_mul_f32_e32 v49, 0x42800000, v50
	ds_write2_b32 v43, v47, v49 offset0:48 offset1:114
	v_mul_f32_e32 v47, 0x42800000, v51
	v_mul_f32_e32 v49, 0x42800000, v52
	ds_write2_b32 v43, v47, v49 offset0:180 offset1:246
	v_mul_f32_e32 v47, 0x42800000, v53
	v_mul_f32_e32 v49, 0x42800000, v54
	ds_write2_b32 v44, v47, v49 offset0:56 offset1:122
	v_mov_b32_e32 v49, 0
	v_lshl_add_u64 v[50:51], v[26:27], 0, s[4:5]
	v_mul_f32_e32 v47, 0x42800000, v48
	v_mul_f32_e32 v46, 0x42800000, v46
	ds_write2_b32 v44, v47, v46 offset0:188 offset1:254
	s_waitcnt lgkmcnt(0)
	ds_read2_b32 v[52:53], v31 offset1:16
	ds_read2_b32 v[54:55], v31 offset0:33 offset1:49
	ds_read2_b32 v[56:57], v31 offset0:66 offset1:82
	ds_read2_b32 v[58:59], v31 offset0:99 offset1:115
	ds_read2_b32 v[60:61], v31 offset0:132 offset1:148
	ds_read2_b32 v[62:63], v31 offset0:165 offset1:181
	ds_read2_b32 v[64:65], v31 offset0:198 offset1:214
	ds_read2_b32 v[66:67], v31 offset0:231 offset1:247
	ds_read2_b32 v[68:69], v45 offset0:8 offset1:24
	ds_read2_b32 v[70:71], v45 offset0:41 offset1:57
	ds_read2_b32 v[72:73], v45 offset0:74 offset1:90
	ds_read2_b32 v[74:75], v45 offset0:107 offset1:123
	ds_read2_b32 v[76:77], v45 offset0:140 offset1:156
	ds_read2_b32 v[78:79], v45 offset0:173 offset1:189
	v_mov_b32_e32 v46, 0
	v_mov_b32_e32 v47, 0
	v_mov_b32_e32 v48, 0
	ds_read2_b32 v[80:81], v45 offset0:206 offset1:222
	ds_read2_b32 v[82:83], v45 offset0:239 offset1:255
	s_waitcnt lgkmcnt(14)
	v_cvt_pk_fp8_f32 v46, v52, v54
	s_waitcnt lgkmcnt(10)
	v_cvt_pk_fp8_f32 v47, v60, v62
	s_waitcnt lgkmcnt(6)
	v_cvt_pk_fp8_f32 v48, v68, v70
	s_waitcnt lgkmcnt(2)
	v_cvt_pk_fp8_f32 v49, v76, v78
	v_cvt_pk_fp8_f32 v46, v56, v58 op_sel:[0,0,1]
	v_cvt_pk_fp8_f32 v47, v64, v66 op_sel:[0,0,1]
	v_cvt_pk_fp8_f32 v48, v72, v74 op_sel:[0,0,1]
	s_waitcnt lgkmcnt(0)
	v_cvt_pk_fp8_f32 v49, v80, v82 op_sel:[0,0,1]
	v_lshl_add_u64 v[84:85], v[50:51], 0, v[84:85]
	v_add_u32_e32 v52, s0, v32
	s_mov_b64 s[4:5], 0
	global_store_dwordx4 v[84:85], v[46:49], off nt
	s_nop 1
	v_mov_b32_e32 v46, 0
	v_mov_b32_e32 v47, 0
	v_mov_b32_e32 v48, 0
	v_mov_b32_e32 v49, 0
	v_cvt_pk_fp8_f32 v46, v53, v55
	v_cvt_pk_fp8_f32 v47, v61, v63
	v_cvt_pk_fp8_f32 v48, v69, v71
	v_cvt_pk_fp8_f32 v49, v77, v79
	v_cvt_pk_fp8_f32 v46, v57, v59 op_sel:[0,0,1]
	v_cvt_pk_fp8_f32 v47, v65, v67 op_sel:[0,0,1]
	v_cvt_pk_fp8_f32 v48, v73, v75 op_sel:[0,0,1]
	v_cvt_pk_fp8_f32 v49, v81, v83 op_sel:[0,0,1]
	v_ashrrev_i32_e32 v53, 31, v52
	v_lshlrev_b64 v[52:53], 10, v[52:53]
	v_lshl_add_u64 v[50:51], v[50:51], 0, v[52:53]
	global_store_dwordx4 v[50:51], v[46:49], off nt
	s_waitcnt lgkmcnt(0)
; #define LAS __attribute__((address_space(3)))
; __device__ __forceinline__ void tr_item8(const float* W, int ld, int K, int nblk, int item, unsigned char* WT, bool gu, float scale, LAS float* scr, int lane) {
;     const int kb = item / nblk, nb = item % nblk, k0 = 64 * kb, n0 = 32 * nb;
;     int drow0 = n0;
;     if (gu) { const int bj = n0 / FF, j = n0 - bj * FF; drow0 = 256 * (j / 128) + 128 * bj + (j % 128); }
;     { float t_[32];
; #pragma unroll
;       for (int i = 0; i < 32; ++i) t_[i] = W[(size_t)(k0 + 2 * i + (lane >> 5)) * ld + n0 + (lane & 31)];
; #pragma unroll
;       for (int i = 0; i < 32; ++i) scr[(2 * i + (lane >> 5)) * 33 + (lane & 31)] = t_[i] * scale; }
; __device__ __forceinline__ void convert_items(Frame& F, const Args& a, int lo, int hi, int w, int nw) {
;     ...
;         if (r < I_DN) { tr_item8(a.in[15], D, FF, 32, r, F.ws + WS_WDN, false, WSC_DN, scr, lane); continue; } r -= I_DN;
.LBB0_566:
	s_andn2_b64 vcc, exec, s[4:5]
	s_cbranch_vccnz .LBB0_568
	s_lshl_b32 s0, s3, 5
	s_and_b32 s4, s10, 0x1ffc0
	s_and_b32 s6, s0, 0x3e0
	v_add_u32_e32 v46, s4, v28
	s_lshl_b32 s0, s6, 2
	v_ashrrev_i32_e32 v47, 31, v46
	v_lshl_add_u64 v[48:49], v[0:1], 0, s[0:1]
	v_lshlrev_b64 v[46:47], 12, v[46:47]
	v_lshl_add_u64 v[46:47], v[48:49], 0, v[46:47]
	v_add_co_u32_e32 v48, vcc, 0x2000, v46
	s_mov_b32 s5, s1
	s_nop 0
	v_addc_co_u32_e32 v49, vcc, 0, v47, vcc
	v_add_co_u32_e32 v50, vcc, 0x4000, v46
	s_nop 1
	v_addc_co_u32_e32 v51, vcc, 0, v47, vcc
	v_add_co_u32_e32 v52, vcc, 0x6000, v46
	s_nop 1
	v_addc_co_u32_e32 v53, vcc, 0, v47, vcc
	v_add_co_u32_e32 v54, vcc, 0x8000, v46
	s_nop 1
	v_addc_co_u32_e32 v55, vcc, 0, v47, vcc
	v_add_co_u32_e32 v56, vcc, 0xa000, v46
	s_nop 1
	v_addc_co_u32_e32 v57, vcc, 0, v47, vcc
	v_add_co_u32_e32 v58, vcc, 0xc000, v46
	s_nop 1
	v_addc_co_u32_e32 v59, vcc, 0, v47, vcc
	v_add_co_u32_e32 v60, vcc, 0xe000, v46
	s_nop 1
	v_addc_co_u32_e32 v61, vcc, 0, v47, vcc
	global_load_dword v64, v[46:47], off nt
	global_load_dword v65, v[48:49], off nt
	global_load_dword v66, v[50:51], off nt
	global_load_dword v67, v[52:53], off nt
	global_load_dword v68, v[54:55], off nt
	global_load_dword v69, v[56:57], off nt
	global_load_dword v70, v[58:59], off nt
	global_load_dword v71, v[60:61], off nt
	v_add_co_u32_e32 v48, vcc, 0x10000, v46
	s_nop 1
	v_addc_co_u32_e32 v49, vcc, 0, v47, vcc
	v_add_co_u32_e32 v50, vcc, 0x12000, v46
	s_nop 1
	v_addc_co_u32_e32 v51, vcc, 0, v47, vcc
	v_add_co_u32_e32 v52, vcc, 0x14000, v46
	s_nop 1
	v_addc_co_u32_e32 v53, vcc, 0, v47, vcc
	v_add_co_u32_e32 v54, vcc, 0x16000, v46
	s_nop 1
	v_addc_co_u32_e32 v55, vcc, 0, v47, vcc
	v_add_co_u32_e32 v56, vcc, 0x18000, v46
	s_nop 1
	v_addc_co_u32_e32 v57, vcc, 0, v47, vcc
	v_add_co_u32_e32 v58, vcc, 0x1a000, v46
	s_nop 1
	v_addc_co_u32_e32 v59, vcc, 0, v47, vcc
	v_add_co_u32_e32 v60, vcc, 0x1c000, v46
	s_nop 1
	v_addc_co_u32_e32 v61, vcc, 0, v47, vcc
	v_add_co_u32_e32 v62, vcc, 0x1e000, v46
	s_nop 1
	v_addc_co_u32_e32 v63, vcc, 0, v47, vcc
	global_load_dword v72, v[48:49], off nt
	global_load_dword v73, v[50:51], off nt
	global_load_dword v74, v[52:53], off nt
	global_load_dword v75, v[54:55], off nt
	global_load_dword v76, v[56:57], off nt
	global_load_dword v77, v[58:59], off nt
	global_load_dword v78, v[60:61], off nt
	global_load_dword v79, v[62:63], off nt
	v_add_co_u32_e32 v48, vcc, 0x20000, v46
	s_nop 1
	v_addc_co_u32_e32 v49, vcc, 0, v47, vcc
	v_add_co_u32_e32 v50, vcc, 0x22000, v46
	s_nop 1
	v_addc_co_u32_e32 v51, vcc, 0, v47, vcc
	v_add_co_u32_e32 v52, vcc, 0x24000, v46
	s_nop 1
	v_addc_co_u32_e32 v53, vcc, 0, v47, vcc
	v_add_co_u32_e32 v54, vcc, 0x26000, v46
	s_nop 1
	v_addc_co_u32_e32 v55, vcc, 0, v47, vcc
	v_add_co_u32_e32 v56, vcc, 0x28000, v46
	s_nop 1
	v_addc_co_u32_e32 v57, vcc, 0, v47, vcc
	v_add_co_u32_e32 v58, vcc, 0x2a000, v46
	s_nop 1
	v_addc_co_u32_e32 v59, vcc, 0, v47, vcc
	v_add_co_u32_e32 v60, vcc, 0x2c000, v46
	s_nop 1
	v_addc_co_u32_e32 v61, vcc, 0, v47, vcc
	v_add_co_u32_e32 v62, vcc, 0x2e000, v46
	s_nop 1
	v_addc_co_u32_e32 v63, vcc, 0, v47, vcc
	global_load_dword v80, v[48:49], off nt
	global_load_dword v81, v[50:51], off nt
	global_load_dword v82, v[52:53], off nt
	global_load_dword v83, v[54:55], off nt
	global_load_dword v84, v[56:57], off nt
	global_load_dword v85, v[58:59], off nt
	s_nop 0
	global_load_dword v60, v[60:61], off nt
	s_nop 0
	global_load_dword v61, v[62:63], off nt
	v_add_co_u32_e32 v48, vcc, 0x30000, v46
	s_nop 1
	v_addc_co_u32_e32 v49, vcc, 0, v47, vcc
	v_add_co_u32_e32 v50, vcc, 0x32000, v46
	s_nop 1
	v_addc_co_u32_e32 v51, vcc, 0, v47, vcc
	v_add_co_u32_e32 v52, vcc, 0x34000, v46
	s_nop 1
	v_addc_co_u32_e32 v53, vcc, 0, v47, vcc
	v_add_co_u32_e32 v54, vcc, 0x36000, v46
	s_nop 1
	v_addc_co_u32_e32 v55, vcc, 0, v47, vcc
	v_add_co_u32_e32 v56, vcc, 0x38000, v46
	s_nop 1
	v_addc_co_u32_e32 v57, vcc, 0, v47, vcc
	v_add_co_u32_e32 v58, vcc, 0x3a000, v46
	s_nop 1
	v_addc_co_u32_e32 v59, vcc, 0, v47, vcc
	global_load_dword v62, v[48:49], off nt
	s_nop 0
	global_load_dword v50, v[50:51], off nt
	s_nop 0
	global_load_dword v51, v[52:53], off nt
	s_nop 0
	global_load_dword v52, v[54:55], off nt
	global_load_dword v53, v[56:57], off nt
	s_nop 0
	global_load_dword v54, v[58:59], off nt
	v_add_co_u32_e32 v48, vcc, 0x3c000, v46
	s_nop 1
	v_addc_co_u32_e32 v49, vcc, 0, v47, vcc
	v_add_co_u32_e32 v46, vcc, 0x3e000, v46
	s_nop 1
	v_addc_co_u32_e32 v47, vcc, 0, v47, vcc
	global_load_dword v48, v[48:49], off nt
	s_nop 0
	global_load_dword v46, v[46:47], off nt
	s_waitcnt vmcnt(0)
; __device__ __forceinline__ unsigned cvt_pk4_fp8(float a, float b, float c, float d) { int w = 0; w = __builtin_amdgcn_cvt_pk_fp8_f32(a, b, w, false); w = __builtin_amdgcn_cvt_pk_fp8_f32(c, d, w, true); return (unsigned)w; }
; #define GAS __attribute__((address_space(1)))
; #define LAS __attribute__((address_space(3)))
; #define LDS_WAIT() asm volatile("s_waitcnt lgkmcnt(0)" ::: "memory")
; __device__ __forceinline__ void tr_item8(const float* W, int ld, int K, int nblk, int item, unsigned char* WT, bool gu, float scale, LAS float* scr, int lane) {
;     ...
;       for (int i = 0; i < 32; ++i) scr[(2 * i + (lane >> 5)) * 33 + (lane & 31)] = t_[i] * scale; }
;     LDS_WAIT(); asm volatile("" ::: "memory");
;     const int c = lane & 3;
; #pragma unroll
;     for (int j = 0; j < 2; ++j) { const int n = (lane >> 2) + 16 * j; const LAS float* sp = scr + (16 * c) * 33 + n;
;         v4u o; o.x = pg8::cvt_pk4_fp8(sp[0 * 33], sp[1 * 33], sp[2 * 33], sp[3 * 33]); o.y = pg8::cvt_pk4_fp8(sp[4 * 33], sp[5 * 33], sp[6 * 33], sp[7 * 33]);
;         o.z = pg8::cvt_pk4_fp8(sp[8 * 33], sp[9 * 33], sp[10 * 33], sp[11 * 33]); o.w = pg8::cvt_pk4_fp8(sp[12 * 33], sp[13 * 33], sp[14 * 33], sp[15 * 33]);
;         *(GAS v4u*)(WT + (size_t)(drow0 + n) * K + k0 + 16 * c) = o; }
;     LDS_WAIT(); asm volatile("" ::: "memory");
	v_mul_f32_e32 v47, 0x43000000, v64
	v_mul_f32_e32 v49, 0x43000000, v65
	ds_write2_b32 v29, v47, v49 offset1:66
	v_mul_f32_e32 v47, 0x43000000, v66
	v_mul_f32_e32 v49, 0x43000000, v67
	ds_write2_b32 v29, v47, v49 offset0:132 offset1:198
	v_mul_f32_e32 v47, 0x43000000, v68
	v_mul_f32_e32 v49, 0x43000000, v69
	ds_write2_b32 v38, v47, v49 offset0:8 offset1:74
	v_mul_f32_e32 v47, 0x43000000, v70
	v_mul_f32_e32 v49, 0x43000000, v71
	ds_write2_b32 v38, v47, v49 offset0:140 offset1:206
	v_mul_f32_e32 v47, 0x43000000, v72
	v_mul_f32_e32 v49, 0x43000000, v73
	ds_write2_b32 v39, v47, v49 offset0:16 offset1:82
	v_mul_f32_e32 v47, 0x43000000, v74
	v_mul_f32_e32 v49, 0x43000000, v75
	ds_write2_b32 v39, v47, v49 offset0:148 offset1:214
	v_mul_f32_e32 v47, 0x43000000, v76
	v_mul_f32_e32 v49, 0x43000000, v77
	ds_write2_b32 v40, v47, v49 offset0:24 offset1:90
	v_mul_f32_e32 v47, 0x43000000, v78
	v_mul_f32_e32 v49, 0x43000000, v79
	ds_write2_b32 v40, v47, v49 offset0:156 offset1:222
	v_mul_f32_e32 v47, 0x43000000, v80
	v_mul_f32_e32 v49, 0x43000000, v81
	ds_write2_b32 v41, v47, v49 offset0:32 offset1:98
	v_mul_f32_e32 v47, 0x43000000, v82
	v_mul_f32_e32 v49, 0x43000000, v83
	ds_write2_b32 v41, v47, v49 offset0:164 offset1:230
	v_mul_f32_e32 v47, 0x43000000, v84
	v_mul_f32_e32 v49, 0x43000000, v85
	ds_write2_b32 v42, v47, v49 offset0:40 offset1:106
	v_mul_f32_e32 v47, 0x43000000, v60
	v_mul_f32_e32 v49, 0x43000000, v61
	ds_write2_b32 v42, v47, v49 offset0:172 offset1:238
	v_mul_f32_e32 v47, 0x43000000, v62
	v_mul_f32_e32 v49, 0x43000000, v50
	ds_write2_b32 v43, v47, v49 offset0:48 offset1:114
	v_mul_f32_e32 v47, 0x43000000, v51
	v_mul_f32_e32 v49, 0x43000000, v52
	ds_write2_b32 v43, v47, v49 offset0:180 offset1:246
	v_mul_f32_e32 v47, 0x43000000, v53
	v_mul_f32_e32 v49, 0x43000000, v54
	ds_write2_b32 v44, v47, v49 offset0:56 offset1:122
	v_mov_b32_e32 v49, 0
	v_lshl_add_u64 v[50:51], v[12:13], 0, s[4:5]
	v_mul_f32_e32 v47, 0x43000000, v48
	v_mul_f32_e32 v46, 0x43000000, v46
	ds_write2_b32 v44, v47, v46 offset0:188 offset1:254
	s_waitcnt lgkmcnt(0)
	ds_read2_b32 v[52:53], v31 offset1:16
	ds_read2_b32 v[54:55], v31 offset0:33 offset1:49
	ds_read2_b32 v[56:57], v31 offset0:66 offset1:82
	ds_read2_b32 v[58:59], v31 offset0:99 offset1:115
	ds_read2_b32 v[60:61], v31 offset0:132 offset1:148
	ds_read2_b32 v[62:63], v31 offset0:165 offset1:181
	ds_read2_b32 v[64:65], v31 offset0:198 offset1:214
	ds_read2_b32 v[66:67], v31 offset0:231 offset1:247
	ds_read2_b32 v[68:69], v45 offset0:8 offset1:24
	ds_read2_b32 v[70:71], v45 offset0:41 offset1:57
	ds_read2_b32 v[72:73], v45 offset0:74 offset1:90
	ds_read2_b32 v[74:75], v45 offset0:107 offset1:123
	ds_read2_b32 v[76:77], v45 offset0:140 offset1:156
	ds_read2_b32 v[78:79], v45 offset0:173 offset1:189
	v_mov_b32_e32 v46, 0
	v_mov_b32_e32 v47, 0
	v_mov_b32_e32 v48, 0
	ds_read2_b32 v[80:81], v45 offset0:206 offset1:222
	ds_read2_b32 v[82:83], v45 offset0:239 offset1:255
	s_waitcnt lgkmcnt(14)
	v_cvt_pk_fp8_f32 v46, v52, v54
	s_waitcnt lgkmcnt(10)
	v_cvt_pk_fp8_f32 v47, v60, v62
	s_waitcnt lgkmcnt(6)
	v_cvt_pk_fp8_f32 v48, v68, v70
	s_waitcnt lgkmcnt(2)
	v_cvt_pk_fp8_f32 v49, v76, v78
	v_cvt_pk_fp8_f32 v46, v56, v58 op_sel:[0,0,1]
	v_cvt_pk_fp8_f32 v47, v64, v66 op_sel:[0,0,1]
	v_cvt_pk_fp8_f32 v48, v72, v74 op_sel:[0,0,1]
	s_waitcnt lgkmcnt(0)
	v_cvt_pk_fp8_f32 v49, v80, v82 op_sel:[0,0,1]
	v_add_u32_e32 v52, s6, v30
	v_mad_i64_i32 v[84:85], s[4:5], v52, s11, v[50:51]
	global_store_dwordx4 v[84:85], v[46:49], off nt
	v_add_u32_e32 v52, s6, v32
	v_mad_i64_i32 v[50:51], s[4:5], v52, s11, v[50:51]
	v_mov_b32_e32 v46, 0
	v_mov_b32_e32 v47, 0
	v_mov_b32_e32 v48, 0
	v_mov_b32_e32 v49, 0
	v_cvt_pk_fp8_f32 v46, v53, v55
	v_cvt_pk_fp8_f32 v47, v61, v63
	v_cvt_pk_fp8_f32 v48, v69, v71
	v_cvt_pk_fp8_f32 v49, v77, v79
	v_cvt_pk_fp8_f32 v46, v57, v59 op_sel:[0,0,1]
	v_cvt_pk_fp8_f32 v47, v65, v67 op_sel:[0,0,1]
	v_cvt_pk_fp8_f32 v48, v73, v75 op_sel:[0,0,1]
	v_cvt_pk_fp8_f32 v49, v81, v83 op_sel:[0,0,1]
	global_store_dwordx4 v[50:51], v[46:49], off nt
	s_waitcnt lgkmcnt(0)

; #define LAS __attribute__((address_space(3)))
; __device__ __forceinline__ void tr_item8(const float* W, int ld, int K, int nblk, int item, unsigned char* WT, bool gu, float scale, LAS float* scr, int lane) {
;     const int kb = item / nblk, nb = item % nblk, k0 = 64 * kb, n0 = 32 * nb;
;     int drow0 = n0;
;     if (gu) { const int bj = n0 / FF, j = n0 - bj * FF; drow0 = 256 * (j / 128) + 128 * bj + (j % 128); }
;     { float t_[32];
; #pragma unroll
;       for (int i = 0; i < 32; ++i) t_[i] = W[(size_t)(k0 + 2 * i + (lane >> 5)) * ld + n0 + (lane & 31)];
; #pragma unroll
;       for (int i = 0; i < 32; ++i) scr[(2 * i + (lane >> 5)) * 33 + (lane & 31)] = t_[i] * scale; }
; __device__ __forceinline__ void convert_items(Frame& F, const Args& a, int lo, int hi, int w, int nw) {
;     ...
;         if (r < I_GU) { tr_item8(a.in[14], 2 * FF, D, 224, r, F.ws + WS_WGU, true, WSC_GU, scr, lane); continue; } r -= I_GU;
.LBB0_569:
	s_andn2_b64 vcc, exec, s[4:5]
	s_cbranch_vccnz .LBB0_571
	s_add_i32 s0, s3, 0xf300
	s_bfe_u32 s4, s0, 0xb0005
	s_mulk_i32 s4, 0x2493
	s_lshr_b32 s4, s4, 16
	s_mul_i32 s5, s4, 0xe0
	s_sub_i32 s0, s0, s5
	s_lshl_b32 s5, s0, 5
	s_and_b32 s6, s0, 0xffff
	s_cmpk_gt_u32 s6, 0x6f
	s_cselect_b32 s17, 0xfffff200, 0
	s_cselect_b32 s18, 0x80, 0
	s_lshl_b32 s0, s0, 7
	s_lshl_b32 s4, s4, 6
	s_and_b32 s0, s0, 0x3ff80
	v_add_u32_e32 v64, s4, v28
	v_lshl_add_u64 v[46:47], v[2:3], 0, s[0:1]
	v_mad_i64_i32 v[48:49], s[6:7], v64, s12, v[46:47]
	v_add_u32_e32 v50, 2, v64
	v_add_u32_e32 v52, 4, v64
	v_add_u32_e32 v54, 6, v64
	v_add_u32_e32 v56, 8, v64
	v_add_u32_e32 v58, 10, v64
	v_add_u32_e32 v60, 12, v64
	v_add_u32_e32 v62, 14, v64
	v_mad_i64_i32 v[50:51], s[6:7], v50, s12, v[46:47]
	v_mad_i64_i32 v[52:53], s[6:7], v52, s12, v[46:47]
	v_mad_i64_i32 v[54:55], s[6:7], v54, s12, v[46:47]
	v_mad_i64_i32 v[56:57], s[6:7], v56, s12, v[46:47]
	v_mad_i64_i32 v[58:59], s[6:7], v58, s12, v[46:47]
	v_mad_i64_i32 v[60:61], s[6:7], v60, s12, v[46:47]
	v_mad_i64_i32 v[62:63], s[6:7], v62, s12, v[46:47]
	global_load_dword v65, v[48:49], off nt
	global_load_dword v66, v[50:51], off nt
	global_load_dword v67, v[52:53], off nt
	global_load_dword v68, v[54:55], off nt
	global_load_dword v69, v[56:57], off nt
	global_load_dword v70, v[58:59], off nt
	global_load_dword v71, v[60:61], off nt
	global_load_dword v72, v[62:63], off nt
	v_add_u32_e32 v48, 16, v64
	v_mad_i64_i32 v[48:49], s[6:7], v48, s12, v[46:47]
	v_add_u32_e32 v50, 18, v64
	v_add_u32_e32 v52, 20, v64
	v_add_u32_e32 v54, 22, v64
	v_add_u32_e32 v56, 24, v64
	v_add_u32_e32 v58, 26, v64
	v_add_u32_e32 v60, 28, v64
	v_add_u32_e32 v62, 30, v64
	v_mad_i64_i32 v[50:51], s[6:7], v50, s12, v[46:47]
	v_mad_i64_i32 v[52:53], s[6:7], v52, s12, v[46:47]
	v_mad_i64_i32 v[54:55], s[6:7], v54, s12, v[46:47]
	v_mad_i64_i32 v[56:57], s[6:7], v56, s12, v[46:47]
	v_mad_i64_i32 v[58:59], s[6:7], v58, s12, v[46:47]
	v_mad_i64_i32 v[60:61], s[6:7], v60, s12, v[46:47]
	v_mad_i64_i32 v[62:63], s[6:7], v62, s12, v[46:47]
	global_load_dword v73, v[48:49], off nt
	global_load_dword v74, v[50:51], off nt
	global_load_dword v75, v[52:53], off nt
	global_load_dword v76, v[54:55], off nt
	global_load_dword v77, v[56:57], off nt
	global_load_dword v78, v[58:59], off nt
	global_load_dword v79, v[60:61], off nt
	global_load_dword v80, v[62:63], off nt
	v_add_u32_e32 v48, 32, v64
	v_add_u32_e32 v50, 34, v64
	v_add_u32_e32 v52, 36, v64
	v_add_u32_e32 v54, 38, v64
	v_add_u32_e32 v60, 44, v64
	v_mad_i64_i32 v[48:49], s[6:7], v48, s12, v[46:47]
	v_mad_i64_i32 v[50:51], s[6:7], v50, s12, v[46:47]
	v_mad_i64_i32 v[52:53], s[6:7], v52, s12, v[46:47]
	v_mad_i64_i32 v[54:55], s[6:7], v54, s12, v[46:47]
	v_add_u32_e32 v56, 40, v64
	v_add_u32_e32 v58, 42, v64
	v_mad_i64_i32 v[60:61], s[6:7], v60, s12, v[46:47]
	v_add_u32_e32 v62, 46, v64
	v_mad_i64_i32 v[56:57], s[6:7], v56, s12, v[46:47]
	v_mad_i64_i32 v[58:59], s[6:7], v58, s12, v[46:47]
	v_mad_i64_i32 v[62:63], s[6:7], v62, s12, v[46:47]
	global_load_dword v81, v[48:49], off nt
	global_load_dword v82, v[50:51], off nt
	global_load_dword v83, v[52:53], off nt
	global_load_dword v84, v[54:55], off nt
	global_load_dword v85, v[56:57], off nt
	global_load_dword v86, v[58:59], off nt
	s_nop 0
	global_load_dword v60, v[60:61], off nt
	s_nop 0
	global_load_dword v61, v[62:63], off nt
	v_add_u32_e32 v48, 48, v64
	v_add_u32_e32 v50, 50, v64
	v_add_u32_e32 v52, 52, v64
	v_add_u32_e32 v54, 54, v64
	v_mad_i64_i32 v[48:49], s[6:7], v48, s12, v[46:47]
	v_mad_i64_i32 v[50:51], s[6:7], v50, s12, v[46:47]
	v_mad_i64_i32 v[52:53], s[6:7], v52, s12, v[46:47]
	v_mad_i64_i32 v[54:55], s[6:7], v54, s12, v[46:47]
	v_add_u32_e32 v56, 56, v64
	v_add_u32_e32 v58, 58, v64
	v_mad_i64_i32 v[56:57], s[6:7], v56, s12, v[46:47]
	v_mad_i64_i32 v[58:59], s[6:7], v58, s12, v[46:47]
	global_load_dword v62, v[48:49], off nt
	s_nop 0
	global_load_dword v50, v[50:51], off nt
	s_nop 0
	global_load_dword v51, v[52:53], off nt
	s_nop 0
	global_load_dword v52, v[54:55], off nt
	global_load_dword v53, v[56:57], off nt
	s_nop 0
	global_load_dword v54, v[58:59], off nt
	v_add_u32_e32 v48, 60, v64
	v_add_u32_e32 v55, 62, v64
	v_mad_i64_i32 v[48:49], s[6:7], v48, s12, v[46:47]
	v_mad_i64_i32 v[46:47], s[6:7], v55, s12, v[46:47]
	global_load_dword v48, v[48:49], off nt
	s_nop 0
	global_load_dword v46, v[46:47], off nt
	s_waitcnt vmcnt(0)
; __device__ __forceinline__ unsigned cvt_pk4_fp8(float a, float b, float c, float d) { int w = 0; w = __builtin_amdgcn_cvt_pk_fp8_f32(a, b, w, false); w = __builtin_amdgcn_cvt_pk_fp8_f32(c, d, w, true); return (unsigned)w; }
; #define GAS __attribute__((address_space(1)))
; #define LAS __attribute__((address_space(3)))
; #define LDS_WAIT() asm volatile("s_waitcnt lgkmcnt(0)" ::: "memory")
; __device__ __forceinline__ void tr_item8(const float* W, int ld, int K, int nblk, int item, unsigned char* WT, bool gu, float scale, LAS float* scr, int lane) {
;     ...
;       for (int i = 0; i < 32; ++i) scr[(2 * i + (lane >> 5)) * 33 + (lane & 31)] = t_[i] * scale; }
;     LDS_WAIT(); asm volatile("" ::: "memory");
;     const int c = lane & 3;
; #pragma unroll
;     for (int j = 0; j < 2; ++j) { const int n = (lane >> 2) + 16 * j; const LAS float* sp = scr + (16 * c) * 33 + n;
;         v4u o; o.x = pg8::cvt_pk4_fp8(sp[0 * 33], sp[1 * 33], sp[2 * 33], sp[3 * 33]); o.y = pg8::cvt_pk4_fp8(sp[4 * 33], sp[5 * 33], sp[6 * 33], sp[7 * 33]);
;         o.z = pg8::cvt_pk4_fp8(sp[8 * 33], sp[9 * 33], sp[10 * 33], sp[11 * 33]); o.w = pg8::cvt_pk4_fp8(sp[12 * 33], sp[13 * 33], sp[14 * 33], sp[15 * 33]);
;         *(GAS v4u*)(WT + (size_t)(drow0 + n) * K + k0 + 16 * c) = o; }
;     LDS_WAIT(); asm volatile("" ::: "memory");
	v_mul_f32_e32 v47, 0x42800000, v65
	v_mul_f32_e32 v49, 0x42800000, v66
	ds_write2_b32 v29, v47, v49 offset1:66
	v_mul_f32_e32 v47, 0x42800000, v67
	v_mul_f32_e32 v49, 0x42800000, v68
	ds_write2_b32 v29, v47, v49 offset0:132 offset1:198
	v_mul_f32_e32 v47, 0x42800000, v69
	v_mul_f32_e32 v49, 0x42800000, v70
	ds_write2_b32 v38, v47, v49 offset0:8 offset1:74
	v_mul_f32_e32 v47, 0x42800000, v71
	v_mul_f32_e32 v49, 0x42800000, v72
	ds_write2_b32 v38, v47, v49 offset0:140 offset1:206
	s_add_i32 s0, s17, s5
	s_sext_i32_i16 s5, s0
	s_bfe_u32 s5, s5, 0x70018
	s_add_i32 s5, s0, s5
	s_sext_i32_i16 s6, s5
	s_and_b32 s5, s5, 0xff80
	s_sub_i32 s0, s0, s5
	s_lshl_b32 s6, s6, 1
	s_sext_i32_i16 s0, s0
	v_mul_f32_e32 v47, 0x42800000, v73
	v_mul_f32_e32 v49, 0x42800000, v74
	ds_write2_b32 v39, v47, v49 offset0:16 offset1:82
	v_mul_f32_e32 v47, 0x42800000, v75
	v_mul_f32_e32 v49, 0x42800000, v76
	ds_write2_b32 v39, v47, v49 offset0:148 offset1:214
	v_mul_f32_e32 v47, 0x42800000, v77
	v_mul_f32_e32 v49, 0x42800000, v78
	ds_write2_b32 v40, v47, v49 offset0:24 offset1:90
	v_mul_f32_e32 v47, 0x42800000, v79
	v_mul_f32_e32 v49, 0x42800000, v80
	ds_write2_b32 v40, v47, v49 offset0:156 offset1:222
	s_and_b32 s6, s6, 0xffffff00
	s_add_i32 s0, s18, s0
	s_add_i32 s0, s0, s6
	s_mov_b32 s5, s1
	v_mul_f32_e32 v47, 0x42800000, v81
	v_mul_f32_e32 v49, 0x42800000, v82
	ds_write2_b32 v41, v47, v49 offset0:32 offset1:98
	v_mul_f32_e32 v47, 0x42800000, v83
	v_mul_f32_e32 v49, 0x42800000, v84
	ds_write2_b32 v41, v47, v49 offset0:164 offset1:230
	v_mul_f32_e32 v47, 0x42800000, v85
	v_mul_f32_e32 v49, 0x42800000, v86
	ds_write2_b32 v42, v47, v49 offset0:40 offset1:106
	v_mul_f32_e32 v47, 0x42800000, v60
	v_mul_f32_e32 v49, 0x42800000, v61
	ds_write2_b32 v42, v47, v49 offset0:172 offset1:238
	v_add_u32_e32 v84, s0, v30
	v_ashrrev_i32_e32 v85, 31, v84
	v_lshlrev_b64 v[84:85], 10, v[84:85]
	v_mul_f32_e32 v47, 0x42800000, v62
	v_mul_f32_e32 v49, 0x42800000, v50
	ds_write2_b32 v43, v47, v49 offset0:48 offset1:114
	v_mul_f32_e32 v47, 0x42800000, v51
	v_mul_f32_e32 v49, 0x42800000, v52
	ds_write2_b32 v43, v47, v49 offset0:180 offset1:246
	v_mul_f32_e32 v47, 0x42800000, v53
	v_mul_f32_e32 v49, 0x42800000, v54
	ds_write2_b32 v44, v47, v49 offset0:56 offset1:122
	v_mov_b32_e32 v49, 0
	v_lshl_add_u64 v[50:51], v[14:15], 0, s[4:5]
	v_mul_f32_e32 v47, 0x42800000, v48
	v_mul_f32_e32 v46, 0x42800000, v46
	ds_write2_b32 v44, v47, v46 offset0:188 offset1:254
	s_waitcnt lgkmcnt(0)
	ds_read2_b32 v[52:53], v31 offset1:16
	ds_read2_b32 v[54:55], v31 offset0:33 offset1:49
	ds_read2_b32 v[56:57], v31 offset0:66 offset1:82
	ds_read2_b32 v[58:59], v31 offset0:99 offset1:115
	ds_read2_b32 v[60:61], v31 offset0:132 offset1:148
	ds_read2_b32 v[62:63], v31 offset0:165 offset1:181
	ds_read2_b32 v[64:65], v31 offset0:198 offset1:214
	ds_read2_b32 v[66:67], v31 offset0:231 offset1:247
	ds_read2_b32 v[68:69], v45 offset0:8 offset1:24
	ds_read2_b32 v[70:71], v45 offset0:41 offset1:57
	ds_read2_b32 v[72:73], v45 offset0:74 offset1:90
	ds_read2_b32 v[74:75], v45 offset0:107 offset1:123
	ds_read2_b32 v[76:77], v45 offset0:140 offset1:156
	ds_read2_b32 v[78:79], v45 offset0:173 offset1:189
	v_mov_b32_e32 v46, 0
	v_mov_b32_e32 v47, 0
	v_mov_b32_e32 v48, 0
	ds_read2_b32 v[80:81], v45 offset0:206 offset1:222
	ds_read2_b32 v[82:83], v45 offset0:239 offset1:255
	s_waitcnt lgkmcnt(14)
	v_cvt_pk_fp8_f32 v46, v52, v54
	s_waitcnt lgkmcnt(10)
	v_cvt_pk_fp8_f32 v47, v60, v62
	s_waitcnt lgkmcnt(6)
	v_cvt_pk_fp8_f32 v48, v68, v70
	s_waitcnt lgkmcnt(2)
	v_cvt_pk_fp8_f32 v49, v76, v78
	v_cvt_pk_fp8_f32 v46, v56, v58 op_sel:[0,0,1]
	v_cvt_pk_fp8_f32 v47, v64, v66 op_sel:[0,0,1]
	v_cvt_pk_fp8_f32 v48, v72, v74 op_sel:[0,0,1]
	s_waitcnt lgkmcnt(0)
	v_cvt_pk_fp8_f32 v49, v80, v82 op_sel:[0,0,1]
	v_lshl_add_u64 v[84:85], v[50:51], 0, v[84:85]
	v_add_u32_e32 v52, s0, v32
	global_store_dwordx4 v[84:85], v[46:49], off nt
	s_nop 1
	v_mov_b32_e32 v46, 0
	v_mov_b32_e32 v47, 0
	v_mov_b32_e32 v48, 0
	v_mov_b32_e32 v49, 0
	v_cvt_pk_fp8_f32 v46, v53, v55
	v_cvt_pk_fp8_f32 v47, v61, v63
	v_cvt_pk_fp8_f32 v48, v69, v71
	v_cvt_pk_fp8_f32 v49, v77, v79
	v_cvt_pk_fp8_f32 v46, v57, v59 op_sel:[0,0,1]
	v_cvt_pk_fp8_f32 v47, v65, v67 op_sel:[0,0,1]
	v_cvt_pk_fp8_f32 v48, v73, v75 op_sel:[0,0,1]
	v_cvt_pk_fp8_f32 v49, v81, v83 op_sel:[0,0,1]
	v_ashrrev_i32_e32 v53, 31, v52
	v_lshlrev_b64 v[52:53], 10, v[52:53]
	v_lshl_add_u64 v[50:51], v[50:51], 0, v[52:53]
	global_store_dwordx4 v[50:51], v[46:49], off nt
	s_waitcnt lgkmcnt(0)

; #define LAS __attribute__((address_space(3)))
; __device__ __forceinline__ void tr_item(const float* W, int ld, int K, int nblk, int item, bf16* WT, bool gu, LAS float* scr, int lane) {
;     const int kb = item / nblk, nb = item % nblk, k0 = 64 * kb, n0 = 32 * nb;
;     int drow0 = n0;
;     if (gu) { const int bj = n0 / FF, j = n0 - bj * FF; drow0 = 256 * (j / 128) + 128 * bj + (j % 128); }
;     { float t_[32];
; #pragma unroll
;       for (int i = 0; i < 32; ++i) t_[i] = W[(size_t)(k0 + 2 * i + (lane >> 5)) * ld + n0 + (lane & 31)];
; #pragma unroll
;       for (int i = 0; i < 32; ++i) scr[(2 * i + (lane >> 5)) * 33 + (lane & 31)] = t_[i]; }
; __device__ __forceinline__ void convert_items(Frame& F, const Args& a, int lo, int hi, int w, int nw) {
;     ...
;         if (r < I_FO) { tr_item(a.in[9], D, D, 32, r, (bf16*)(F.ws + WS_WFOXOUT), false, scr, lane); continue; } r -= I_FO;
.LBB0_572:
	s_andn2_b64 vcc, exec, s[4:5]
	s_cbranch_vccnz .LBB0_574
	s_add_i32 s0, s10, 0x2000
	s_and_b32 s5, s0, 0x1ffc0
	s_and_b32 s4, s9, 0x3e0
	v_add_u32_e32 v46, s5, v28
	s_lshl_b32 s0, s4, 2
	v_ashrrev_i32_e32 v47, 31, v46
	v_lshl_add_u64 v[48:49], v[4:5], 0, s[0:1]
	v_lshlrev_b64 v[46:47], 12, v[46:47]
	v_lshl_add_u64 v[46:47], v[48:49], 0, v[46:47]
	v_add_co_u32_e32 v48, vcc, 0x2000, v46
	s_lshl_b32 s0, s5, 1
	s_nop 0
	v_addc_co_u32_e32 v49, vcc, 0, v47, vcc
	v_add_co_u32_e32 v50, vcc, 0x4000, v46
	s_nop 1
	v_addc_co_u32_e32 v51, vcc, 0, v47, vcc
	v_add_co_u32_e32 v52, vcc, 0x6000, v46
	s_nop 1
	v_addc_co_u32_e32 v53, vcc, 0, v47, vcc
	v_add_co_u32_e32 v54, vcc, 0x8000, v46
	s_nop 1
	v_addc_co_u32_e32 v55, vcc, 0, v47, vcc
	v_add_co_u32_e32 v56, vcc, 0xa000, v46
	s_nop 1
	v_addc_co_u32_e32 v57, vcc, 0, v47, vcc
	v_add_co_u32_e32 v58, vcc, 0xc000, v46
	s_nop 1
	v_addc_co_u32_e32 v59, vcc, 0, v47, vcc
	v_add_co_u32_e32 v60, vcc, 0xe000, v46
	s_nop 1
	v_addc_co_u32_e32 v61, vcc, 0, v47, vcc
	global_load_dword v64, v[46:47], off nt
	global_load_dword v65, v[48:49], off nt
	global_load_dword v66, v[50:51], off nt
	global_load_dword v67, v[52:53], off nt
	global_load_dword v68, v[54:55], off nt
	global_load_dword v69, v[56:57], off nt
	global_load_dword v70, v[58:59], off nt
	global_load_dword v71, v[60:61], off nt
	v_add_co_u32_e32 v48, vcc, 0x10000, v46
	s_nop 1
	v_addc_co_u32_e32 v49, vcc, 0, v47, vcc
	v_add_co_u32_e32 v50, vcc, 0x12000, v46
	s_nop 1
	v_addc_co_u32_e32 v51, vcc, 0, v47, vcc
	v_add_co_u32_e32 v52, vcc, 0x14000, v46
	s_nop 1
	v_addc_co_u32_e32 v53, vcc, 0, v47, vcc
	v_add_co_u32_e32 v54, vcc, 0x16000, v46
	s_nop 1
	v_addc_co_u32_e32 v55, vcc, 0, v47, vcc
	v_add_co_u32_e32 v56, vcc, 0x18000, v46
	s_nop 1
	v_addc_co_u32_e32 v57, vcc, 0, v47, vcc
	v_add_co_u32_e32 v58, vcc, 0x1a000, v46
	s_nop 1
	v_addc_co_u32_e32 v59, vcc, 0, v47, vcc
	v_add_co_u32_e32 v60, vcc, 0x1c000, v46
	s_nop 1
	v_addc_co_u32_e32 v61, vcc, 0, v47, vcc
	v_add_co_u32_e32 v62, vcc, 0x1e000, v46
	s_nop 1
	v_addc_co_u32_e32 v63, vcc, 0, v47, vcc
	global_load_dword v72, v[48:49], off nt
	global_load_dword v73, v[50:51], off nt
	global_load_dword v74, v[52:53], off nt
	global_load_dword v75, v[54:55], off nt
	global_load_dword v76, v[56:57], off nt
	global_load_dword v77, v[58:59], off nt
	global_load_dword v78, v[60:61], off nt
	global_load_dword v79, v[62:63], off nt
	v_add_co_u32_e32 v48, vcc, 0x20000, v46
	s_nop 1
	v_addc_co_u32_e32 v49, vcc, 0, v47, vcc
	v_add_co_u32_e32 v50, vcc, 0x22000, v46
	s_nop 1
	v_addc_co_u32_e32 v51, vcc, 0, v47, vcc
	v_add_co_u32_e32 v52, vcc, 0x24000, v46
	s_nop 1
	v_addc_co_u32_e32 v53, vcc, 0, v47, vcc
	v_add_co_u32_e32 v54, vcc, 0x26000, v46
	s_nop 1
	v_addc_co_u32_e32 v55, vcc, 0, v47, vcc
	v_add_co_u32_e32 v56, vcc, 0x28000, v46
	s_nop 1
	v_addc_co_u32_e32 v57, vcc, 0, v47, vcc
	v_add_co_u32_e32 v58, vcc, 0x2a000, v46
	s_nop 1
	v_addc_co_u32_e32 v59, vcc, 0, v47, vcc
	v_add_co_u32_e32 v60, vcc, 0x2c000, v46
	s_nop 1
	v_addc_co_u32_e32 v61, vcc, 0, v47, vcc
	v_add_co_u32_e32 v62, vcc, 0x2e000, v46
	s_nop 1
	v_addc_co_u32_e32 v63, vcc, 0, v47, vcc
	global_load_dword v80, v[48:49], off nt
	global_load_dword v81, v[50:51], off nt
	global_load_dword v82, v[52:53], off nt
	global_load_dword v83, v[54:55], off nt
	global_load_dword v84, v[56:57], off nt
	global_load_dword v85, v[58:59], off nt
	global_load_dword v86, v[60:61], off nt
	s_nop 0
	global_load_dword v62, v[62:63], off nt
	v_add_co_u32_e32 v48, vcc, 0x30000, v46
	s_nop 1
	v_addc_co_u32_e32 v49, vcc, 0, v47, vcc
	v_add_co_u32_e32 v50, vcc, 0x32000, v46
	s_nop 1
	v_addc_co_u32_e32 v51, vcc, 0, v47, vcc
	v_add_co_u32_e32 v52, vcc, 0x34000, v46
	s_nop 1
	v_addc_co_u32_e32 v53, vcc, 0, v47, vcc
	v_add_co_u32_e32 v54, vcc, 0x36000, v46
	s_nop 1
	v_addc_co_u32_e32 v55, vcc, 0, v47, vcc
	v_add_co_u32_e32 v56, vcc, 0x38000, v46
	s_nop 1
	v_addc_co_u32_e32 v57, vcc, 0, v47, vcc
	v_add_co_u32_e32 v58, vcc, 0x3a000, v46
	s_nop 1
	v_addc_co_u32_e32 v59, vcc, 0, v47, vcc
	v_add_co_u32_e32 v60, vcc, 0x3c000, v46
	s_nop 1
	v_addc_co_u32_e32 v61, vcc, 0, v47, vcc
	v_add_co_u32_e32 v46, vcc, 0x3e000, v46
	s_nop 1
	v_addc_co_u32_e32 v47, vcc, 0, v47, vcc
	global_load_dword v48, v[48:49], off nt
	s_nop 0
	global_load_dword v49, v[50:51], off nt
	s_nop 0
	global_load_dword v50, v[52:53], off nt
	global_load_dword v51, v[54:55], off nt
	s_nop 0
	global_load_dword v52, v[56:57], off nt
	global_load_dword v53, v[58:59], off nt
	global_load_dword v54, v[60:61], off nt
	s_nop 0
	global_load_dword v46, v[46:47], off nt
	s_waitcnt vmcnt(0)
	ds_write2_b32 v29, v64, v65 offset1:66
	ds_write2_b32 v29, v66, v67 offset0:132 offset1:198
	ds_write2_b32 v38, v68, v69 offset0:8 offset1:74
	ds_write2_b32 v38, v70, v71 offset0:140 offset1:206
	ds_write2_b32 v39, v72, v73 offset0:16 offset1:82
	ds_write2_b32 v39, v74, v75 offset0:148 offset1:214
	ds_write2_b32 v40, v76, v77 offset0:24 offset1:90
	ds_write2_b32 v40, v78, v79 offset0:156 offset1:222
	ds_write2_b32 v41, v80, v81 offset0:32 offset1:98
	ds_write2_b32 v41, v82, v83 offset0:164 offset1:230
	ds_write2_b32 v42, v84, v85 offset0:40 offset1:106
	ds_write2_b32 v42, v86, v62 offset0:172 offset1:238
	ds_write2_b32 v43, v48, v49 offset0:48 offset1:114
	ds_write2_b32 v43, v50, v51 offset0:180 offset1:246
	ds_write2_b32 v44, v52, v53 offset0:56 offset1:122
	ds_write2_b32 v44, v54, v46 offset0:188 offset1:254
	s_waitcnt lgkmcnt(0)
; #define GAS __attribute__((address_space(1)))
; #define LAS __attribute__((address_space(3)))
; #define LDS_WAIT() asm volatile("s_waitcnt lgkmcnt(0)" ::: "memory")
; __device__ __forceinline__ unsigned pk2(float lo, float hi) { return f2bf(lo) | (f2bf(hi) << 16); }
; __device__ __forceinline__ void tr_item(const float* W, int ld, int K, int nblk, int item, bf16* WT, bool gu, LAS float* scr, int lane) {
;     ...
;       for (int i = 0; i < 32; ++i) scr[(2 * i + (lane >> 5)) * 33 + (lane & 31)] = t_[i]; }
;     LDS_WAIT(); asm volatile("" ::: "memory");
;     const int c = lane & 7;
; #pragma unroll
;     for (int j = 0; j < 4; ++j) { const int n = (lane >> 3) + 8 * j; const LAS float* s = scr + (8 * c) * 33 + n;
;         v4u o; o.x = pk2(s[0 * 33], s[1 * 33]); o.y = pk2(s[2 * 33], s[3 * 33]); o.z = pk2(s[4 * 33], s[5 * 33]); o.w = pk2(s[6 * 33], s[7 * 33]);
;         *(GAS v4u*)(WT + (size_t)(drow0 + n) * K + k0 + 8 * c) = o; }
;     LDS_WAIT(); asm volatile("" ::: "memory");
	ds_read2_b32 v[50:51], v34 offset1:8
	ds_read2_b32 v[54:55], v34 offset0:33 offset1:41
	ds_read2_b32 v[56:57], v34 offset0:66 offset1:74
	ds_read2_b32 v[58:59], v34 offset0:99 offset1:107
	ds_read2_b32 v[60:61], v34 offset0:132 offset1:140
	s_waitcnt lgkmcnt(4)
	v_bfe_u32 v46, v50, 16, 1
	v_add3_u32 v46, v50, v46, s13
	s_waitcnt lgkmcnt(3)
	v_bfe_u32 v47, v54, 16, 1
	v_lshrrev_b32_e32 v46, 16, v46
	v_add3_u32 v47, v54, v47, s13
	ds_read2_b32 v[62:63], v34 offset0:165 offset1:173
	v_and_or_b32 v46, v47, s14, v46
	s_waitcnt lgkmcnt(3)
	v_bfe_u32 v47, v56, 16, 1
	v_add3_u32 v47, v56, v47, s13
	s_waitcnt lgkmcnt(2)
	v_bfe_u32 v48, v58, 16, 1
	ds_read2_b32 v[64:65], v34 offset0:198 offset1:206
	v_lshrrev_b32_e32 v47, 16, v47
	v_add3_u32 v48, v58, v48, s13
	ds_read2_b32 v[66:67], v34 offset0:231 offset1:239
	v_and_or_b32 v47, v48, s14, v47
	s_waitcnt lgkmcnt(3)
	v_bfe_u32 v48, v60, 16, 1
	v_add3_u32 v48, v60, v48, s13
	s_waitcnt lgkmcnt(2)
	v_bfe_u32 v49, v62, 16, 1
	v_lshrrev_b32_e32 v48, 16, v48
	v_add3_u32 v49, v62, v49, s13
	v_and_or_b32 v48, v49, s14, v48
	s_waitcnt lgkmcnt(1)
	v_bfe_u32 v49, v64, 16, 1
	v_add_u32_e32 v68, s4, v33
	v_add3_u32 v49, v64, v49, s13
	s_waitcnt lgkmcnt(0)
	v_bfe_u32 v50, v66, 16, 1
	v_ashrrev_i32_e32 v69, 31, v68
	v_lshl_add_u64 v[52:53], v[16:17], 0, s[0:1]
	v_lshrrev_b32_e32 v49, 16, v49
	v_add3_u32 v50, v66, v50, s13
	v_lshlrev_b64 v[68:69], 11, v[68:69]
	v_and_or_b32 v49, v50, s14, v49
	v_lshl_add_u64 v[68:69], v[52:53], 0, v[68:69]
	global_store_dwordx4 v[68:69], v[46:49], off nt
	v_bfe_u32 v50, v67, 16, 1
	v_add3_u32 v50, v67, v50, s13
	v_bfe_u32 v46, v51, 16, 1
	v_add3_u32 v46, v51, v46, s13
	v_bfe_u32 v47, v55, 16, 1
	v_lshrrev_b32_e32 v46, 16, v46
	v_add3_u32 v47, v55, v47, s13
	v_and_or_b32 v46, v47, s14, v46
	v_bfe_u32 v47, v57, 16, 1
	v_add3_u32 v47, v57, v47, s13
	v_bfe_u32 v48, v59, 16, 1
	v_lshrrev_b32_e32 v47, 16, v47
	v_add3_u32 v48, v59, v48, s13
	v_and_or_b32 v47, v48, s14, v47
	v_bfe_u32 v48, v61, 16, 1
	v_add3_u32 v48, v61, v48, s13
	v_bfe_u32 v49, v63, 16, 1
	v_lshrrev_b32_e32 v48, 16, v48
	v_add3_u32 v49, v63, v49, s13
	v_and_or_b32 v48, v49, s14, v48
	v_bfe_u32 v49, v65, 16, 1
	v_add3_u32 v49, v65, v49, s13
	v_lshrrev_b32_e32 v49, 16, v49
	v_and_or_b32 v49, v50, s14, v49
	v_add_u32_e32 v50, s4, v35
	v_ashrrev_i32_e32 v51, 31, v50
	v_lshlrev_b64 v[50:51], 11, v[50:51]
	ds_read2_b32 v[54:55], v34 offset0:16 offset1:24
	v_lshl_add_u64 v[50:51], v[52:53], 0, v[50:51]
	global_store_dwordx4 v[50:51], v[46:49], off nt
	ds_read2_b32 v[50:51], v34 offset0:49 offset1:57
	ds_read2_b32 v[56:57], v34 offset0:82 offset1:90
	ds_read2_b32 v[58:59], v34 offset0:115 offset1:123
	s_waitcnt lgkmcnt(3)
	v_bfe_u32 v46, v54, 16, 1
	v_add3_u32 v46, v54, v46, s13
	s_waitcnt lgkmcnt(2)
	v_bfe_u32 v47, v50, 16, 1
	ds_read2_b32 v[60:61], v34 offset0:148 offset1:156
	v_lshrrev_b32_e32 v46, 16, v46
	v_add3_u32 v47, v50, v47, s13
	ds_read2_b32 v[62:63], v34 offset0:181 offset1:189
	v_and_or_b32 v46, v47, s14, v46
	s_waitcnt lgkmcnt(3)
	v_bfe_u32 v47, v56, 16, 1
	v_add3_u32 v47, v56, v47, s13
	s_waitcnt lgkmcnt(2)
	v_bfe_u32 v48, v58, 16, 1
	ds_read2_b32 v[64:65], v34 offset0:214 offset1:222
	v_lshrrev_b32_e32 v47, 16, v47
	v_add3_u32 v48, v58, v48, s13
	ds_read2_b32 v[66:67], v34 offset0:247 offset1:255
	v_and_or_b32 v47, v48, s14, v47
	s_waitcnt lgkmcnt(3)
	v_bfe_u32 v48, v60, 16, 1
	v_add3_u32 v48, v60, v48, s13
	s_waitcnt lgkmcnt(2)
	v_bfe_u32 v49, v62, 16, 1
	v_lshrrev_b32_e32 v48, 16, v48
	v_add3_u32 v49, v62, v49, s13
	v_and_or_b32 v48, v49, s14, v48
	s_waitcnt lgkmcnt(1)
	v_bfe_u32 v49, v64, 16, 1
	v_add_u32_e32 v68, s4, v36
	v_add3_u32 v49, v64, v49, s13
	s_waitcnt lgkmcnt(0)
	v_bfe_u32 v50, v66, 16, 1
	v_ashrrev_i32_e32 v69, 31, v68
	v_lshrrev_b32_e32 v49, 16, v49
	v_add3_u32 v50, v66, v50, s13
	v_lshlrev_b64 v[68:69], 11, v[68:69]
	v_and_or_b32 v49, v50, s14, v49
	v_lshl_add_u64 v[68:69], v[52:53], 0, v[68:69]
	global_store_dwordx4 v[68:69], v[46:49], off nt
	v_bfe_u32 v50, v67, 16, 1
	v_add3_u32 v50, v67, v50, s13
	v_bfe_u32 v46, v55, 16, 1
	v_add3_u32 v46, v55, v46, s13
	v_bfe_u32 v47, v51, 16, 1
	v_lshrrev_b32_e32 v46, 16, v46
	v_add3_u32 v47, v51, v47, s13
	v_and_or_b32 v46, v47, s14, v46
	v_bfe_u32 v47, v57, 16, 1
	v_add3_u32 v47, v57, v47, s13
	v_bfe_u32 v48, v59, 16, 1
	v_lshrrev_b32_e32 v47, 16, v47
	v_add3_u32 v48, v59, v48, s13
	v_and_or_b32 v47, v48, s14, v47
	v_bfe_u32 v48, v61, 16, 1
	v_add3_u32 v48, v61, v48, s13
	v_bfe_u32 v49, v63, 16, 1
	v_lshrrev_b32_e32 v48, 16, v48
	v_add3_u32 v49, v63, v49, s13
	v_and_or_b32 v48, v49, s14, v48
	v_bfe_u32 v49, v65, 16, 1
	v_add3_u32 v49, v65, v49, s13
	v_lshrrev_b32_e32 v49, 16, v49
	v_and_or_b32 v49, v50, s14, v49
	v_add_u32_e32 v50, s4, v37
	v_ashrrev_i32_e32 v51, 31, v50
	v_lshlrev_b64 v[50:51], 11, v[50:51]
	v_lshl_add_u64 v[50:51], v[52:53], 0, v[50:51]
	global_store_dwordx4 v[50:51], v[46:49], off nt
	s_waitcnt lgkmcnt(0)

; #define LAS __attribute__((address_space(3)))
; __device__ __forceinline__ void tr_item(const float* W, int ld, int K, int nblk, int item, bf16* WT, bool gu, LAS float* scr, int lane) {
;     const int kb = item / nblk, nb = item % nblk, k0 = 64 * kb, n0 = 32 * nb;
;     int drow0 = n0;
;     if (gu) { const int bj = n0 / FF, j = n0 - bj * FF; drow0 = 256 * (j / 128) + 128 * bj + (j % 128); }
;     { float t_[32];
; #pragma unroll
;       for (int i = 0; i < 32; ++i) t_[i] = W[(size_t)(k0 + 2 * i + (lane >> 5)) * ld + n0 + (lane & 31)];
; #pragma unroll
;       for (int i = 0; i < 32; ++i) scr[(2 * i + (lane >> 5)) * 33 + (lane & 31)] = t_[i]; }
; __device__ __forceinline__ void convert_items(Frame& F, const Args& a, int lo, int hi, int w, int nw) {
;     ...
;         if (r < I_SI) { tr_item(a.in[10], D + 512, D, 48, r, (bf16*)(F.ws + WS_WSWAIN), false, scr, lane); continue; } r -= I_SI;
.LBB0_575:
	s_andn2_b64 vcc, exec, s[4:5]
	s_cbranch_vccnz .LBB0_577
	s_add_i32 s0, s3, 0xf800
	s_and_b32 s4, s0, 0xffff
	s_mul_i32 s4, s4, 0xaaab
	s_lshr_b32 s5, s4, 21
	s_mul_i32 s4, s5, 48
	s_sub_i32 s0, s0, s4
	s_lshl_b32 s0, s0, 5
	s_and_b32 s4, s0, 0xffe0
	v_lshl_add_u32 v64, s5, 6, v28
	s_lshl_b32 s0, s4, 2
	v_lshl_add_u64 v[46:47], v[6:7], 0, s[0:1]
	v_add_u32_e32 v50, 2, v64
	v_add_u32_e32 v52, 4, v64
	v_add_u32_e32 v54, 6, v64
	v_add_u32_e32 v56, 8, v64
	v_add_u32_e32 v58, 10, v64
	v_add_u32_e32 v60, 12, v64
	v_add_u32_e32 v62, 14, v64
	v_mad_i64_i32 v[48:49], s[6:7], v64, s15, v[46:47]
	v_mad_i64_i32 v[50:51], s[6:7], v50, s15, v[46:47]
	v_mad_i64_i32 v[52:53], s[6:7], v52, s15, v[46:47]
	v_mad_i64_i32 v[54:55], s[6:7], v54, s15, v[46:47]
	v_mad_i64_i32 v[56:57], s[6:7], v56, s15, v[46:47]
	v_mad_i64_i32 v[58:59], s[6:7], v58, s15, v[46:47]
	v_mad_i64_i32 v[60:61], s[6:7], v60, s15, v[46:47]
	v_mad_i64_i32 v[62:63], s[6:7], v62, s15, v[46:47]
	global_load_dword v65, v[48:49], off nt
	global_load_dword v66, v[50:51], off nt
	global_load_dword v67, v[52:53], off nt
	global_load_dword v68, v[54:55], off nt
	global_load_dword v69, v[56:57], off nt
	global_load_dword v70, v[58:59], off nt
	global_load_dword v71, v[60:61], off nt
	global_load_dword v72, v[62:63], off nt
	v_add_u32_e32 v48, 16, v64
	v_add_u32_e32 v50, 18, v64
	v_add_u32_e32 v52, 20, v64
	v_add_u32_e32 v54, 22, v64
	v_add_u32_e32 v56, 24, v64
	v_add_u32_e32 v58, 26, v64
	v_add_u32_e32 v60, 28, v64
	v_add_u32_e32 v62, 30, v64
	v_mad_i64_i32 v[48:49], s[6:7], v48, s15, v[46:47]
	v_mad_i64_i32 v[50:51], s[6:7], v50, s15, v[46:47]
	v_mad_i64_i32 v[52:53], s[6:7], v52, s15, v[46:47]
	v_mad_i64_i32 v[54:55], s[6:7], v54, s15, v[46:47]
	v_mad_i64_i32 v[56:57], s[6:7], v56, s15, v[46:47]
	v_mad_i64_i32 v[58:59], s[6:7], v58, s15, v[46:47]
	v_mad_i64_i32 v[60:61], s[6:7], v60, s15, v[46:47]
	v_mad_i64_i32 v[62:63], s[6:7], v62, s15, v[46:47]
	global_load_dword v73, v[48:49], off nt
	global_load_dword v74, v[50:51], off nt
	global_load_dword v75, v[52:53], off nt
	global_load_dword v76, v[54:55], off nt
	global_load_dword v77, v[56:57], off nt
	global_load_dword v78, v[58:59], off nt
	global_load_dword v79, v[60:61], off nt
	global_load_dword v80, v[62:63], off nt
	v_add_u32_e32 v48, 32, v64
	v_add_u32_e32 v50, 34, v64
	v_add_u32_e32 v52, 36, v64
	v_add_u32_e32 v54, 38, v64
	v_add_u32_e32 v56, 40, v64
	v_add_u32_e32 v58, 42, v64
	v_add_u32_e32 v60, 44, v64
	v_add_u32_e32 v62, 46, v64
	v_mad_i64_i32 v[48:49], s[6:7], v48, s15, v[46:47]
	v_mad_i64_i32 v[50:51], s[6:7], v50, s15, v[46:47]
	v_mad_i64_i32 v[52:53], s[6:7], v52, s15, v[46:47]
	v_mad_i64_i32 v[54:55], s[6:7], v54, s15, v[46:47]
	v_mad_i64_i32 v[56:57], s[6:7], v56, s15, v[46:47]
	v_mad_i64_i32 v[58:59], s[6:7], v58, s15, v[46:47]
	v_mad_i64_i32 v[60:61], s[6:7], v60, s15, v[46:47]
	v_mad_i64_i32 v[62:63], s[6:7], v62, s15, v[46:47]
	global_load_dword v81, v[48:49], off nt
	global_load_dword v82, v[50:51], off nt
	global_load_dword v83, v[52:53], off nt
	global_load_dword v84, v[54:55], off nt
	global_load_dword v85, v[56:57], off nt
	global_load_dword v86, v[58:59], off nt
	global_load_dword v87, v[60:61], off nt
	s_nop 0
	global_load_dword v62, v[62:63], off nt
	v_add_u32_e32 v48, 48, v64
	v_add_u32_e32 v50, 50, v64
	v_add_u32_e32 v52, 52, v64
	v_add_u32_e32 v54, 54, v64
	v_add_u32_e32 v56, 56, v64
	v_add_u32_e32 v58, 58, v64
	v_add_u32_e32 v60, 60, v64
	v_add_u32_e32 v63, 62, v64
	v_mad_i64_i32 v[48:49], s[6:7], v48, s15, v[46:47]
	v_mad_i64_i32 v[50:51], s[6:7], v50, s15, v[46:47]
	v_mad_i64_i32 v[52:53], s[6:7], v52, s15, v[46:47]
	v_mad_i64_i32 v[54:55], s[6:7], v54, s15, v[46:47]
	v_mad_i64_i32 v[56:57], s[6:7], v56, s15, v[46:47]
	v_mad_i64_i32 v[58:59], s[6:7], v58, s15, v[46:47]
	v_mad_i64_i32 v[60:61], s[6:7], v60, s15, v[46:47]
	v_mad_i64_i32 v[46:47], s[6:7], v63, s15, v[46:47]
	global_load_dword v48, v[48:49], off nt
	s_nop 0
	global_load_dword v49, v[50:51], off nt
	s_nop 0
	global_load_dword v50, v[52:53], off nt
	global_load_dword v51, v[54:55], off nt
	s_nop 0
	global_load_dword v52, v[56:57], off nt
	global_load_dword v53, v[58:59], off nt
	global_load_dword v54, v[60:61], off nt
	s_nop 0
	global_load_dword v46, v[46:47], off nt
	s_waitcnt vmcnt(0)
	ds_write2_b32 v29, v65, v66 offset1:66
	ds_write2_b32 v29, v67, v68 offset0:132 offset1:198
	ds_write2_b32 v38, v69, v70 offset0:8 offset1:74
	ds_write2_b32 v38, v71, v72 offset0:140 offset1:206
	ds_write2_b32 v39, v73, v74 offset0:16 offset1:82
	ds_write2_b32 v39, v75, v76 offset0:148 offset1:214
	ds_write2_b32 v40, v77, v78 offset0:24 offset1:90
	ds_write2_b32 v40, v79, v80 offset0:156 offset1:222
	ds_write2_b32 v41, v81, v82 offset0:32 offset1:98
	ds_write2_b32 v41, v83, v84 offset0:164 offset1:230
	ds_write2_b32 v42, v85, v86 offset0:40 offset1:106
	ds_write2_b32 v42, v87, v62 offset0:172 offset1:238
	ds_write2_b32 v43, v48, v49 offset0:48 offset1:114
	ds_write2_b32 v43, v50, v51 offset0:180 offset1:246
	ds_write2_b32 v44, v52, v53 offset0:56 offset1:122
	ds_write2_b32 v44, v54, v46 offset0:188 offset1:254
	s_waitcnt lgkmcnt(0)
; #define GAS __attribute__((address_space(1)))
; #define LAS __attribute__((address_space(3)))
; #define LDS_WAIT() asm volatile("s_waitcnt lgkmcnt(0)" ::: "memory")
; __device__ __forceinline__ unsigned pk2(float lo, float hi) { return f2bf(lo) | (f2bf(hi) << 16); }
; __device__ __forceinline__ void tr_item(const float* W, int ld, int K, int nblk, int item, bf16* WT, bool gu, LAS float* scr, int lane) {
;     ...
;       for (int i = 0; i < 32; ++i) scr[(2 * i + (lane >> 5)) * 33 + (lane & 31)] = t_[i]; }
;     LDS_WAIT(); asm volatile("" ::: "memory");
;     const int c = lane & 7;
; #pragma unroll
;     for (int j = 0; j < 4; ++j) { const int n = (lane >> 3) + 8 * j; const LAS float* s = scr + (8 * c) * 33 + n;
;         v4u o; o.x = pk2(s[0 * 33], s[1 * 33]); o.y = pk2(s[2 * 33], s[3 * 33]); o.z = pk2(s[4 * 33], s[5 * 33]); o.w = pk2(s[6 * 33], s[7 * 33]);
;         *(GAS v4u*)(WT + (size_t)(drow0 + n) * K + k0 + 8 * c) = o; }
;     LDS_WAIT(); asm volatile("" ::: "memory");
	ds_read2_b32 v[50:51], v34 offset1:8
	ds_read2_b32 v[54:55], v34 offset0:33 offset1:41
	ds_read2_b32 v[56:57], v34 offset0:66 offset1:74
	ds_read2_b32 v[58:59], v34 offset0:99 offset1:107
	ds_read2_b32 v[60:61], v34 offset0:132 offset1:140
	s_waitcnt lgkmcnt(4)
	v_bfe_u32 v46, v50, 16, 1
	v_add3_u32 v46, v50, v46, s13
	s_waitcnt lgkmcnt(3)
	v_bfe_u32 v47, v54, 16, 1
	v_lshrrev_b32_e32 v46, 16, v46
	v_add3_u32 v47, v54, v47, s13
	ds_read2_b32 v[62:63], v34 offset0:165 offset1:173
	v_and_or_b32 v46, v47, s14, v46
	s_waitcnt lgkmcnt(3)
	v_bfe_u32 v47, v56, 16, 1
	v_add3_u32 v47, v56, v47, s13
	s_waitcnt lgkmcnt(2)
	v_bfe_u32 v48, v58, 16, 1
	ds_read2_b32 v[64:65], v34 offset0:198 offset1:206
	v_lshrrev_b32_e32 v47, 16, v47
	v_add3_u32 v48, v58, v48, s13
	ds_read2_b32 v[66:67], v34 offset0:231 offset1:239
	v_and_or_b32 v47, v48, s14, v47
	s_waitcnt lgkmcnt(3)
	v_bfe_u32 v48, v60, 16, 1
	v_add3_u32 v48, v60, v48, s13
	s_waitcnt lgkmcnt(2)
	v_bfe_u32 v49, v62, 16, 1
	v_lshrrev_b32_e32 v48, 16, v48
	v_add3_u32 v49, v62, v49, s13
	v_and_or_b32 v48, v49, s14, v48
	s_waitcnt lgkmcnt(1)
	v_bfe_u32 v49, v64, 16, 1
	v_add_u32_e32 v68, s4, v33
	s_lshl_b32 s0, s5, 7
	v_add3_u32 v49, v64, v49, s13
	s_waitcnt lgkmcnt(0)
	v_bfe_u32 v50, v66, 16, 1
	v_ashrrev_i32_e32 v69, 31, v68
	v_lshl_add_u64 v[52:53], v[18:19], 0, s[0:1]
	v_lshrrev_b32_e32 v49, 16, v49
	v_add3_u32 v50, v66, v50, s13
	v_lshlrev_b64 v[68:69], 11, v[68:69]
	v_and_or_b32 v49, v50, s14, v49
	v_lshl_add_u64 v[68:69], v[52:53], 0, v[68:69]
	global_store_dwordx4 v[68:69], v[46:49], off nt
	v_bfe_u32 v50, v67, 16, 1
	v_add3_u32 v50, v67, v50, s13
	v_bfe_u32 v46, v51, 16, 1
	v_add3_u32 v46, v51, v46, s13
	v_bfe_u32 v47, v55, 16, 1
	v_lshrrev_b32_e32 v46, 16, v46
	v_add3_u32 v47, v55, v47, s13
	v_and_or_b32 v46, v47, s14, v46
	v_bfe_u32 v47, v57, 16, 1
	v_add3_u32 v47, v57, v47, s13
	v_bfe_u32 v48, v59, 16, 1
	v_lshrrev_b32_e32 v47, 16, v47
	v_add3_u32 v48, v59, v48, s13
	v_and_or_b32 v47, v48, s14, v47
	v_bfe_u32 v48, v61, 16, 1
	v_add3_u32 v48, v61, v48, s13
	v_bfe_u32 v49, v63, 16, 1
	v_lshrrev_b32_e32 v48, 16, v48
	v_add3_u32 v49, v63, v49, s13
	v_and_or_b32 v48, v49, s14, v48
	v_bfe_u32 v49, v65, 16, 1
	v_add3_u32 v49, v65, v49, s13
	v_lshrrev_b32_e32 v49, 16, v49
	v_and_or_b32 v49, v50, s14, v49
	v_add_u32_e32 v50, s4, v35
	v_ashrrev_i32_e32 v51, 31, v50
	v_lshlrev_b64 v[50:51], 11, v[50:51]
	ds_read2_b32 v[54:55], v34 offset0:16 offset1:24
	v_lshl_add_u64 v[50:51], v[52:53], 0, v[50:51]
	global_store_dwordx4 v[50:51], v[46:49], off nt
	ds_read2_b32 v[50:51], v34 offset0:49 offset1:57
	ds_read2_b32 v[56:57], v34 offset0:82 offset1:90
	ds_read2_b32 v[58:59], v34 offset0:115 offset1:123
	s_waitcnt lgkmcnt(3)
	v_bfe_u32 v46, v54, 16, 1
	v_add3_u32 v46, v54, v46, s13
	s_waitcnt lgkmcnt(2)
	v_bfe_u32 v47, v50, 16, 1
	ds_read2_b32 v[60:61], v34 offset0:148 offset1:156
	v_lshrrev_b32_e32 v46, 16, v46
	v_add3_u32 v47, v50, v47, s13
	ds_read2_b32 v[62:63], v34 offset0:181 offset1:189
	v_and_or_b32 v46, v47, s14, v46
	s_waitcnt lgkmcnt(3)
	v_bfe_u32 v47, v56, 16, 1
	v_add3_u32 v47, v56, v47, s13
	s_waitcnt lgkmcnt(2)
	v_bfe_u32 v48, v58, 16, 1
	ds_read2_b32 v[64:65], v34 offset0:214 offset1:222
	v_lshrrev_b32_e32 v47, 16, v47
	v_add3_u32 v48, v58, v48, s13
	ds_read2_b32 v[66:67], v34 offset0:247 offset1:255
	v_and_or_b32 v47, v48, s14, v47
	s_waitcnt lgkmcnt(3)
	v_bfe_u32 v48, v60, 16, 1
	v_add3_u32 v48, v60, v48, s13
	s_waitcnt lgkmcnt(2)
	v_bfe_u32 v49, v62, 16, 1
	v_lshrrev_b32_e32 v48, 16, v48
	v_add3_u32 v49, v62, v49, s13
	v_and_or_b32 v48, v49, s14, v48
	s_waitcnt lgkmcnt(1)
	v_bfe_u32 v49, v64, 16, 1
	v_add_u32_e32 v68, s4, v36
	v_add3_u32 v49, v64, v49, s13
	s_waitcnt lgkmcnt(0)
	v_bfe_u32 v50, v66, 16, 1
	v_ashrrev_i32_e32 v69, 31, v68
	v_lshrrev_b32_e32 v49, 16, v49
	v_add3_u32 v50, v66, v50, s13
	v_lshlrev_b64 v[68:69], 11, v[68:69]
	v_and_or_b32 v49, v50, s14, v49
	v_lshl_add_u64 v[68:69], v[52:53], 0, v[68:69]
	global_store_dwordx4 v[68:69], v[46:49], off nt
	v_bfe_u32 v50, v67, 16, 1
	v_add3_u32 v50, v67, v50, s13
	v_bfe_u32 v46, v55, 16, 1
	v_add3_u32 v46, v55, v46, s13
	v_bfe_u32 v47, v51, 16, 1
	v_lshrrev_b32_e32 v46, 16, v46
	v_add3_u32 v47, v51, v47, s13
	v_and_or_b32 v46, v47, s14, v46
	v_bfe_u32 v47, v57, 16, 1
	v_add3_u32 v47, v57, v47, s13
	v_bfe_u32 v48, v59, 16, 1
	v_lshrrev_b32_e32 v47, 16, v47
	v_add3_u32 v48, v59, v48, s13
	v_and_or_b32 v47, v48, s14, v47
	v_bfe_u32 v48, v61, 16, 1
	v_add3_u32 v48, v61, v48, s13
	v_bfe_u32 v49, v63, 16, 1
	v_lshrrev_b32_e32 v48, 16, v48
	v_add3_u32 v49, v63, v49, s13
	v_and_or_b32 v48, v49, s14, v48
	v_bfe_u32 v49, v65, 16, 1
	v_add3_u32 v49, v65, v49, s13
	v_lshrrev_b32_e32 v49, 16, v49
	v_and_or_b32 v49, v50, s14, v49
	v_add_u32_e32 v50, s4, v37
	v_ashrrev_i32_e32 v51, 31, v50
	v_lshlrev_b64 v[50:51], 11, v[50:51]
	v_lshl_add_u64 v[50:51], v[52:53], 0, v[50:51]
	global_store_dwordx4 v[50:51], v[46:49], off nt
	s_waitcnt lgkmcnt(0)

; #define LAS __attribute__((address_space(3)))
; __device__ __forceinline__ void tr_item(const float* W, int ld, int K, int nblk, int item, bf16* WT, bool gu, LAS float* scr, int lane) {
;     const int kb = item / nblk, nb = item % nblk, k0 = 64 * kb, n0 = 32 * nb;
;     int drow0 = n0;
;     if (gu) { const int bj = n0 / FF, j = n0 - bj * FF; drow0 = 256 * (j / 128) + 128 * bj + (j % 128); }
;     { float t_[32];
; #pragma unroll
;       for (int i = 0; i < 32; ++i) t_[i] = W[(size_t)(k0 + 2 * i + (lane >> 5)) * ld + n0 + (lane & 31)];
; #pragma unroll
;       for (int i = 0; i < 32; ++i) scr[(2 * i + (lane >> 5)) * 33 + (lane & 31)] = t_[i]; }
; __device__ __forceinline__ void convert_items(Frame& F, const Args& a, int lo, int hi, int w, int nw) {
;     ...
;         if (r < I_SO) { tr_item(a.in[12], D, D, 32, r, (bf16*)(F.ws + WS_WSWAOUT), false, scr, lane); continue; } r -= I_SO;
.LBB0_578:
	s_andn2_b64 vcc, exec, s[4:5]
	s_cbranch_vccnz .LBB0_580
	s_add_i32 s0, s10, 0x2a00
	s_and_b32 s5, s0, 0x1ffc0
	s_and_b32 s4, s9, 0x3e0
	v_add_u32_e32 v46, s5, v28
	s_lshl_b32 s0, s4, 2
	v_ashrrev_i32_e32 v47, 31, v46
	v_lshl_add_u64 v[48:49], v[8:9], 0, s[0:1]
	v_lshlrev_b64 v[46:47], 12, v[46:47]
	v_lshl_add_u64 v[46:47], v[48:49], 0, v[46:47]
	v_add_co_u32_e32 v48, vcc, 0x2000, v46
	s_lshl_b32 s0, s5, 1
	s_nop 0
	v_addc_co_u32_e32 v49, vcc, 0, v47, vcc
	v_add_co_u32_e32 v50, vcc, 0x4000, v46
	s_nop 1
	v_addc_co_u32_e32 v51, vcc, 0, v47, vcc
	v_add_co_u32_e32 v52, vcc, 0x6000, v46
	s_nop 1
	v_addc_co_u32_e32 v53, vcc, 0, v47, vcc
	v_add_co_u32_e32 v54, vcc, 0x8000, v46
	s_nop 1
	v_addc_co_u32_e32 v55, vcc, 0, v47, vcc
	v_add_co_u32_e32 v56, vcc, 0xa000, v46
	s_nop 1
	v_addc_co_u32_e32 v57, vcc, 0, v47, vcc
	v_add_co_u32_e32 v58, vcc, 0xc000, v46
	s_nop 1
	v_addc_co_u32_e32 v59, vcc, 0, v47, vcc
	v_add_co_u32_e32 v60, vcc, 0xe000, v46
	s_nop 1
	v_addc_co_u32_e32 v61, vcc, 0, v47, vcc
	global_load_dword v64, v[46:47], off nt
	global_load_dword v65, v[48:49], off nt
	global_load_dword v66, v[50:51], off nt
	global_load_dword v67, v[52:53], off nt
	global_load_dword v68, v[54:55], off nt
	global_load_dword v69, v[56:57], off nt
	global_load_dword v70, v[58:59], off nt
	global_load_dword v71, v[60:61], off nt
	v_add_co_u32_e32 v48, vcc, 0x10000, v46
	s_nop 1
	v_addc_co_u32_e32 v49, vcc, 0, v47, vcc
	v_add_co_u32_e32 v50, vcc, 0x12000, v46
	s_nop 1
	v_addc_co_u32_e32 v51, vcc, 0, v47, vcc
	v_add_co_u32_e32 v52, vcc, 0x14000, v46
	s_nop 1
	v_addc_co_u32_e32 v53, vcc, 0, v47, vcc
	v_add_co_u32_e32 v54, vcc, 0x16000, v46
	s_nop 1
	v_addc_co_u32_e32 v55, vcc, 0, v47, vcc
	v_add_co_u32_e32 v56, vcc, 0x18000, v46
	s_nop 1
	v_addc_co_u32_e32 v57, vcc, 0, v47, vcc
	v_add_co_u32_e32 v58, vcc, 0x1a000, v46
	s_nop 1
	v_addc_co_u32_e32 v59, vcc, 0, v47, vcc
	v_add_co_u32_e32 v60, vcc, 0x1c000, v46
	s_nop 1
	v_addc_co_u32_e32 v61, vcc, 0, v47, vcc
	v_add_co_u32_e32 v62, vcc, 0x1e000, v46
	s_nop 1
	v_addc_co_u32_e32 v63, vcc, 0, v47, vcc
	global_load_dword v72, v[48:49], off nt
	global_load_dword v73, v[50:51], off nt
	global_load_dword v74, v[52:53], off nt
	global_load_dword v75, v[54:55], off nt
	global_load_dword v76, v[56:57], off nt
	global_load_dword v77, v[58:59], off nt
	global_load_dword v78, v[60:61], off nt
	global_load_dword v79, v[62:63], off nt
	v_add_co_u32_e32 v48, vcc, 0x20000, v46
	s_nop 1
	v_addc_co_u32_e32 v49, vcc, 0, v47, vcc
	v_add_co_u32_e32 v50, vcc, 0x22000, v46
	s_nop 1
	v_addc_co_u32_e32 v51, vcc, 0, v47, vcc
	v_add_co_u32_e32 v52, vcc, 0x24000, v46
	s_nop 1
	v_addc_co_u32_e32 v53, vcc, 0, v47, vcc
	v_add_co_u32_e32 v54, vcc, 0x26000, v46
	s_nop 1
	v_addc_co_u32_e32 v55, vcc, 0, v47, vcc
	v_add_co_u32_e32 v56, vcc, 0x28000, v46
	s_nop 1
	v_addc_co_u32_e32 v57, vcc, 0, v47, vcc
	v_add_co_u32_e32 v58, vcc, 0x2a000, v46
	s_nop 1
	v_addc_co_u32_e32 v59, vcc, 0, v47, vcc
	v_add_co_u32_e32 v60, vcc, 0x2c000, v46
	s_nop 1
	v_addc_co_u32_e32 v61, vcc, 0, v47, vcc
	v_add_co_u32_e32 v62, vcc, 0x2e000, v46
	s_nop 1
	v_addc_co_u32_e32 v63, vcc, 0, v47, vcc
	global_load_dword v80, v[48:49], off nt
	global_load_dword v81, v[50:51], off nt
	global_load_dword v82, v[52:53], off nt
	global_load_dword v83, v[54:55], off nt
	global_load_dword v84, v[56:57], off nt
	global_load_dword v85, v[58:59], off nt
	global_load_dword v86, v[60:61], off nt
	s_nop 0
	global_load_dword v62, v[62:63], off nt
	v_add_co_u32_e32 v48, vcc, 0x30000, v46
	s_nop 1
	v_addc_co_u32_e32 v49, vcc, 0, v47, vcc
	v_add_co_u32_e32 v50, vcc, 0x32000, v46
	s_nop 1
	v_addc_co_u32_e32 v51, vcc, 0, v47, vcc
	v_add_co_u32_e32 v52, vcc, 0x34000, v46
	s_nop 1
	v_addc_co_u32_e32 v53, vcc, 0, v47, vcc
	v_add_co_u32_e32 v54, vcc, 0x36000, v46
	s_nop 1
	v_addc_co_u32_e32 v55, vcc, 0, v47, vcc
	v_add_co_u32_e32 v56, vcc, 0x38000, v46
	s_nop 1
	v_addc_co_u32_e32 v57, vcc, 0, v47, vcc
	v_add_co_u32_e32 v58, vcc, 0x3a000, v46
	s_nop 1
	v_addc_co_u32_e32 v59, vcc, 0, v47, vcc
	v_add_co_u32_e32 v60, vcc, 0x3c000, v46
	s_nop 1
	v_addc_co_u32_e32 v61, vcc, 0, v47, vcc
	v_add_co_u32_e32 v46, vcc, 0x3e000, v46
	s_nop 1
	v_addc_co_u32_e32 v47, vcc, 0, v47, vcc
	global_load_dword v48, v[48:49], off nt
	s_nop 0
	global_load_dword v49, v[50:51], off nt
	s_nop 0
	global_load_dword v50, v[52:53], off nt
	global_load_dword v51, v[54:55], off nt
	s_nop 0
	global_load_dword v52, v[56:57], off nt
	global_load_dword v53, v[58:59], off nt
	global_load_dword v54, v[60:61], off nt
	s_nop 0
	global_load_dword v46, v[46:47], off nt
	s_waitcnt vmcnt(0)
	ds_write2_b32 v29, v64, v65 offset1:66
	ds_write2_b32 v29, v66, v67 offset0:132 offset1:198
	ds_write2_b32 v38, v68, v69 offset0:8 offset1:74
	ds_write2_b32 v38, v70, v71 offset0:140 offset1:206
	ds_write2_b32 v39, v72, v73 offset0:16 offset1:82
	ds_write2_b32 v39, v74, v75 offset0:148 offset1:214
	ds_write2_b32 v40, v76, v77 offset0:24 offset1:90
	ds_write2_b32 v40, v78, v79 offset0:156 offset1:222
	ds_write2_b32 v41, v80, v81 offset0:32 offset1:98
	ds_write2_b32 v41, v82, v83 offset0:164 offset1:230
	ds_write2_b32 v42, v84, v85 offset0:40 offset1:106
	ds_write2_b32 v42, v86, v62 offset0:172 offset1:238
	ds_write2_b32 v43, v48, v49 offset0:48 offset1:114
	ds_write2_b32 v43, v50, v51 offset0:180 offset1:246
	ds_write2_b32 v44, v52, v53 offset0:56 offset1:122
	ds_write2_b32 v44, v54, v46 offset0:188 offset1:254
	s_waitcnt lgkmcnt(0)
; #define GAS __attribute__((address_space(1)))
; #define LAS __attribute__((address_space(3)))
; #define LDS_WAIT() asm volatile("s_waitcnt lgkmcnt(0)" ::: "memory")
; __device__ __forceinline__ unsigned pk2(float lo, float hi) { return f2bf(lo) | (f2bf(hi) << 16); }
; __device__ __forceinline__ void tr_item(const float* W, int ld, int K, int nblk, int item, bf16* WT, bool gu, LAS float* scr, int lane) {
;     ...
;       for (int i = 0; i < 32; ++i) scr[(2 * i + (lane >> 5)) * 33 + (lane & 31)] = t_[i]; }
;     LDS_WAIT(); asm volatile("" ::: "memory");
;     const int c = lane & 7;
; #pragma unroll
;     for (int j = 0; j < 4; ++j) { const int n = (lane >> 3) + 8 * j; const LAS float* s = scr + (8 * c) * 33 + n;
;         v4u o; o.x = pk2(s[0 * 33], s[1 * 33]); o.y = pk2(s[2 * 33], s[3 * 33]); o.z = pk2(s[4 * 33], s[5 * 33]); o.w = pk2(s[6 * 33], s[7 * 33]);
;         *(GAS v4u*)(WT + (size_t)(drow0 + n) * K + k0 + 8 * c) = o; }
;     LDS_WAIT(); asm volatile("" ::: "memory");
	ds_read2_b32 v[50:51], v34 offset1:8
	ds_read2_b32 v[54:55], v34 offset0:33 offset1:41
	ds_read2_b32 v[56:57], v34 offset0:66 offset1:74
	ds_read2_b32 v[58:59], v34 offset0:99 offset1:107
	ds_read2_b32 v[60:61], v34 offset0:132 offset1:140
	s_waitcnt lgkmcnt(4)
	v_bfe_u32 v46, v50, 16, 1
	v_add3_u32 v46, v50, v46, s13
	s_waitcnt lgkmcnt(3)
	v_bfe_u32 v47, v54, 16, 1
	v_lshrrev_b32_e32 v46, 16, v46
	v_add3_u32 v47, v54, v47, s13
	ds_read2_b32 v[62:63], v34 offset0:165 offset1:173
	v_and_or_b32 v46, v47, s14, v46
	s_waitcnt lgkmcnt(3)
	v_bfe_u32 v47, v56, 16, 1
	v_add3_u32 v47, v56, v47, s13
	s_waitcnt lgkmcnt(2)
	v_bfe_u32 v48, v58, 16, 1
	ds_read2_b32 v[64:65], v34 offset0:198 offset1:206
	v_lshrrev_b32_e32 v47, 16, v47
	v_add3_u32 v48, v58, v48, s13
	ds_read2_b32 v[66:67], v34 offset0:231 offset1:239
	v_and_or_b32 v47, v48, s14, v47
	s_waitcnt lgkmcnt(3)
	v_bfe_u32 v48, v60, 16, 1
	v_add3_u32 v48, v60, v48, s13
	s_waitcnt lgkmcnt(2)
	v_bfe_u32 v49, v62, 16, 1
	v_lshrrev_b32_e32 v48, 16, v48
	v_add3_u32 v49, v62, v49, s13
	v_and_or_b32 v48, v49, s14, v48
	s_waitcnt lgkmcnt(1)
	v_bfe_u32 v49, v64, 16, 1
	v_add_u32_e32 v68, s4, v33
	v_add3_u32 v49, v64, v49, s13
	s_waitcnt lgkmcnt(0)
	v_bfe_u32 v50, v66, 16, 1
	v_ashrrev_i32_e32 v69, 31, v68
	v_lshl_add_u64 v[52:53], v[20:21], 0, s[0:1]
	v_lshrrev_b32_e32 v49, 16, v49
	v_add3_u32 v50, v66, v50, s13
	v_lshlrev_b64 v[68:69], 11, v[68:69]
	v_and_or_b32 v49, v50, s14, v49
	v_lshl_add_u64 v[68:69], v[52:53], 0, v[68:69]
	global_store_dwordx4 v[68:69], v[46:49], off nt
	v_bfe_u32 v50, v67, 16, 1
	v_add3_u32 v50, v67, v50, s13
	v_bfe_u32 v46, v51, 16, 1
	v_add3_u32 v46, v51, v46, s13
	v_bfe_u32 v47, v55, 16, 1
	v_lshrrev_b32_e32 v46, 16, v46
	v_add3_u32 v47, v55, v47, s13
	v_and_or_b32 v46, v47, s14, v46
	v_bfe_u32 v47, v57, 16, 1
	v_add3_u32 v47, v57, v47, s13
	v_bfe_u32 v48, v59, 16, 1
	v_lshrrev_b32_e32 v47, 16, v47
	v_add3_u32 v48, v59, v48, s13
	v_and_or_b32 v47, v48, s14, v47
	v_bfe_u32 v48, v61, 16, 1
	v_add3_u32 v48, v61, v48, s13
	v_bfe_u32 v49, v63, 16, 1
	v_lshrrev_b32_e32 v48, 16, v48
	v_add3_u32 v49, v63, v49, s13
	v_and_or_b32 v48, v49, s14, v48
	v_bfe_u32 v49, v65, 16, 1
	v_add3_u32 v49, v65, v49, s13
	v_lshrrev_b32_e32 v49, 16, v49
	v_and_or_b32 v49, v50, s14, v49
	v_add_u32_e32 v50, s4, v35
	v_ashrrev_i32_e32 v51, 31, v50
	v_lshlrev_b64 v[50:51], 11, v[50:51]
	ds_read2_b32 v[54:55], v34 offset0:16 offset1:24
	v_lshl_add_u64 v[50:51], v[52:53], 0, v[50:51]
	global_store_dwordx4 v[50:51], v[46:49], off nt
	ds_read2_b32 v[50:51], v34 offset0:49 offset1:57
	ds_read2_b32 v[56:57], v34 offset0:82 offset1:90
	ds_read2_b32 v[58:59], v34 offset0:115 offset1:123
	s_waitcnt lgkmcnt(3)
	v_bfe_u32 v46, v54, 16, 1
	v_add3_u32 v46, v54, v46, s13
	s_waitcnt lgkmcnt(2)
	v_bfe_u32 v47, v50, 16, 1
	ds_read2_b32 v[60:61], v34 offset0:148 offset1:156
	v_lshrrev_b32_e32 v46, 16, v46
	v_add3_u32 v47, v50, v47, s13
	ds_read2_b32 v[62:63], v34 offset0:181 offset1:189
	v_and_or_b32 v46, v47, s14, v46
	s_waitcnt lgkmcnt(3)
	v_bfe_u32 v47, v56, 16, 1
	v_add3_u32 v47, v56, v47, s13
	s_waitcnt lgkmcnt(2)
	v_bfe_u32 v48, v58, 16, 1
	ds_read2_b32 v[64:65], v34 offset0:214 offset1:222
	v_lshrrev_b32_e32 v47, 16, v47
	v_add3_u32 v48, v58, v48, s13
	ds_read2_b32 v[66:67], v34 offset0:247 offset1:255
	v_and_or_b32 v47, v48, s14, v47
	s_waitcnt lgkmcnt(3)
	v_bfe_u32 v48, v60, 16, 1
	v_add3_u32 v48, v60, v48, s13
	s_waitcnt lgkmcnt(2)
	v_bfe_u32 v49, v62, 16, 1
	v_lshrrev_b32_e32 v48, 16, v48
	v_add3_u32 v49, v62, v49, s13
	v_and_or_b32 v48, v49, s14, v48
	s_waitcnt lgkmcnt(1)
	v_bfe_u32 v49, v64, 16, 1
	v_add_u32_e32 v68, s4, v36
	v_add3_u32 v49, v64, v49, s13
	s_waitcnt lgkmcnt(0)
	v_bfe_u32 v50, v66, 16, 1
	v_ashrrev_i32_e32 v69, 31, v68
	v_lshrrev_b32_e32 v49, 16, v49
	v_add3_u32 v50, v66, v50, s13
	v_lshlrev_b64 v[68:69], 11, v[68:69]
	v_and_or_b32 v49, v50, s14, v49
	v_lshl_add_u64 v[68:69], v[52:53], 0, v[68:69]
	global_store_dwordx4 v[68:69], v[46:49], off nt
	v_bfe_u32 v50, v67, 16, 1
	v_add3_u32 v50, v67, v50, s13
	v_bfe_u32 v46, v55, 16, 1
	v_add3_u32 v46, v55, v46, s13
	v_bfe_u32 v47, v51, 16, 1
	v_lshrrev_b32_e32 v46, 16, v46
	v_add3_u32 v47, v51, v47, s13
	v_and_or_b32 v46, v47, s14, v46
	v_bfe_u32 v47, v57, 16, 1
	v_add3_u32 v47, v57, v47, s13
	v_bfe_u32 v48, v59, 16, 1
	v_lshrrev_b32_e32 v47, 16, v47
	v_add3_u32 v48, v59, v48, s13
	v_and_or_b32 v47, v48, s14, v47
	v_bfe_u32 v48, v61, 16, 1
	v_add3_u32 v48, v61, v48, s13
	v_bfe_u32 v49, v63, 16, 1
	v_lshrrev_b32_e32 v48, 16, v48
	v_add3_u32 v49, v63, v49, s13
	v_and_or_b32 v48, v49, s14, v48
	v_bfe_u32 v49, v65, 16, 1
	v_add3_u32 v49, v65, v49, s13
	v_lshrrev_b32_e32 v49, 16, v49
	v_and_or_b32 v49, v50, s14, v49
	v_add_u32_e32 v50, s4, v37
	v_ashrrev_i32_e32 v51, 31, v50
	v_lshlrev_b64 v[50:51], 11, v[50:51]
	v_lshl_add_u64 v[50:51], v[52:53], 0, v[50:51]
	global_store_dwordx4 v[50:51], v[46:49], off nt
	s_waitcnt lgkmcnt(0)

; #define LAS __attribute__((address_space(3)))
; __device__ __forceinline__ void tr_item(const float* W, int ld, int K, int nblk, int item, bf16* WT, bool gu, LAS float* scr, int lane) {
;     const int kb = item / nblk, nb = item % nblk, k0 = 64 * kb, n0 = 32 * nb;
;     int drow0 = n0;
;     if (gu) { const int bj = n0 / FF, j = n0 - bj * FF; drow0 = 256 * (j / 128) + 128 * bj + (j % 128); }
;     { float t_[32];
; #pragma unroll
;       for (int i = 0; i < 32; ++i) t_[i] = W[(size_t)(k0 + 2 * i + (lane >> 5)) * ld + n0 + (lane & 31)];
; #pragma unroll
;       for (int i = 0; i < 32; ++i) scr[(2 * i + (lane >> 5)) * 33 + (lane & 31)] = t_[i]; }
; __device__ __forceinline__ void convert_items(Frame& F, const Args& a, int lo, int hi, int w, int nw) {
;     ...
;         if (r < I_FI) { tr_item(a.in[7], 3 * D + 16, D, 96, r, (bf16*)(F.ws + WS_WFOXIN), false, scr, lane); continue; } r -= I_FI;
.LBB0_581:
	s_andn2_b64 vcc, exec, s[4:5]
	s_cbranch_vccnz .LBB0_558
	s_mul_hi_i32 s0, s3, 0x2aaaaaab
	s_lshr_b32 s4, s0, 31
	s_ashr_i32 s0, s0, 4
	s_add_i32 s0, s0, s4
	s_lshl_b32 s6, s0, 6
	s_mulk_i32 s0, 0xf400
	s_add_i32 s4, s9, s0
	v_add_u32_e32 v64, s6, v28
	s_ashr_i32 s5, s4, 31
	v_lshl_add_u64 v[46:47], s[4:5], 2, v[10:11]
	v_add_u32_e32 v50, 2, v64
	v_add_u32_e32 v52, 4, v64
	v_add_u32_e32 v54, 6, v64
	v_add_u32_e32 v56, 8, v64
	v_add_u32_e32 v58, 10, v64
	v_add_u32_e32 v60, 12, v64
	v_add_u32_e32 v62, 14, v64
	v_mad_i64_i32 v[48:49], s[18:19], v64, s16, v[46:47]
	v_mad_i64_i32 v[50:51], s[18:19], v50, s16, v[46:47]
	v_mad_i64_i32 v[52:53], s[18:19], v52, s16, v[46:47]
	v_mad_i64_i32 v[54:55], s[18:19], v54, s16, v[46:47]
	v_mad_i64_i32 v[56:57], s[18:19], v56, s16, v[46:47]
	v_mad_i64_i32 v[58:59], s[18:19], v58, s16, v[46:47]
	v_mad_i64_i32 v[60:61], s[18:19], v60, s16, v[46:47]
	v_mad_i64_i32 v[62:63], s[18:19], v62, s16, v[46:47]
	global_load_dword v65, v[48:49], off nt
	global_load_dword v66, v[50:51], off nt
	global_load_dword v67, v[52:53], off nt
	global_load_dword v68, v[54:55], off nt
	global_load_dword v69, v[56:57], off nt
	global_load_dword v70, v[58:59], off nt
	global_load_dword v71, v[60:61], off nt
	global_load_dword v72, v[62:63], off nt
	v_add_u32_e32 v48, 16, v64
	v_add_u32_e32 v50, 18, v64
	v_add_u32_e32 v52, 20, v64
	v_add_u32_e32 v54, 22, v64
	v_add_u32_e32 v56, 24, v64
	v_add_u32_e32 v58, 26, v64
	v_add_u32_e32 v60, 28, v64
	v_add_u32_e32 v62, 30, v64
	v_mad_i64_i32 v[48:49], s[18:19], v48, s16, v[46:47]
	v_mad_i64_i32 v[50:51], s[18:19], v50, s16, v[46:47]
	v_mad_i64_i32 v[52:53], s[18:19], v52, s16, v[46:47]
	v_mad_i64_i32 v[54:55], s[18:19], v54, s16, v[46:47]
	v_mad_i64_i32 v[56:57], s[18:19], v56, s16, v[46:47]
	v_mad_i64_i32 v[58:59], s[18:19], v58, s16, v[46:47]
	v_mad_i64_i32 v[60:61], s[18:19], v60, s16, v[46:47]
	v_mad_i64_i32 v[62:63], s[18:19], v62, s16, v[46:47]
	global_load_dword v73, v[48:49], off nt
	global_load_dword v74, v[50:51], off nt
	global_load_dword v75, v[52:53], off nt
	global_load_dword v76, v[54:55], off nt
	global_load_dword v77, v[56:57], off nt
	global_load_dword v78, v[58:59], off nt
	global_load_dword v79, v[60:61], off nt
	global_load_dword v80, v[62:63], off nt
	v_add_u32_e32 v48, 32, v64
	v_add_u32_e32 v50, 34, v64
	v_add_u32_e32 v52, 36, v64
	v_add_u32_e32 v54, 38, v64
	v_add_u32_e32 v56, 40, v64
	v_add_u32_e32 v58, 42, v64
	v_add_u32_e32 v60, 44, v64
	v_add_u32_e32 v62, 46, v64
	v_mad_i64_i32 v[48:49], s[18:19], v48, s16, v[46:47]
	v_mad_i64_i32 v[50:51], s[18:19], v50, s16, v[46:47]
	v_mad_i64_i32 v[52:53], s[18:19], v52, s16, v[46:47]
	v_mad_i64_i32 v[54:55], s[18:19], v54, s16, v[46:47]
	v_mad_i64_i32 v[56:57], s[18:19], v56, s16, v[46:47]
	v_mad_i64_i32 v[58:59], s[18:19], v58, s16, v[46:47]
	v_mad_i64_i32 v[60:61], s[18:19], v60, s16, v[46:47]
	v_mad_i64_i32 v[62:63], s[18:19], v62, s16, v[46:47]
	global_load_dword v81, v[48:49], off nt
	global_load_dword v82, v[50:51], off nt
	global_load_dword v83, v[52:53], off nt
	global_load_dword v84, v[54:55], off nt
	global_load_dword v85, v[56:57], off nt
	global_load_dword v86, v[58:59], off nt
	global_load_dword v87, v[60:61], off nt
	s_nop 0
	global_load_dword v62, v[62:63], off nt
	v_add_u32_e32 v48, 48, v64
	v_add_u32_e32 v50, 50, v64
	v_add_u32_e32 v52, 52, v64
	v_add_u32_e32 v54, 54, v64
	v_add_u32_e32 v56, 56, v64
	v_add_u32_e32 v58, 58, v64
	v_add_u32_e32 v60, 60, v64
	v_add_u32_e32 v63, 62, v64
	v_mad_i64_i32 v[48:49], s[18:19], v48, s16, v[46:47]
	v_mad_i64_i32 v[50:51], s[18:19], v50, s16, v[46:47]
	v_mad_i64_i32 v[52:53], s[18:19], v52, s16, v[46:47]
	v_mad_i64_i32 v[54:55], s[18:19], v54, s16, v[46:47]
	v_mad_i64_i32 v[56:57], s[18:19], v56, s16, v[46:47]
	v_mad_i64_i32 v[58:59], s[18:19], v58, s16, v[46:47]
	v_mad_i64_i32 v[60:61], s[18:19], v60, s16, v[46:47]
	v_mad_i64_i32 v[46:47], s[18:19], v63, s16, v[46:47]
	global_load_dword v48, v[48:49], off nt
	s_nop 0
	global_load_dword v49, v[50:51], off nt
	s_nop 0
	global_load_dword v50, v[52:53], off nt
	global_load_dword v51, v[54:55], off nt
	s_nop 0
	global_load_dword v52, v[56:57], off nt
	global_load_dword v53, v[58:59], off nt
	global_load_dword v54, v[60:61], off nt
	s_nop 0
	global_load_dword v46, v[46:47], off nt
	s_waitcnt vmcnt(0)
	ds_write2_b32 v29, v65, v66 offset1:66
	ds_write2_b32 v29, v67, v68 offset0:132 offset1:198
	ds_write2_b32 v38, v69, v70 offset0:8 offset1:74
	ds_write2_b32 v38, v71, v72 offset0:140 offset1:206
	ds_write2_b32 v39, v73, v74 offset0:16 offset1:82
	ds_write2_b32 v39, v75, v76 offset0:148 offset1:214
	ds_write2_b32 v40, v77, v78 offset0:24 offset1:90
	ds_write2_b32 v40, v79, v80 offset0:156 offset1:222
	ds_write2_b32 v41, v81, v82 offset0:32 offset1:98
	ds_write2_b32 v41, v83, v84 offset0:164 offset1:230
	ds_write2_b32 v42, v85, v86 offset0:40 offset1:106
	ds_write2_b32 v42, v87, v62 offset0:172 offset1:238
	ds_write2_b32 v43, v48, v49 offset0:48 offset1:114
	ds_write2_b32 v43, v50, v51 offset0:180 offset1:246
	ds_write2_b32 v44, v52, v53 offset0:56 offset1:122
	ds_write2_b32 v44, v54, v46 offset0:188 offset1:254
	s_waitcnt lgkmcnt(0)
; #define GAS __attribute__((address_space(1)))
; #define LAS __attribute__((address_space(3)))
; #define LDS_WAIT() asm volatile("s_waitcnt lgkmcnt(0)" ::: "memory")
; __device__ __forceinline__ unsigned pk2(float lo, float hi) { return f2bf(lo) | (f2bf(hi) << 16); }
; __device__ __forceinline__ void tr_item(const float* W, int ld, int K, int nblk, int item, bf16* WT, bool gu, LAS float* scr, int lane) {
;     ...
;       for (int i = 0; i < 32; ++i) scr[(2 * i + (lane >> 5)) * 33 + (lane & 31)] = t_[i]; }
;     LDS_WAIT(); asm volatile("" ::: "memory");
;     const int c = lane & 7;
; #pragma unroll
;     for (int j = 0; j < 4; ++j) { const int n = (lane >> 3) + 8 * j; const LAS float* s = scr + (8 * c) * 33 + n;
;         v4u o; o.x = pk2(s[0 * 33], s[1 * 33]); o.y = pk2(s[2 * 33], s[3 * 33]); o.z = pk2(s[4 * 33], s[5 * 33]); o.w = pk2(s[6 * 33], s[7 * 33]);
;         *(GAS v4u*)(WT + (size_t)(drow0 + n) * K + k0 + 8 * c) = o; }
;     LDS_WAIT(); asm volatile("" ::: "memory");
; __device__ __forceinline__ void convert_items(Frame& F, const Args& a, int lo, int hi, int w, int nw) {
;     ...
;     for (int it = lo + w; it < hi; it += nw) {
	ds_read2_b32 v[50:51], v34 offset1:8
	ds_read2_b32 v[54:55], v34 offset0:33 offset1:41
	ds_read2_b32 v[56:57], v34 offset0:66 offset1:74
	ds_read2_b32 v[58:59], v34 offset0:99 offset1:107
	ds_read2_b32 v[60:61], v34 offset0:132 offset1:140
	s_waitcnt lgkmcnt(4)
	v_bfe_u32 v46, v50, 16, 1
	v_add3_u32 v46, v50, v46, s13
	s_waitcnt lgkmcnt(3)
	v_bfe_u32 v47, v54, 16, 1
	v_lshrrev_b32_e32 v46, 16, v46
	v_add3_u32 v47, v54, v47, s13
	ds_read2_b32 v[62:63], v34 offset0:165 offset1:173
	v_and_or_b32 v46, v47, s14, v46
	s_waitcnt lgkmcnt(3)
	v_bfe_u32 v47, v56, 16, 1
	v_add3_u32 v47, v56, v47, s13
	s_waitcnt lgkmcnt(2)
	v_bfe_u32 v48, v58, 16, 1
	ds_read2_b32 v[64:65], v34 offset0:198 offset1:206
	v_lshrrev_b32_e32 v47, 16, v47
	v_add3_u32 v48, v58, v48, s13
	ds_read2_b32 v[66:67], v34 offset0:231 offset1:239
	v_and_or_b32 v47, v48, s14, v47
	s_waitcnt lgkmcnt(3)
	v_bfe_u32 v48, v60, 16, 1
	v_add3_u32 v48, v60, v48, s13
	s_waitcnt lgkmcnt(2)
	v_bfe_u32 v49, v62, 16, 1
	v_lshrrev_b32_e32 v48, 16, v48
	v_add3_u32 v49, v62, v49, s13
	v_and_or_b32 v48, v49, s14, v48
	s_waitcnt lgkmcnt(1)
	v_bfe_u32 v49, v64, 16, 1
	v_add_u32_e32 v68, s4, v33
	s_ashr_i32 s7, s6, 31
	v_add3_u32 v49, v64, v49, s13
	s_waitcnt lgkmcnt(0)
	v_bfe_u32 v50, v66, 16, 1
	v_ashrrev_i32_e32 v69, 31, v68
	v_lshl_add_u64 v[52:53], s[6:7], 1, v[22:23]
	v_lshrrev_b32_e32 v49, 16, v49
	v_add3_u32 v50, v66, v50, s13
	v_lshlrev_b64 v[70:71], 11, v[68:69]
	v_and_or_b32 v49, v50, s14, v49
	v_lshl_add_u64 v[70:71], v[52:53], 0, v[70:71]
	global_store_dwordx4 v[70:71], v[46:49], off nt
	v_bfe_u32 v50, v67, 16, 1
	v_add3_u32 v50, v67, v50, s13
	v_bfe_u32 v46, v51, 16, 1
	v_add3_u32 v46, v51, v46, s13
	v_bfe_u32 v47, v55, 16, 1
	v_lshrrev_b32_e32 v46, 16, v46
	v_add3_u32 v47, v55, v47, s13
	v_and_or_b32 v46, v47, s14, v46
	v_bfe_u32 v47, v57, 16, 1
	v_add3_u32 v47, v57, v47, s13
	v_bfe_u32 v48, v59, 16, 1
	v_lshrrev_b32_e32 v47, 16, v47
	v_add3_u32 v48, v59, v48, s13
	v_and_or_b32 v47, v48, s14, v47
	v_bfe_u32 v48, v61, 16, 1
	v_add3_u32 v48, v61, v48, s13
	v_bfe_u32 v49, v63, 16, 1
	v_lshrrev_b32_e32 v48, 16, v48
	v_add3_u32 v49, v63, v49, s13
	v_and_or_b32 v48, v49, s14, v48
	v_bfe_u32 v49, v65, 16, 1
	v_add3_u32 v49, v65, v49, s13
	v_lshrrev_b32_e32 v49, 16, v49
	v_and_or_b32 v49, v50, s14, v49
	v_add_u32_e32 v50, 8, v68
	v_ashrrev_i32_e32 v51, 31, v50
	v_lshlrev_b64 v[50:51], 11, v[50:51]
	ds_read2_b32 v[54:55], v34 offset0:16 offset1:24
	v_lshl_add_u64 v[50:51], v[52:53], 0, v[50:51]
	global_store_dwordx4 v[50:51], v[46:49], off nt
	ds_read2_b32 v[50:51], v34 offset0:49 offset1:57
	ds_read2_b32 v[56:57], v34 offset0:82 offset1:90
	ds_read2_b32 v[58:59], v34 offset0:115 offset1:123
	s_waitcnt lgkmcnt(3)
	v_bfe_u32 v46, v54, 16, 1
	v_add3_u32 v46, v54, v46, s13
	s_waitcnt lgkmcnt(2)
	v_bfe_u32 v47, v50, 16, 1
	ds_read2_b32 v[60:61], v34 offset0:148 offset1:156
	v_lshrrev_b32_e32 v46, 16, v46
	v_add3_u32 v47, v50, v47, s13
	ds_read2_b32 v[62:63], v34 offset0:181 offset1:189
	v_and_or_b32 v46, v47, s14, v46
	s_waitcnt lgkmcnt(3)
	v_bfe_u32 v47, v56, 16, 1
	v_add3_u32 v47, v56, v47, s13
	s_waitcnt lgkmcnt(2)
	v_bfe_u32 v48, v58, 16, 1
	ds_read2_b32 v[64:65], v34 offset0:214 offset1:222
	v_lshrrev_b32_e32 v47, 16, v47
	v_add3_u32 v48, v58, v48, s13
	ds_read2_b32 v[66:67], v34 offset0:247 offset1:255
	v_and_or_b32 v47, v48, s14, v47
	s_waitcnt lgkmcnt(3)
	v_bfe_u32 v48, v60, 16, 1
	v_add3_u32 v48, v60, v48, s13
	s_waitcnt lgkmcnt(2)
	v_bfe_u32 v49, v62, 16, 1
	v_lshrrev_b32_e32 v48, 16, v48
	v_add3_u32 v49, v62, v49, s13
	v_and_or_b32 v48, v49, s14, v48
	s_waitcnt lgkmcnt(1)
	v_bfe_u32 v49, v64, 16, 1
	v_add_u32_e32 v70, 16, v68
	v_add3_u32 v49, v64, v49, s13
	s_waitcnt lgkmcnt(0)
	v_bfe_u32 v50, v66, 16, 1
	v_ashrrev_i32_e32 v71, 31, v70
	v_lshrrev_b32_e32 v49, 16, v49
	v_add3_u32 v50, v66, v50, s13
	v_lshlrev_b64 v[70:71], 11, v[70:71]
	v_and_or_b32 v49, v50, s14, v49
	v_lshl_add_u64 v[70:71], v[52:53], 0, v[70:71]
	global_store_dwordx4 v[70:71], v[46:49], off nt
	v_bfe_u32 v50, v67, 16, 1
	v_add3_u32 v50, v67, v50, s13
	v_bfe_u32 v46, v55, 16, 1
	v_add3_u32 v46, v55, v46, s13
	v_bfe_u32 v47, v51, 16, 1
	v_lshrrev_b32_e32 v46, 16, v46
	v_add3_u32 v47, v51, v47, s13
	v_and_or_b32 v46, v47, s14, v46
	v_bfe_u32 v47, v57, 16, 1
	v_add3_u32 v47, v57, v47, s13
	v_bfe_u32 v48, v59, 16, 1
	v_lshrrev_b32_e32 v47, 16, v47
	v_add3_u32 v48, v59, v48, s13
	v_and_or_b32 v47, v48, s14, v47
	v_bfe_u32 v48, v61, 16, 1
	v_add3_u32 v48, v61, v48, s13
	v_bfe_u32 v49, v63, 16, 1
	v_lshrrev_b32_e32 v48, 16, v48
	v_add3_u32 v49, v63, v49, s13
	v_and_or_b32 v48, v49, s14, v48
	v_bfe_u32 v49, v65, 16, 1
	v_add3_u32 v49, v65, v49, s13
	v_lshrrev_b32_e32 v49, 16, v49
	v_and_or_b32 v49, v50, s14, v49
	v_add_u32_e32 v50, 24, v68
	v_ashrrev_i32_e32 v51, 31, v50
	v_lshlrev_b64 v[50:51], 11, v[50:51]
	v_lshl_add_u64 v[50:51], v[52:53], 0, v[50:51]
	global_store_dwordx4 v[50:51], v[46:49], off nt
	s_waitcnt lgkmcnt(0)
	s_branch .LBB0_558
